# v63 + GEMM K-loops: LDS-DMA loads (with m0/address setup) issued before the fragment ds_reads in each load segment (41 segments, pure reorder)
# speedup vs baseline: 1.0044x; 1.0044x over previous
; #define PG8_STAGE(bufoff, gbase, voff) do { _Pragma("unroll") for (int _i = 0; _i < 2; ++_i) \
;         __builtin_amdgcn_global_load_lds((const unsigned*)(wsb + (size_t)(gbase) + (voff)[_i]), (LAS unsigned*)(lds + (bufoff) + ldsw + _i * 8192), 16, 0, 0); } while (0)
; #define PG8_LDA(dst, b, h) do { _Pragma("unroll") for (int m = 0; m < 4; ++m) { if constexpr (FP8) dst##8[m] = PG8_LD8(pa, PG8_SA(b, h) + m * 2048); \
;         else { _Pragma("unroll") for (int k = 0; k < 2; ++k) dst[m][k] = *(const LAS bf16x8*)(pa + PG8_SA(b, h) + m * 2048 + k * 1024); } } } while (0)
; #define PG8_LDB(dst, b, h) do { _Pragma("unroll") for (int n = 0; n < 2; ++n) { if constexpr (FP8) dst##8[n] = PG8_LD8(pb, PG8_SA(b, h) + n * 2048); \
;         else { _Pragma("unroll") for (int k = 0; k < 2; ++k) dst[n][k] = *(const LAS bf16x8*)(pb + PG8_SA(b, h) + n * 2048 + k * 1024); } } } while (0)
; #define PG8_WAIT_V(n) asm volatile("s_waitcnt vmcnt(" #n ")" ::: "memory")
; #define PG8_WAIT_L(n) asm volatile("s_waitcnt lgkmcnt(" #n ")" ::: "memory")
; #define PG8_BAR __builtin_amdgcn_s_barrier()
; #define PG8_SCHED __builtin_amdgcn_sched_barrier(0)
; template <class Epi, class Sched, bool PERM, bool FP8 = false, bool GATHER = false>
; DI void gemm_phase(LAS unsigned char* lds, const unsigned char* wsb, const unsigned lda, const unsigned ldb, const int nt, const Sched& S, const Epi& E) {
;     ...
;             PG8_LDB(B0, 0, 0); PG8_LDB(B1, 0, 1); PG8_SCHED; PG8_LDA(At, 0, 0); PG8_STAGEA(PG8_SA(1, 1), t + 1, 1, false);
;             if constexpr (GATHER) { if (last) {
;                 int tz = tid; asm volatile("" : "+v"(tz));
; #pragma unroll
;                 for (int i = 0; i < 2; ++i) { int R, C; stage_rc(tz * 16 + i * 8192, R, C);
; #pragma unroll
;                     for (int h = 0; h < 2; ++h) { const unsigned tk = (unsigned)tokt[h * HALF + R]; offC[h][i] = (tk < (unsigned)NTOK ? tk : (unsigned)(NTOK - 1)) * lda + (unsigned)C * 2u; } } } }
;             PG8_WAIT_V(8); PG8_WAIT_L(0); PG8_BAR; PG8_MMA(0, 0, At, B0); PG8_MMA(0, 1, At, B1); PG8_BAR; PG8_SCHED;
;             PG8_LDA(At, 0, 1); PG8_STAGE(PG8_SB(0, 0), b2, voffB); PG8_STAGE(PG8_SB(0, 1), b2 + hstepB, voffB); PG8_STAGEA(PG8_SA(0, 0), k2, 0, last);
;             PG8_WAIT_V(8); PG8_WAIT_L(0); PG8_BAR; PG8_MMA(1, 0, At, B0); PG8_MMA(1, 1, At, B1); PG8_BAR; PG8_SCHED;
.LBB0_405:
	s_add_i32 s41, s5, 0xfffe0080
	s_cmp_eq_u32 s7, 4
	s_cselect_b32 s40, s38, s4
	s_cselect_b32 s41, s37, s41
	s_add_i32 s52, s40, 0x80
	s_add_u32 s54, s10, s5
	s_addc_u32 s55, s11, 0
	s_mov_b32 m0, s29
	v_lshl_add_u64 v[206:207], s[54:55], 0, v[154:155]
	global_load_lds_dwordx4 v[206:207], off
	v_lshl_add_u64 v[206:207], s[54:55], 0, v[156:157]
	s_mov_b32 m0, s82
	s_nop 0
	global_load_lds_dwordx4 v[206:207], off
	ds_read_b128 v[130:133], v186
	ds_read_b128 v[134:137], v186 offset:1024
	ds_read_b128 v[138:141], v186 offset:2048
	ds_read_b128 v[142:145], v186 offset:3072
	ds_read_b128 v[146:149], v186 offset:16384
	ds_read_b128 v[150:153], v186 offset:17408
	ds_read_b128 v[160:163], v186 offset:18432
	ds_read_b128 v[164:167], v186 offset:19456
	ds_read_b128 v[168:171], v185
	ds_read_b128 v[172:175], v185 offset:1024
	ds_read_b128 v[176:179], v185 offset:2048
	ds_read_b128 v[180:183], v185 offset:3072
	ds_read_b128 v[190:193], v185 offset:4096
	ds_read_b128 v[194:197], v185 offset:5120
	ds_read_b128 v[198:201], v185 offset:6144
	ds_read_b128 v[202:205], v185 offset:7168
	s_waitcnt vmcnt(8)
	s_waitcnt lgkmcnt(0)
	s_barrier
	s_setprio 1
	s_waitcnt lgkmcnt(0)
	v_mfma_f32_16x16x128_f8f6f4 v[126:129], v[130:137], v[168:175], v[126:129]
	v_mfma_f32_16x16x128_f8f6f4 v[122:125], v[138:145], v[168:175], v[122:125]
	v_mfma_f32_16x16x128_f8f6f4 v[110:113], v[130:137], v[176:183], v[110:113]
	v_mfma_f32_16x16x128_f8f6f4 v[106:109], v[138:145], v[176:183], v[106:109]
	v_mfma_f32_16x16x128_f8f6f4 v[206:209], v[130:137], v[190:197], v[94:97]
	v_mfma_f32_16x16x128_f8f6f4 v[210:213], v[138:145], v[190:197], v[90:93]
	v_mfma_f32_16x16x128_f8f6f4 v[214:217], v[130:137], v[198:205], v[78:81]
	v_mfma_f32_16x16x128_f8f6f4 v[218:221], v[138:145], v[198:205], v[74:77]
	s_setprio 0
	s_setprio 1
	v_mfma_f32_16x16x128_f8f6f4 v[118:121], v[146:153], v[168:175], v[118:121]
	v_mfma_f32_16x16x128_f8f6f4 v[114:117], v[160:167], v[168:175], v[114:117]
	v_mfma_f32_16x16x128_f8f6f4 v[102:105], v[146:153], v[176:183], v[102:105]
	v_mfma_f32_16x16x128_f8f6f4 v[98:101], v[160:167], v[176:183], v[98:101]
	v_mfma_f32_16x16x128_f8f6f4 v[168:171], v[146:153], v[190:197], v[86:89]
	v_mfma_f32_16x16x128_f8f6f4 v[172:175], v[160:167], v[190:197], v[82:85]
	v_mfma_f32_16x16x128_f8f6f4 v[176:179], v[146:153], v[198:205], v[70:73]
	v_mfma_f32_16x16x128_f8f6f4 v[180:183], v[160:167], v[198:205], v[66:69]
	s_setprio 0
	s_barrier
	s_add_u32 s54, s10, s40
	s_addc_u32 s55, s11, 0
	s_mov_b32 m0, s58
	v_lshl_add_u64 v[190:191], s[54:55], 0, v[154:155]
	s_add_i32 s53, s40, 0x20000
	global_load_lds_dwordx4 v[190:191], off
	v_lshl_add_u64 v[190:191], s[54:55], 0, v[156:157]
	s_add_u32 s54, s10, s53
	s_mov_b32 m0, s59
	s_addc_u32 s55, s11, 0
	global_load_lds_dwordx4 v[190:191], off
	v_lshl_add_u64 v[190:191], s[54:55], 0, v[154:155]
	s_mov_b32 m0, s60
	s_nop 0
	global_load_lds_dwordx4 v[190:191], off
	v_lshl_add_u64 v[190:191], s[54:55], 0, v[156:157]
	s_add_u32 s54, s10, s41
	s_mov_b32 m0, s61
	s_addc_u32 s55, s11, 0
	global_load_lds_dwordx4 v[190:191], off
	v_lshl_add_u64 v[190:191], s[54:55], 0, v[154:155]
	s_mov_b32 m0, s57
	s_nop 0
	global_load_lds_dwordx4 v[190:191], off
	v_lshl_add_u64 v[190:191], s[54:55], 0, v[156:157]
	s_mov_b32 m0, s62
	s_nop 0
	global_load_lds_dwordx4 v[190:191], off
	ds_read_b128 v[66:69], v185 offset:16384
	ds_read_b128 v[70:73], v185 offset:17408
	ds_read_b128 v[74:77], v185 offset:18432
	ds_read_b128 v[78:81], v185 offset:19456
	ds_read_b128 v[82:85], v185 offset:20480
	ds_read_b128 v[86:89], v185 offset:21504
	ds_read_b128 v[90:93], v185 offset:22528
	ds_read_b128 v[94:97], v185 offset:23552
	s_waitcnt vmcnt(8)
	s_waitcnt lgkmcnt(0)
	s_barrier
	s_setprio 1
	s_waitcnt lgkmcnt(0)
	v_mfma_f32_16x16x128_f8f6f4 v[62:65], v[130:137], v[66:73], v[62:65]
	v_mfma_f32_16x16x128_f8f6f4 v[58:61], v[138:145], v[66:73], v[58:61]
	v_mfma_f32_16x16x128_f8f6f4 v[190:193], v[130:137], v[74:81], v[46:49]
	v_mfma_f32_16x16x128_f8f6f4 v[194:197], v[138:145], v[74:81], v[42:45]
	v_mfma_f32_16x16x128_f8f6f4 v[198:201], v[130:137], v[82:89], v[30:33]
	v_mfma_f32_16x16x128_f8f6f4 v[202:205], v[138:145], v[82:89], v[26:29]
	v_mfma_f32_16x16x128_f8f6f4 v[222:225], v[130:137], v[90:97], v[14:17]
	v_mfma_f32_16x16x128_f8f6f4 v[226:229], v[138:145], v[90:97], v[10:13]
	s_setprio 0
	s_setprio 1
	v_mfma_f32_16x16x128_f8f6f4 v[54:57], v[146:153], v[66:73], v[54:57]
	v_mfma_f32_16x16x128_f8f6f4 v[50:53], v[160:167], v[66:73], v[50:53]
	v_mfma_f32_16x16x128_f8f6f4 v[230:233], v[146:153], v[74:81], v[38:41]
	v_mfma_f32_16x16x128_f8f6f4 v[234:237], v[160:167], v[74:81], v[34:37]
	v_mfma_f32_16x16x128_f8f6f4 v[238:241], v[146:153], v[82:89], v[22:25]
	v_mfma_f32_16x16x128_f8f6f4 v[242:245], v[160:167], v[82:89], v[18:21]
	v_mfma_f32_16x16x128_f8f6f4 v[246:249], v[146:153], v[90:97], v[6:9]
	v_mfma_f32_16x16x128_f8f6f4 v[250:253], v[160:167], v[90:97], v[2:5]
	s_setprio 0
	s_barrier
; #define PG8_STAGE(bufoff, gbase, voff) do { _Pragma("unroll") for (int _i = 0; _i < 2; ++_i) \
;         __builtin_amdgcn_global_load_lds((const unsigned*)(wsb + (size_t)(gbase) + (voff)[_i]), (LAS unsigned*)(lds + (bufoff) + ldsw + _i * 8192), 16, 0, 0); } while (0)
; #define PG8_LDA(dst, b, h) do { _Pragma("unroll") for (int m = 0; m < 4; ++m) { if constexpr (FP8) dst##8[m] = PG8_LD8(pa, PG8_SA(b, h) + m * 2048); \
;         else { _Pragma("unroll") for (int k = 0; k < 2; ++k) dst[m][k] = *(const LAS bf16x8*)(pa + PG8_SA(b, h) + m * 2048 + k * 1024); } } } while (0)
; #define PG8_LDB(dst, b, h) do { _Pragma("unroll") for (int n = 0; n < 2; ++n) { if constexpr (FP8) dst##8[n] = PG8_LD8(pb, PG8_SA(b, h) + n * 2048); \
;         else { _Pragma("unroll") for (int k = 0; k < 2; ++k) dst[n][k] = *(const LAS bf16x8*)(pb + PG8_SA(b, h) + n * 2048 + k * 1024); } } } while (0)
; #define PG8_WAIT_V(n) asm volatile("s_waitcnt vmcnt(" #n ")" ::: "memory")
; #define PG8_WAIT_L(n) asm volatile("s_waitcnt lgkmcnt(" #n ")" ::: "memory")
; #define PG8_BAR __builtin_amdgcn_s_barrier()
; #define PG8_SCHED __builtin_amdgcn_sched_barrier(0)
; template <class Epi, class Sched, bool PERM, bool FP8 = false, bool GATHER = false>
; DI void gemm_phase(LAS unsigned char* lds, const unsigned char* wsb, const unsigned lda, const unsigned ldb, const int nt, const Sched& S, const Epi& E) {
;     ...
;             PG8_LDB(B0, 1, 0); PG8_LDB(B1, 1, 1); PG8_SCHED; PG8_LDA(At, 1, 0); PG8_STAGEA(PG8_SA(0, 1), k2, 1, last);
;             PG8_WAIT_V(8); PG8_WAIT_L(0); PG8_BAR; PG8_MMA(0, 0, At, B0); PG8_MMA(0, 1, At, B1); PG8_BAR; PG8_SCHED;
;             PG8_LDA(At, 1, 1); PG8_STAGE(PG8_SB(1, 0), b3, voffB); PG8_STAGE(PG8_SB(1, 1), b3 + hstepB, voffB); PG8_STAGEA(PG8_SA(1, 0), k3, 0, last);
;             PG8_WAIT_V(8); PG8_WAIT_L(0); PG8_BAR; PG8_MMA(1, 0, At, B0); PG8_MMA(1, 1, At, B1); PG8_BAR; PG8_SCHED;
;         }
;         if (wr == 0) PG8_BAR;
	s_nop 4
	s_add_i32 s53, s41, 0x20000
	s_add_u32 s54, s10, s53
	s_addc_u32 s55, s11, 0
	s_mov_b32 m0, s63
	v_lshl_add_u64 v[66:67], s[54:55], 0, v[154:155]
	global_load_lds_dwordx4 v[66:67], off
	v_lshl_add_u64 v[66:67], s[54:55], 0, v[156:157]
	s_mov_b32 m0, s64
	s_nop 0
	global_load_lds_dwordx4 v[66:67], off
	ds_read_b128 v[2:5], v186 offset:32768
	ds_read_b128 v[6:9], v186 offset:33792
	ds_read_b128 v[18:21], v186 offset:34816
	ds_read_b128 v[22:25], v186 offset:35840
	ds_read_b128 v[130:133], v186 offset:49152
	ds_read_b128 v[134:137], v186 offset:50176
	ds_read_b128 v[138:141], v186 offset:51200
	ds_read_b128 v[142:145], v186 offset:52224
	ds_read_b128 v[10:13], v185 offset:32768
	ds_read_b128 v[14:17], v185 offset:33792
	ds_read_b128 v[26:29], v185 offset:34816
	ds_read_b128 v[30:33], v185 offset:35840
	ds_read_b128 v[34:37], v185 offset:36864
	ds_read_b128 v[38:41], v185 offset:37888
	ds_read_b128 v[42:45], v185 offset:38912
	ds_read_b128 v[46:49], v185 offset:39936
	s_waitcnt vmcnt(8)
	s_waitcnt lgkmcnt(0)
	s_barrier
	s_setprio 1
	s_waitcnt lgkmcnt(0)
	v_mfma_f32_16x16x128_f8f6f4 v[126:129], v[2:9], v[10:17], v[126:129]
	v_mfma_f32_16x16x128_f8f6f4 v[122:125], v[18:25], v[10:17], v[122:125]
	v_mfma_f32_16x16x128_f8f6f4 v[110:113], v[2:9], v[26:33], v[110:113]
	v_mfma_f32_16x16x128_f8f6f4 v[106:109], v[18:25], v[26:33], v[106:109]
	v_mfma_f32_16x16x128_f8f6f4 v[94:97], v[2:9], v[34:41], v[206:209]
	v_mfma_f32_16x16x128_f8f6f4 v[90:93], v[18:25], v[34:41], v[210:213]
	v_mfma_f32_16x16x128_f8f6f4 v[78:81], v[2:9], v[42:49], v[214:217]
	v_mfma_f32_16x16x128_f8f6f4 v[74:77], v[18:25], v[42:49], v[218:221]
	s_setprio 0
	s_setprio 1
	v_mfma_f32_16x16x128_f8f6f4 v[118:121], v[130:137], v[10:17], v[118:121]
	v_mfma_f32_16x16x128_f8f6f4 v[114:117], v[138:145], v[10:17], v[114:117]
	v_mfma_f32_16x16x128_f8f6f4 v[102:105], v[130:137], v[26:33], v[102:105]
	v_mfma_f32_16x16x128_f8f6f4 v[98:101], v[138:145], v[26:33], v[98:101]
	v_mfma_f32_16x16x128_f8f6f4 v[86:89], v[130:137], v[34:41], v[168:171]
	v_mfma_f32_16x16x128_f8f6f4 v[82:85], v[138:145], v[34:41], v[172:175]
	v_mfma_f32_16x16x128_f8f6f4 v[70:73], v[130:137], v[42:49], v[176:179]
	v_mfma_f32_16x16x128_f8f6f4 v[66:69], v[138:145], v[42:49], v[180:183]
	s_setprio 0
	s_barrier
	s_add_u32 s52, s10, s52
	s_addc_u32 s53, s11, 0
	s_mov_b32 m0, s74
	v_lshl_add_u64 v[10:11], s[52:53], 0, v[154:155]
	s_add_i32 s40, s40, 0x20080
	global_load_lds_dwordx4 v[10:11], off
	v_lshl_add_u64 v[10:11], s[52:53], 0, v[156:157]
	s_add_u32 s52, s10, s40
	s_mov_b32 m0, s75
	s_addc_u32 s53, s11, 0
	s_addk_i32 s41, 0x80
	global_load_lds_dwordx4 v[10:11], off
	v_lshl_add_u64 v[10:11], s[52:53], 0, v[154:155]
	s_mov_b32 m0, s78
	s_add_u32 s40, s10, s41
	global_load_lds_dwordx4 v[10:11], off
	v_lshl_add_u64 v[10:11], s[52:53], 0, v[156:157]
	s_mov_b32 m0, s79
	s_addc_u32 s41, s11, 0
	global_load_lds_dwordx4 v[10:11], off
	v_lshl_add_u64 v[10:11], s[40:41], 0, v[154:155]
	s_mov_b32 m0, s76
	s_nop 0
	global_load_lds_dwordx4 v[10:11], off
	v_lshl_add_u64 v[10:11], s[40:41], 0, v[156:157]
	s_mov_b32 m0, s77
	s_nop 0
	global_load_lds_dwordx4 v[10:11], off
	ds_read_b128 v[34:37], v185 offset:49152
	ds_read_b128 v[38:41], v185 offset:50176
	ds_read_b128 v[146:149], v185 offset:51200
	ds_read_b128 v[150:153], v185 offset:52224
	ds_read_b128 v[160:163], v185 offset:53248
	ds_read_b128 v[164:167], v185 offset:54272
	ds_read_b128 v[168:171], v185 offset:55296
	ds_read_b128 v[172:175], v185 offset:56320
	s_waitcnt vmcnt(8)
	s_waitcnt lgkmcnt(0)
	s_barrier
	s_setprio 1
	s_waitcnt lgkmcnt(0)
	v_mfma_f32_16x16x128_f8f6f4 v[62:65], v[2:9], v[34:41], v[62:65]
	v_mfma_f32_16x16x128_f8f6f4 v[58:61], v[18:25], v[34:41], v[58:61]
	v_mfma_f32_16x16x128_f8f6f4 v[46:49], v[2:9], v[146:153], v[190:193]
	v_mfma_f32_16x16x128_f8f6f4 v[42:45], v[18:25], v[146:153], v[194:197]
	v_mfma_f32_16x16x128_f8f6f4 v[30:33], v[2:9], v[160:167], v[198:201]
	v_mfma_f32_16x16x128_f8f6f4 v[26:29], v[18:25], v[160:167], v[202:205]
	v_mfma_f32_16x16x128_f8f6f4 v[14:17], v[2:9], v[168:175], v[222:225]
	v_mfma_f32_16x16x128_f8f6f4 v[10:13], v[18:25], v[168:175], v[226:229]
	s_setprio 0
	s_setprio 1
	v_mfma_f32_16x16x128_f8f6f4 v[54:57], v[130:137], v[34:41], v[54:57]
	v_mfma_f32_16x16x128_f8f6f4 v[50:53], v[138:145], v[34:41], v[50:53]
	v_mfma_f32_16x16x128_f8f6f4 v[38:41], v[130:137], v[146:153], v[230:233]
	v_mfma_f32_16x16x128_f8f6f4 v[34:37], v[138:145], v[146:153], v[234:237]
	v_mfma_f32_16x16x128_f8f6f4 v[22:25], v[130:137], v[160:167], v[238:241]
	v_mfma_f32_16x16x128_f8f6f4 v[18:21], v[138:145], v[160:167], v[242:245]
	v_mfma_f32_16x16x128_f8f6f4 v[6:9], v[130:137], v[168:175], v[246:249]
	v_mfma_f32_16x16x128_f8f6f4 v[2:5], v[138:145], v[168:175], v[250:253]
	s_setprio 0
	s_barrier
	s_add_i32 s7, s7, 2
	s_addk_i32 s5, 0x100
	s_addk_i32 s4, 0x100
	s_cmp_gt_u32 s7, 5
	s_cbranch_scc0 .LBB0_405
	s_and_b64 vcc, exec, s[14:15]
	s_cbranch_vccz .LBB0_408
	s_barrier

; #define PG8_STAGE(bufoff, gbase, voff) do { _Pragma("unroll") for (int _i = 0; _i < 2; ++_i) \
;         __builtin_amdgcn_global_load_lds((const unsigned*)(wsb + (size_t)(gbase) + (voff)[_i]), (LAS unsigned*)(lds + (bufoff) + ldsw + _i * 8192), 16, 0, 0); } while (0)
; #define PG8_LDA(dst, b, h) do { _Pragma("unroll") for (int m = 0; m < 4; ++m) { if constexpr (FP8) dst##8[m] = PG8_LD8(pa, PG8_SA(b, h) + m * 2048); \
;         else { _Pragma("unroll") for (int k = 0; k < 2; ++k) dst[m][k] = *(const LAS bf16x8*)(pa + PG8_SA(b, h) + m * 2048 + k * 1024); } } } while (0)
; #define PG8_LDB(dst, b, h) do { _Pragma("unroll") for (int n = 0; n < 2; ++n) { if constexpr (FP8) dst##8[n] = PG8_LD8(pb, PG8_SA(b, h) + n * 2048); \
;         else { _Pragma("unroll") for (int k = 0; k < 2; ++k) dst[n][k] = *(const LAS bf16x8*)(pb + PG8_SA(b, h) + n * 2048 + k * 1024); } } } while (0)
; #define PG8_WAIT_V(n) asm volatile("s_waitcnt vmcnt(" #n ")" ::: "memory")
; #define PG8_WAIT_L(n) asm volatile("s_waitcnt lgkmcnt(" #n ")" ::: "memory")
; #define PG8_BAR __builtin_amdgcn_s_barrier()
; #define PG8_SCHED __builtin_amdgcn_sched_barrier(0)
; template <class Epi, class Sched, bool PERM, bool FP8 = false, bool GATHER = false>
; DI void gemm_phase(LAS unsigned char* lds, const unsigned char* wsb, const unsigned lda, const unsigned ldb, const int nt, const Sched& S, const Epi& E) {
;     ...
;             PG8_LDB(B0, 0, 0); PG8_LDB(B1, 0, 1); PG8_SCHED; PG8_LDA(At, 0, 0); PG8_STAGEA(PG8_SA(1, 1), t + 1, 1, false);
;             if constexpr (GATHER) { if (last) {
;                 int tz = tid; asm volatile("" : "+v"(tz));
; #pragma unroll
;                 for (int i = 0; i < 2; ++i) { int R, C; stage_rc(tz * 16 + i * 8192, R, C);
; #pragma unroll
;                     for (int h = 0; h < 2; ++h) { const unsigned tk = (unsigned)tokt[h * HALF + R]; offC[h][i] = (tk < (unsigned)NTOK ? tk : (unsigned)(NTOK - 1)) * lda + (unsigned)C * 2u; } } } }
;             PG8_WAIT_V(8); PG8_WAIT_L(0); PG8_BAR; PG8_MMA(0, 0, At, B0); PG8_MMA(0, 1, At, B1); PG8_BAR; PG8_SCHED;
;             PG8_LDA(At, 0, 1); PG8_STAGE(PG8_SB(0, 0), b2, voffB); PG8_STAGE(PG8_SB(0, 1), b2 + hstepB, voffB); PG8_STAGEA(PG8_SA(0, 0), k2, 0, last);
;             PG8_WAIT_V(8); PG8_WAIT_L(0); PG8_BAR; PG8_MMA(1, 0, At, B0); PG8_MMA(1, 1, At, B1); PG8_BAR; PG8_SCHED;
.LBB0_573:
	s_add_i32 s23, s19, 0xfffe0080
	s_cmp_eq_u32 s20, 4
	s_cselect_b32 s22, s66, s18
	s_cselect_b32 s23, s65, s23
	s_add_i32 s24, s22, 0x80
	s_add_u32 s26, s4, s19
	s_addc_u32 s27, s5, 0
	s_mov_b32 m0, s59
	v_lshl_add_u64 v[130:131], s[26:27], 0, v[136:137]
	global_load_lds_dwordx4 v[130:131], off
	v_lshl_add_u64 v[130:131], s[26:27], 0, v[138:139]
	s_mov_b32 m0, s60
	s_nop 0
	global_load_lds_dwordx4 v[130:131], off
	ds_read_b128 v[144:147], v142
	ds_read_b128 v[148:151], v142 offset:1024
	ds_read_b128 v[152:155], v142 offset:2048
	ds_read_b128 v[156:159], v142 offset:3072
	ds_read_b128 v[160:163], v142 offset:16384
	ds_read_b128 v[164:167], v142 offset:17408
	ds_read_b128 v[168:171], v142 offset:18432
	ds_read_b128 v[172:175], v142 offset:19456
	ds_read_b128 v[176:179], v141
	ds_read_b128 v[180:183], v141 offset:1024
	ds_read_b128 v[184:187], v141 offset:2048
	ds_read_b128 v[188:191], v141 offset:3072
	ds_read_b128 v[192:195], v141 offset:4096
	ds_read_b128 v[196:199], v141 offset:5120
	ds_read_b128 v[200:203], v141 offset:6144
	ds_read_b128 v[204:207], v141 offset:7168
	s_waitcnt vmcnt(8)
	s_waitcnt lgkmcnt(0)
	s_barrier
	s_setprio 1
	s_waitcnt lgkmcnt(0)
	v_mfma_f32_16x16x128_f8f6f4 v[126:129], v[144:151], v[176:183], v[126:129]
	v_mfma_f32_16x16x128_f8f6f4 v[122:125], v[152:159], v[176:183], v[122:125]
	v_mfma_f32_16x16x128_f8f6f4 v[114:117], v[144:151], v[184:191], v[114:117]
	v_mfma_f32_16x16x128_f8f6f4 v[106:109], v[152:159], v[184:191], v[106:109]
	v_mfma_f32_16x16x128_f8f6f4 v[98:101], v[144:151], v[192:199], v[98:101]
	v_mfma_f32_16x16x128_f8f6f4 v[208:211], v[152:159], v[192:199], v[90:93]
	v_mfma_f32_16x16x128_f8f6f4 v[212:215], v[144:151], v[200:207], v[82:85]
	v_mfma_f32_16x16x128_f8f6f4 v[216:219], v[152:159], v[200:207], v[74:77]
	s_setprio 0
	s_setprio 1
	v_mfma_f32_16x16x128_f8f6f4 v[118:121], v[160:167], v[176:183], v[118:121]
	v_mfma_f32_16x16x128_f8f6f4 v[110:113], v[168:175], v[176:183], v[110:113]
	v_mfma_f32_16x16x128_f8f6f4 v[102:105], v[160:167], v[184:191], v[102:105]
	v_mfma_f32_16x16x128_f8f6f4 v[176:179], v[168:175], v[184:191], v[94:97]
	v_mfma_f32_16x16x128_f8f6f4 v[180:183], v[160:167], v[192:199], v[86:89]
	v_mfma_f32_16x16x128_f8f6f4 v[184:187], v[168:175], v[192:199], v[78:81]
	v_mfma_f32_16x16x128_f8f6f4 v[188:191], v[160:167], v[200:207], v[70:73]
	v_mfma_f32_16x16x128_f8f6f4 v[192:195], v[168:175], v[200:207], v[66:69]
	s_setprio 0
	s_barrier
	s_add_u32 s26, s4, s22
	s_addc_u32 s27, s5, 0
	s_mov_b32 m0, s38
	v_lshl_add_u64 v[130:131], s[26:27], 0, v[134:135]
	s_add_i32 s25, s22, 0x20000
	global_load_lds_dwordx4 v[130:131], off
	v_lshl_add_u64 v[130:131], s[26:27], 0, v[252:253]
	s_add_u32 s26, s4, s25
	s_mov_b32 m0, s39
	s_addc_u32 s27, s5, 0
	global_load_lds_dwordx4 v[130:131], off
	v_lshl_add_u64 v[130:131], s[26:27], 0, v[134:135]
	s_mov_b32 m0, s40
	s_nop 0
	global_load_lds_dwordx4 v[130:131], off
	v_lshl_add_u64 v[130:131], s[26:27], 0, v[252:253]
	s_add_u32 s26, s4, s23
	s_mov_b32 m0, s41
	s_addc_u32 s27, s5, 0
	global_load_lds_dwordx4 v[130:131], off
	v_lshl_add_u64 v[130:131], s[26:27], 0, v[136:137]
	s_mov_b32 m0, s29
	s_nop 0
	global_load_lds_dwordx4 v[130:131], off
	v_lshl_add_u64 v[130:131], s[26:27], 0, v[138:139]
	s_mov_b32 m0, s42
	s_nop 0
	global_load_lds_dwordx4 v[130:131], off
	ds_read_b128 v[66:69], v141 offset:16384
	ds_read_b128 v[70:73], v141 offset:17408
	ds_read_b128 v[74:77], v141 offset:18432
	ds_read_b128 v[78:81], v141 offset:19456
	ds_read_b128 v[82:85], v141 offset:20480
	ds_read_b128 v[86:89], v141 offset:21504
	ds_read_b128 v[90:93], v141 offset:22528
	ds_read_b128 v[94:97], v141 offset:23552
	s_waitcnt vmcnt(8)
	s_waitcnt lgkmcnt(0)
	s_barrier
	s_setprio 1
	s_waitcnt lgkmcnt(0)
	v_mfma_f32_16x16x128_f8f6f4 v[62:65], v[144:151], v[66:73], v[62:65]
	v_mfma_f32_16x16x128_f8f6f4 v[58:61], v[152:159], v[66:73], v[58:61]
	v_mfma_f32_16x16x128_f8f6f4 v[50:53], v[144:151], v[74:81], v[50:53]
	v_mfma_f32_16x16x128_f8f6f4 v[196:199], v[152:159], v[74:81], v[42:45]
	v_mfma_f32_16x16x128_f8f6f4 v[200:203], v[144:151], v[82:89], v[34:37]
	v_mfma_f32_16x16x128_f8f6f4 v[204:207], v[152:159], v[82:89], v[26:29]
	v_mfma_f32_16x16x128_f8f6f4 v[220:223], v[144:151], v[90:97], v[18:21]
	v_mfma_f32_16x16x128_f8f6f4 v[224:227], v[152:159], v[90:97], v[10:13]
	s_setprio 0
	s_setprio 1
	v_mfma_f32_16x16x128_f8f6f4 v[54:57], v[160:167], v[66:73], v[54:57]
	v_mfma_f32_16x16x128_f8f6f4 v[228:231], v[168:175], v[66:73], v[46:49]
	v_mfma_f32_16x16x128_f8f6f4 v[232:235], v[160:167], v[74:81], v[38:41]
	v_mfma_f32_16x16x128_f8f6f4 v[236:239], v[168:175], v[74:81], v[30:33]
	v_mfma_f32_16x16x128_f8f6f4 v[240:243], v[160:167], v[82:89], v[22:25]
	v_mfma_f32_16x16x128_f8f6f4 v[244:247], v[168:175], v[82:89], v[14:17]
	v_mfma_f32_16x16x128_f8f6f4 v[248:251], v[160:167], v[90:97], v[6:9]
	v_mfma_f32_16x16x128_f8f6f4 v[130:133], v[168:175], v[90:97], v[2:5]
	s_setprio 0
	s_barrier
; #define PG8_STAGE(bufoff, gbase, voff) do { _Pragma("unroll") for (int _i = 0; _i < 2; ++_i) \
;         __builtin_amdgcn_global_load_lds((const unsigned*)(wsb + (size_t)(gbase) + (voff)[_i]), (LAS unsigned*)(lds + (bufoff) + ldsw + _i * 8192), 16, 0, 0); } while (0)
; #define PG8_LDA(dst, b, h) do { _Pragma("unroll") for (int m = 0; m < 4; ++m) { if constexpr (FP8) dst##8[m] = PG8_LD8(pa, PG8_SA(b, h) + m * 2048); \
;         else { _Pragma("unroll") for (int k = 0; k < 2; ++k) dst[m][k] = *(const LAS bf16x8*)(pa + PG8_SA(b, h) + m * 2048 + k * 1024); } } } while (0)
; #define PG8_LDB(dst, b, h) do { _Pragma("unroll") for (int n = 0; n < 2; ++n) { if constexpr (FP8) dst##8[n] = PG8_LD8(pb, PG8_SA(b, h) + n * 2048); \
;         else { _Pragma("unroll") for (int k = 0; k < 2; ++k) dst[n][k] = *(const LAS bf16x8*)(pb + PG8_SA(b, h) + n * 2048 + k * 1024); } } } while (0)
; #define PG8_WAIT_V(n) asm volatile("s_waitcnt vmcnt(" #n ")" ::: "memory")
; #define PG8_WAIT_L(n) asm volatile("s_waitcnt lgkmcnt(" #n ")" ::: "memory")
; #define PG8_BAR __builtin_amdgcn_s_barrier()
; #define PG8_SCHED __builtin_amdgcn_sched_barrier(0)
; template <class Epi, class Sched, bool PERM, bool FP8 = false, bool GATHER = false>
; DI void gemm_phase(LAS unsigned char* lds, const unsigned char* wsb, const unsigned lda, const unsigned ldb, const int nt, const Sched& S, const Epi& E) {
;     ...
;             PG8_LDB(B0, 1, 0); PG8_LDB(B1, 1, 1); PG8_SCHED; PG8_LDA(At, 1, 0); PG8_STAGEA(PG8_SA(0, 1), k2, 1, last);
;             PG8_WAIT_V(8); PG8_WAIT_L(0); PG8_BAR; PG8_MMA(0, 0, At, B0); PG8_MMA(0, 1, At, B1); PG8_BAR; PG8_SCHED;
;             PG8_LDA(At, 1, 1); PG8_STAGE(PG8_SB(1, 0), b3, voffB); PG8_STAGE(PG8_SB(1, 1), b3 + hstepB, voffB); PG8_STAGEA(PG8_SA(1, 0), k3, 0, last);
;             PG8_WAIT_V(8); PG8_WAIT_L(0); PG8_BAR; PG8_MMA(1, 0, At, B0); PG8_MMA(1, 1, At, B1); PG8_BAR; PG8_SCHED;
;         }
;         if (wr == 0) PG8_BAR;
	s_nop 4
	s_add_i32 s25, s23, 0x20000
	s_add_u32 s26, s4, s25
	s_addc_u32 s27, s5, 0
	s_mov_b32 m0, s43
	v_lshl_add_u64 v[66:67], s[26:27], 0, v[136:137]
	global_load_lds_dwordx4 v[66:67], off
	v_lshl_add_u64 v[66:67], s[26:27], 0, v[138:139]
	s_mov_b32 m0, s44
	s_nop 0
	global_load_lds_dwordx4 v[66:67], off
	ds_read_b128 v[2:5], v142 offset:32768
	ds_read_b128 v[6:9], v142 offset:33792
	ds_read_b128 v[10:13], v142 offset:34816
	ds_read_b128 v[14:17], v142 offset:35840
	ds_read_b128 v[144:147], v142 offset:49152
	ds_read_b128 v[148:151], v142 offset:50176
	ds_read_b128 v[152:155], v142 offset:51200
	ds_read_b128 v[156:159], v142 offset:52224
	ds_read_b128 v[18:21], v141 offset:32768
	ds_read_b128 v[22:25], v141 offset:33792
	ds_read_b128 v[26:29], v141 offset:34816
	ds_read_b128 v[30:33], v141 offset:35840
	ds_read_b128 v[34:37], v141 offset:36864
	ds_read_b128 v[38:41], v141 offset:37888
	ds_read_b128 v[42:45], v141 offset:38912
	ds_read_b128 v[46:49], v141 offset:39936
	s_waitcnt vmcnt(8)
	s_waitcnt lgkmcnt(0)
	s_barrier
	s_setprio 1
	s_waitcnt lgkmcnt(0)
	v_mfma_f32_16x16x128_f8f6f4 v[126:129], v[2:9], v[18:25], v[126:129]
	v_mfma_f32_16x16x128_f8f6f4 v[122:125], v[10:17], v[18:25], v[122:125]
	v_mfma_f32_16x16x128_f8f6f4 v[114:117], v[2:9], v[26:33], v[114:117]
	v_mfma_f32_16x16x128_f8f6f4 v[106:109], v[10:17], v[26:33], v[106:109]
	v_mfma_f32_16x16x128_f8f6f4 v[98:101], v[2:9], v[34:41], v[98:101]
	v_mfma_f32_16x16x128_f8f6f4 v[90:93], v[10:17], v[34:41], v[208:211]
	v_mfma_f32_16x16x128_f8f6f4 v[82:85], v[2:9], v[42:49], v[212:215]
	v_mfma_f32_16x16x128_f8f6f4 v[74:77], v[10:17], v[42:49], v[216:219]
	s_setprio 0
	s_setprio 1
	v_mfma_f32_16x16x128_f8f6f4 v[118:121], v[144:151], v[18:25], v[118:121]
	v_mfma_f32_16x16x128_f8f6f4 v[110:113], v[152:159], v[18:25], v[110:113]
	v_mfma_f32_16x16x128_f8f6f4 v[102:105], v[144:151], v[26:33], v[102:105]
	v_mfma_f32_16x16x128_f8f6f4 v[94:97], v[152:159], v[26:33], v[176:179]
	v_mfma_f32_16x16x128_f8f6f4 v[86:89], v[144:151], v[34:41], v[180:183]
	v_mfma_f32_16x16x128_f8f6f4 v[78:81], v[152:159], v[34:41], v[184:187]
	v_mfma_f32_16x16x128_f8f6f4 v[70:73], v[144:151], v[42:49], v[188:191]
	v_mfma_f32_16x16x128_f8f6f4 v[66:69], v[152:159], v[42:49], v[192:195]
	s_setprio 0
	s_barrier
	s_add_u32 s24, s4, s24
	s_addc_u32 s25, s5, 0
	s_mov_b32 m0, s46
	v_lshl_add_u64 v[18:19], s[24:25], 0, v[134:135]
	s_add_i32 s22, s22, 0x20080
	global_load_lds_dwordx4 v[18:19], off
	v_lshl_add_u64 v[18:19], s[24:25], 0, v[252:253]
	s_add_u32 s24, s4, s22
	s_mov_b32 m0, s47
	s_addc_u32 s25, s5, 0
	s_addk_i32 s23, 0x80
	global_load_lds_dwordx4 v[18:19], off
	v_lshl_add_u64 v[18:19], s[24:25], 0, v[134:135]
	s_mov_b32 m0, s50
	s_add_u32 s22, s4, s23
	global_load_lds_dwordx4 v[18:19], off
	v_lshl_add_u64 v[18:19], s[24:25], 0, v[252:253]
	s_mov_b32 m0, s51
	s_addc_u32 s23, s5, 0
	global_load_lds_dwordx4 v[18:19], off
	v_lshl_add_u64 v[18:19], s[22:23], 0, v[136:137]
	s_mov_b32 m0, s48
	s_nop 0
	global_load_lds_dwordx4 v[18:19], off
	v_lshl_add_u64 v[18:19], s[22:23], 0, v[138:139]
	s_mov_b32 m0, s49
	s_nop 0
	global_load_lds_dwordx4 v[18:19], off
	ds_read_b128 v[160:163], v141 offset:49152
	ds_read_b128 v[164:167], v141 offset:50176
	ds_read_b128 v[168:171], v141 offset:51200
	ds_read_b128 v[172:175], v141 offset:52224
	ds_read_b128 v[176:179], v141 offset:53248
	ds_read_b128 v[180:183], v141 offset:54272
	ds_read_b128 v[184:187], v141 offset:55296
	ds_read_b128 v[188:191], v141 offset:56320
	s_waitcnt vmcnt(8)
	s_waitcnt lgkmcnt(0)
	s_barrier
	s_setprio 1
	s_waitcnt lgkmcnt(0)
	v_mfma_f32_16x16x128_f8f6f4 v[62:65], v[2:9], v[160:167], v[62:65]
	v_mfma_f32_16x16x128_f8f6f4 v[58:61], v[10:17], v[160:167], v[58:61]
	v_mfma_f32_16x16x128_f8f6f4 v[50:53], v[2:9], v[168:175], v[50:53]
	v_mfma_f32_16x16x128_f8f6f4 v[42:45], v[10:17], v[168:175], v[196:199]
	v_mfma_f32_16x16x128_f8f6f4 v[34:37], v[2:9], v[176:183], v[200:203]
	v_mfma_f32_16x16x128_f8f6f4 v[26:29], v[10:17], v[176:183], v[204:207]
	v_mfma_f32_16x16x128_f8f6f4 v[18:21], v[2:9], v[184:191], v[220:223]
	v_mfma_f32_16x16x128_f8f6f4 v[10:13], v[10:17], v[184:191], v[224:227]
	s_setprio 0
	s_setprio 1
	v_mfma_f32_16x16x128_f8f6f4 v[54:57], v[144:151], v[160:167], v[54:57]
	v_mfma_f32_16x16x128_f8f6f4 v[46:49], v[152:159], v[160:167], v[228:231]
	v_mfma_f32_16x16x128_f8f6f4 v[38:41], v[144:151], v[168:175], v[232:235]
	v_mfma_f32_16x16x128_f8f6f4 v[30:33], v[152:159], v[168:175], v[236:239]
	v_mfma_f32_16x16x128_f8f6f4 v[22:25], v[144:151], v[176:183], v[240:243]
	v_mfma_f32_16x16x128_f8f6f4 v[14:17], v[152:159], v[176:183], v[244:247]
	v_mfma_f32_16x16x128_f8f6f4 v[6:9], v[144:151], v[184:191], v[248:251]
	v_mfma_f32_16x16x128_f8f6f4 v[2:5], v[152:159], v[184:191], v[130:133]
	s_setprio 0
	s_barrier
	s_add_i32 s20, s20, 2
	s_addk_i32 s19, 0x100
	s_addk_i32 s18, 0x100
	s_cmp_gt_u32 s20, 5
	s_cbranch_scc0 .LBB0_573
	s_and_b64 vcc, exec, s[12:13]
	s_cbranch_vccz .LBB0_576
	s_barrier

; #define PG8_STAGE(bufoff, gbase, voff) do { _Pragma("unroll") for (int _i = 0; _i < 2; ++_i) \
;         __builtin_amdgcn_global_load_lds((const unsigned*)(wsb + (size_t)(gbase) + (voff)[_i]), (LAS unsigned*)(lds + (bufoff) + ldsw + _i * 8192), 16, 0, 0); } while (0)
; #define PG8_LDA(dst, b, h) do { _Pragma("unroll") for (int m = 0; m < 4; ++m) { if constexpr (FP8) dst##8[m] = PG8_LD8(pa, PG8_SA(b, h) + m * 2048); \
;         else { _Pragma("unroll") for (int k = 0; k < 2; ++k) dst[m][k] = *(const LAS bf16x8*)(pa + PG8_SA(b, h) + m * 2048 + k * 1024); } } } while (0)
; #define PG8_LDB(dst, b, h) do { _Pragma("unroll") for (int n = 0; n < 2; ++n) { if constexpr (FP8) dst##8[n] = PG8_LD8(pb, PG8_SA(b, h) + n * 2048); \
;         else { _Pragma("unroll") for (int k = 0; k < 2; ++k) dst[n][k] = *(const LAS bf16x8*)(pb + PG8_SA(b, h) + n * 2048 + k * 1024); } } } while (0)
; #define PG8_WAIT_V(n) asm volatile("s_waitcnt vmcnt(" #n ")" ::: "memory")
; #define PG8_WAIT_L(n) asm volatile("s_waitcnt lgkmcnt(" #n ")" ::: "memory")
; #define PG8_BAR __builtin_amdgcn_s_barrier()
; #define PG8_SCHED __builtin_amdgcn_sched_barrier(0)
; template <class Epi, class Sched, bool PERM, bool FP8 = false, bool GATHER = false>
; DI void gemm_phase(LAS unsigned char* lds, const unsigned char* wsb, const unsigned lda, const unsigned ldb, const int nt, const Sched& S, const Epi& E) {
;     ...
;             PG8_LDB(B0, 0, 0); PG8_LDB(B1, 0, 1); PG8_SCHED; PG8_LDA(At, 0, 0); PG8_STAGEA(PG8_SA(1, 1), t + 1, 1, false);
;             if constexpr (GATHER) { if (last) {
;                 int tz = tid; asm volatile("" : "+v"(tz));
; #pragma unroll
;                 for (int i = 0; i < 2; ++i) { int R, C; stage_rc(tz * 16 + i * 8192, R, C);
; #pragma unroll
;                     for (int h = 0; h < 2; ++h) { const unsigned tk = (unsigned)tokt[h * HALF + R]; offC[h][i] = (tk < (unsigned)NTOK ? tk : (unsigned)(NTOK - 1)) * lda + (unsigned)C * 2u; } } } }
;             PG8_WAIT_V(8); PG8_WAIT_L(0); PG8_BAR; PG8_MMA(0, 0, At, B0); PG8_MMA(0, 1, At, B1); PG8_BAR; PG8_SCHED;
;             PG8_LDA(At, 0, 1); PG8_STAGE(PG8_SB(0, 0), b2, voffB); PG8_STAGE(PG8_SB(0, 1), b2 + hstepB, voffB); PG8_STAGEA(PG8_SA(0, 0), k2, 0, last);
;             PG8_WAIT_V(8); PG8_WAIT_L(0); PG8_BAR; PG8_MMA(1, 0, At, B0); PG8_MMA(1, 1, At, B1); PG8_BAR; PG8_SCHED;
.LBB0_725:
	s_add_i32 s85, s83, s42
	s_add_u32 s54, s42, 0x100
	s_addc_u32 s55, s43, 0
	s_cmp_eq_u32 s84, 4
	s_cselect_b32 s85, s82, s85
	s_mov_b32 m0, s68
	v_lshl_add_u64 v[142:143], v[140:141], 0, s[42:43]
	global_load_lds_dwordx4 v[142:143], off
	v_lshl_add_u64 v[142:143], v[138:139], 0, s[42:43]
	s_mov_b32 m0, s69
	s_cselect_b32 s43, 0, s54
	global_load_lds_dwordx4 v[142:143], off
	ds_read_b128 v[150:153], v147
	ds_read_b128 v[154:157], v147 offset:1024
	ds_read_b128 v[158:161], v147 offset:2048
	ds_read_b128 v[162:165], v147 offset:3072
	ds_read_b128 v[166:169], v147 offset:16384
	ds_read_b128 v[170:173], v147 offset:17408
	ds_read_b128 v[174:177], v147 offset:18432
	ds_read_b128 v[178:181], v147 offset:19456
	ds_read_b128 v[182:185], v146
	ds_read_b128 v[186:189], v146 offset:1024
	ds_read_b128 v[190:193], v146 offset:2048
	ds_read_b128 v[194:197], v146 offset:3072
	ds_read_b128 v[198:201], v146 offset:4096
	ds_read_b128 v[202:205], v146 offset:5120
	ds_read_b128 v[212:215], v146 offset:6144
	ds_read_b128 v[216:219], v146 offset:7168
	s_waitcnt vmcnt(8)
	s_waitcnt lgkmcnt(0)
	s_add_i32 s42, s85, 0x80
	s_barrier
	s_setprio 1
	s_waitcnt lgkmcnt(0)
	v_mfma_f32_16x16x32_bf16 v[126:129], v[150:153], v[182:185], v[126:129]
	v_mfma_f32_16x16x32_bf16 v[122:125], v[158:161], v[182:185], v[122:125]
	v_mfma_f32_16x16x32_bf16 v[110:113], v[150:153], v[190:193], v[110:113]
	v_mfma_f32_16x16x32_bf16 v[106:109], v[158:161], v[190:193], v[106:109]
	v_mfma_f32_16x16x32_bf16 v[94:97], v[150:153], v[198:201], v[94:97]
	v_mfma_f32_16x16x32_bf16 v[90:93], v[158:161], v[198:201], v[90:93]
	v_mfma_f32_16x16x32_bf16 v[78:81], v[150:153], v[212:215], v[78:81]
	v_mfma_f32_16x16x32_bf16 v[74:77], v[158:161], v[212:215], v[74:77]
	v_mfma_f32_16x16x32_bf16 v[126:129], v[154:157], v[186:189], v[126:129]
	v_mfma_f32_16x16x32_bf16 v[122:125], v[162:165], v[186:189], v[122:125]
	v_mfma_f32_16x16x32_bf16 v[110:113], v[154:157], v[194:197], v[110:113]
	v_mfma_f32_16x16x32_bf16 v[106:109], v[162:165], v[194:197], v[106:109]
	v_mfma_f32_16x16x32_bf16 v[94:97], v[154:157], v[202:205], v[94:97]
	v_mfma_f32_16x16x32_bf16 v[90:93], v[162:165], v[202:205], v[90:93]
	v_mfma_f32_16x16x32_bf16 v[78:81], v[154:157], v[216:219], v[78:81]
	v_mfma_f32_16x16x32_bf16 v[74:77], v[162:165], v[216:219], v[74:77]
	s_setprio 0
	s_setprio 1
	v_mfma_f32_16x16x32_bf16 v[118:121], v[166:169], v[182:185], v[118:121]
	v_mfma_f32_16x16x32_bf16 v[114:117], v[174:177], v[182:185], v[114:117]
	v_mfma_f32_16x16x32_bf16 v[102:105], v[166:169], v[190:193], v[102:105]
	v_mfma_f32_16x16x32_bf16 v[98:101], v[174:177], v[190:193], v[98:101]
	v_mfma_f32_16x16x32_bf16 v[86:89], v[166:169], v[198:201], v[86:89]
	v_mfma_f32_16x16x32_bf16 v[82:85], v[174:177], v[198:201], v[82:85]
	v_mfma_f32_16x16x32_bf16 v[70:73], v[166:169], v[212:215], v[70:73]
	v_mfma_f32_16x16x32_bf16 v[66:69], v[174:177], v[212:215], v[66:69]
	v_mfma_f32_16x16x32_bf16 v[118:121], v[170:173], v[186:189], v[118:121]
	v_mfma_f32_16x16x32_bf16 v[114:117], v[178:181], v[186:189], v[114:117]
	v_mfma_f32_16x16x32_bf16 v[102:105], v[170:173], v[194:197], v[102:105]
	v_mfma_f32_16x16x32_bf16 v[98:101], v[178:181], v[194:197], v[98:101]
	v_mfma_f32_16x16x32_bf16 v[86:89], v[170:173], v[202:205], v[86:89]
	v_mfma_f32_16x16x32_bf16 v[82:85], v[178:181], v[202:205], v[82:85]
	v_mfma_f32_16x16x32_bf16 v[70:73], v[170:173], v[216:219], v[70:73]
	v_mfma_f32_16x16x32_bf16 v[66:69], v[178:181], v[216:219], v[66:69]
	s_setprio 0
	s_barrier
	s_add_u32 s86, s6, s85
	s_addc_u32 s87, s7, 0
	s_mov_b32 m0, s47
	v_lshl_add_u64 v[142:143], s[86:87], 0, v[134:135]
	global_load_lds_dwordx4 v[142:143], off
	v_lshl_add_u64 v[142:143], s[86:87], 0, v[130:131]
	s_add_i32 s86, s85, 0x20000
	s_add_u32 s86, s6, s86
	s_addc_u32 s87, s7, 0
	s_mov_b32 m0, s48
	s_add_u32 s88, s6, s43
	global_load_lds_dwordx4 v[142:143], off
	v_lshl_add_u64 v[142:143], s[86:87], 0, v[134:135]
	s_mov_b32 m0, s49
	s_addc_u32 s89, s7, 0
	global_load_lds_dwordx4 v[142:143], off
	v_lshl_add_u64 v[142:143], s[86:87], 0, v[130:131]
	s_add_u32 s86, s88, 0x1d094000
	s_mov_b32 m0, s56
	s_addc_u32 s87, s89, 0
	global_load_lds_dwordx4 v[142:143], off
	v_lshl_add_u64 v[142:143], s[86:87], 0, v[136:137]
	s_mov_b32 m0, s46
	s_nop 0
	global_load_lds_dwordx4 v[142:143], off
	v_lshl_add_u64 v[142:143], s[86:87], 0, v[132:133]
	s_mov_b32 m0, s57
	s_nop 0
	global_load_lds_dwordx4 v[142:143], off
	ds_read_b128 v[182:185], v146 offset:16384
	ds_read_b128 v[186:189], v146 offset:17408
	ds_read_b128 v[190:193], v146 offset:18432
	ds_read_b128 v[194:197], v146 offset:19456
	ds_read_b128 v[198:201], v146 offset:20480
	ds_read_b128 v[202:205], v146 offset:21504
	ds_read_b128 v[212:215], v146 offset:22528
	ds_read_b128 v[216:219], v146 offset:23552
	s_waitcnt vmcnt(8)
	s_waitcnt lgkmcnt(0)
	s_barrier
; #define PG8_STAGE(bufoff, gbase, voff) do { _Pragma("unroll") for (int _i = 0; _i < 2; ++_i) \
;         __builtin_amdgcn_global_load_lds((const unsigned*)(wsb + (size_t)(gbase) + (voff)[_i]), (LAS unsigned*)(lds + (bufoff) + ldsw + _i * 8192), 16, 0, 0); } while (0)
; #define PG8_LDA(dst, b, h) do { _Pragma("unroll") for (int m = 0; m < 4; ++m) { if constexpr (FP8) dst##8[m] = PG8_LD8(pa, PG8_SA(b, h) + m * 2048); \
;         else { _Pragma("unroll") for (int k = 0; k < 2; ++k) dst[m][k] = *(const LAS bf16x8*)(pa + PG8_SA(b, h) + m * 2048 + k * 1024); } } } while (0)
; #define PG8_LDB(dst, b, h) do { _Pragma("unroll") for (int n = 0; n < 2; ++n) { if constexpr (FP8) dst##8[n] = PG8_LD8(pb, PG8_SA(b, h) + n * 2048); \
;         else { _Pragma("unroll") for (int k = 0; k < 2; ++k) dst[n][k] = *(const LAS bf16x8*)(pb + PG8_SA(b, h) + n * 2048 + k * 1024); } } } while (0)
; #define PG8_WAIT_V(n) asm volatile("s_waitcnt vmcnt(" #n ")" ::: "memory")
; #define PG8_WAIT_L(n) asm volatile("s_waitcnt lgkmcnt(" #n ")" ::: "memory")
; #define PG8_BAR __builtin_amdgcn_s_barrier()
; #define PG8_SCHED __builtin_amdgcn_sched_barrier(0)
; template <class Epi, class Sched, bool PERM, bool FP8 = false, bool GATHER = false>
; DI void gemm_phase(LAS unsigned char* lds, const unsigned char* wsb, const unsigned lda, const unsigned ldb, const int nt, const Sched& S, const Epi& E) {
;     ...
;             PG8_WAIT_V(8); PG8_WAIT_L(0); PG8_BAR; PG8_MMA(0, 0, At, B0); PG8_MMA(0, 1, At, B1); PG8_BAR; PG8_SCHED;
;             PG8_LDA(At, 0, 1); PG8_STAGE(PG8_SB(0, 0), b2, voffB); PG8_STAGE(PG8_SB(0, 1), b2 + hstepB, voffB); PG8_STAGEA(PG8_SA(0, 0), k2, 0, last);
;             PG8_WAIT_V(8); PG8_WAIT_L(0); PG8_BAR; PG8_MMA(1, 0, At, B0); PG8_MMA(1, 1, At, B1); PG8_BAR; PG8_SCHED;
;             PG8_LDB(B0, 1, 0); PG8_LDB(B1, 1, 1); PG8_SCHED; PG8_LDA(At, 1, 0); PG8_STAGEA(PG8_SA(0, 1), k2, 1, last);
;             PG8_WAIT_V(8); PG8_WAIT_L(0); PG8_BAR; PG8_MMA(0, 0, At, B0); PG8_MMA(0, 1, At, B1); PG8_BAR; PG8_SCHED;
	s_setprio 1
	s_waitcnt lgkmcnt(0)
	v_mfma_f32_16x16x32_bf16 v[62:65], v[150:153], v[182:185], v[62:65]
	v_mfma_f32_16x16x32_bf16 v[58:61], v[158:161], v[182:185], v[58:61]
	v_mfma_f32_16x16x32_bf16 v[46:49], v[150:153], v[190:193], v[46:49]
	v_mfma_f32_16x16x32_bf16 v[42:45], v[158:161], v[190:193], v[42:45]
	v_mfma_f32_16x16x32_bf16 v[30:33], v[150:153], v[198:201], v[30:33]
	v_mfma_f32_16x16x32_bf16 v[26:29], v[158:161], v[198:201], v[26:29]
	v_mfma_f32_16x16x32_bf16 v[14:17], v[150:153], v[212:215], v[14:17]
	v_mfma_f32_16x16x32_bf16 v[10:13], v[158:161], v[212:215], v[10:13]
	v_mfma_f32_16x16x32_bf16 v[62:65], v[154:157], v[186:189], v[62:65]
	v_mfma_f32_16x16x32_bf16 v[58:61], v[162:165], v[186:189], v[58:61]
	v_mfma_f32_16x16x32_bf16 v[46:49], v[154:157], v[194:197], v[46:49]
	v_mfma_f32_16x16x32_bf16 v[42:45], v[162:165], v[194:197], v[42:45]
	v_mfma_f32_16x16x32_bf16 v[30:33], v[154:157], v[202:205], v[30:33]
	v_mfma_f32_16x16x32_bf16 v[26:29], v[162:165], v[202:205], v[26:29]
	v_mfma_f32_16x16x32_bf16 v[14:17], v[154:157], v[216:219], v[14:17]
	v_mfma_f32_16x16x32_bf16 v[10:13], v[162:165], v[216:219], v[10:13]
	s_setprio 0
	s_setprio 1
	v_mfma_f32_16x16x32_bf16 v[54:57], v[166:169], v[182:185], v[54:57]
	v_mfma_f32_16x16x32_bf16 v[50:53], v[174:177], v[182:185], v[50:53]
	v_mfma_f32_16x16x32_bf16 v[38:41], v[166:169], v[190:193], v[38:41]
	v_mfma_f32_16x16x32_bf16 v[34:37], v[174:177], v[190:193], v[34:37]
	v_mfma_f32_16x16x32_bf16 v[22:25], v[166:169], v[198:201], v[22:25]
	v_mfma_f32_16x16x32_bf16 v[18:21], v[174:177], v[198:201], v[18:21]
	v_mfma_f32_16x16x32_bf16 v[6:9], v[166:169], v[212:215], v[6:9]
	v_mfma_f32_16x16x32_bf16 v[2:5], v[174:177], v[212:215], v[2:5]
	v_mfma_f32_16x16x32_bf16 v[54:57], v[170:173], v[186:189], v[54:57]
	v_mfma_f32_16x16x32_bf16 v[50:53], v[178:181], v[186:189], v[50:53]
	v_mfma_f32_16x16x32_bf16 v[38:41], v[170:173], v[194:197], v[38:41]
	v_mfma_f32_16x16x32_bf16 v[34:37], v[178:181], v[194:197], v[34:37]
	v_mfma_f32_16x16x32_bf16 v[22:25], v[170:173], v[202:205], v[22:25]
	v_mfma_f32_16x16x32_bf16 v[18:21], v[178:181], v[202:205], v[18:21]
	v_mfma_f32_16x16x32_bf16 v[6:9], v[170:173], v[216:219], v[6:9]
	v_mfma_f32_16x16x32_bf16 v[2:5], v[178:181], v[216:219], v[2:5]
	s_setprio 0
	s_barrier
	s_add_u32 s86, s88, 0x1d0b4000
	s_addc_u32 s87, s89, 0
	s_mov_b32 m0, s58
	v_lshl_add_u64 v[142:143], s[86:87], 0, v[136:137]
	global_load_lds_dwordx4 v[142:143], off
	v_lshl_add_u64 v[142:143], s[86:87], 0, v[132:133]
	s_mov_b32 m0, s59
	s_nop 0
	global_load_lds_dwordx4 v[142:143], off
	ds_read_b128 v[150:153], v147 offset:32768
	ds_read_b128 v[154:157], v147 offset:33792
	ds_read_b128 v[158:161], v147 offset:34816
	ds_read_b128 v[162:165], v147 offset:35840
	ds_read_b128 v[166:169], v147 offset:49152
	ds_read_b128 v[170:173], v147 offset:50176
	ds_read_b128 v[174:177], v147 offset:51200
	ds_read_b128 v[178:181], v147 offset:52224
	ds_read_b128 v[182:185], v146 offset:32768
	ds_read_b128 v[186:189], v146 offset:33792
	ds_read_b128 v[190:193], v146 offset:34816
	ds_read_b128 v[194:197], v146 offset:35840
	ds_read_b128 v[198:201], v146 offset:36864
	ds_read_b128 v[202:205], v146 offset:37888
	ds_read_b128 v[212:215], v146 offset:38912
	ds_read_b128 v[216:219], v146 offset:39936
	s_waitcnt vmcnt(8)
	s_waitcnt lgkmcnt(0)
	s_barrier
	s_setprio 1
	s_waitcnt lgkmcnt(0)
	v_mfma_f32_16x16x32_bf16 v[126:129], v[150:153], v[182:185], v[126:129]
	v_mfma_f32_16x16x32_bf16 v[122:125], v[158:161], v[182:185], v[122:125]
	v_mfma_f32_16x16x32_bf16 v[110:113], v[150:153], v[190:193], v[110:113]
	v_mfma_f32_16x16x32_bf16 v[106:109], v[158:161], v[190:193], v[106:109]
	v_mfma_f32_16x16x32_bf16 v[94:97], v[150:153], v[198:201], v[94:97]
	v_mfma_f32_16x16x32_bf16 v[90:93], v[158:161], v[198:201], v[90:93]
	v_mfma_f32_16x16x32_bf16 v[78:81], v[150:153], v[212:215], v[78:81]
	v_mfma_f32_16x16x32_bf16 v[74:77], v[158:161], v[212:215], v[74:77]
	v_mfma_f32_16x16x32_bf16 v[126:129], v[154:157], v[186:189], v[126:129]
	v_mfma_f32_16x16x32_bf16 v[122:125], v[162:165], v[186:189], v[122:125]
	v_mfma_f32_16x16x32_bf16 v[110:113], v[154:157], v[194:197], v[110:113]
	v_mfma_f32_16x16x32_bf16 v[106:109], v[162:165], v[194:197], v[106:109]
	v_mfma_f32_16x16x32_bf16 v[94:97], v[154:157], v[202:205], v[94:97]
	v_mfma_f32_16x16x32_bf16 v[90:93], v[162:165], v[202:205], v[90:93]
	v_mfma_f32_16x16x32_bf16 v[78:81], v[154:157], v[216:219], v[78:81]
	v_mfma_f32_16x16x32_bf16 v[74:77], v[162:165], v[216:219], v[74:77]
	s_setprio 0
	s_setprio 1
	v_mfma_f32_16x16x32_bf16 v[118:121], v[166:169], v[182:185], v[118:121]
	v_mfma_f32_16x16x32_bf16 v[114:117], v[174:177], v[182:185], v[114:117]
	v_mfma_f32_16x16x32_bf16 v[102:105], v[166:169], v[190:193], v[102:105]
	v_mfma_f32_16x16x32_bf16 v[98:101], v[174:177], v[190:193], v[98:101]
	v_mfma_f32_16x16x32_bf16 v[86:89], v[166:169], v[198:201], v[86:89]
	v_mfma_f32_16x16x32_bf16 v[82:85], v[174:177], v[198:201], v[82:85]
	v_mfma_f32_16x16x32_bf16 v[70:73], v[166:169], v[212:215], v[70:73]
	v_mfma_f32_16x16x32_bf16 v[66:69], v[174:177], v[212:215], v[66:69]
	v_mfma_f32_16x16x32_bf16 v[118:121], v[170:173], v[186:189], v[118:121]
	v_mfma_f32_16x16x32_bf16 v[114:117], v[178:181], v[186:189], v[114:117]
	v_mfma_f32_16x16x32_bf16 v[102:105], v[170:173], v[194:197], v[102:105]
	v_mfma_f32_16x16x32_bf16 v[98:101], v[178:181], v[194:197], v[98:101]
	v_mfma_f32_16x16x32_bf16 v[86:89], v[170:173], v[202:205], v[86:89]
	v_mfma_f32_16x16x32_bf16 v[82:85], v[178:181], v[202:205], v[82:85]
	v_mfma_f32_16x16x32_bf16 v[70:73], v[170:173], v[216:219], v[70:73]
	v_mfma_f32_16x16x32_bf16 v[66:69], v[178:181], v[216:219], v[66:69]
	s_setprio 0
	s_barrier
; #define PG8_STAGE(bufoff, gbase, voff) do { _Pragma("unroll") for (int _i = 0; _i < 2; ++_i) \
;         __builtin_amdgcn_global_load_lds((const unsigned*)(wsb + (size_t)(gbase) + (voff)[_i]), (LAS unsigned*)(lds + (bufoff) + ldsw + _i * 8192), 16, 0, 0); } while (0)
; #define PG8_LDA(dst, b, h) do { _Pragma("unroll") for (int m = 0; m < 4; ++m) { if constexpr (FP8) dst##8[m] = PG8_LD8(pa, PG8_SA(b, h) + m * 2048); \
;         else { _Pragma("unroll") for (int k = 0; k < 2; ++k) dst[m][k] = *(const LAS bf16x8*)(pa + PG8_SA(b, h) + m * 2048 + k * 1024); } } } while (0)
; #define PG8_WAIT_V(n) asm volatile("s_waitcnt vmcnt(" #n ")" ::: "memory")
; #define PG8_WAIT_L(n) asm volatile("s_waitcnt lgkmcnt(" #n ")" ::: "memory")
; #define PG8_BAR __builtin_amdgcn_s_barrier()
; #define PG8_SCHED __builtin_amdgcn_sched_barrier(0)
; template <class Epi, class Sched, bool PERM, bool FP8 = false, bool GATHER = false>
; DI void gemm_phase(LAS unsigned char* lds, const unsigned char* wsb, const unsigned lda, const unsigned ldb, const int nt, const Sched& S, const Epi& E) {
;     ...
;             PG8_LDA(At, 1, 1); PG8_STAGE(PG8_SB(1, 0), b3, voffB); PG8_STAGE(PG8_SB(1, 1), b3 + hstepB, voffB); PG8_STAGEA(PG8_SA(1, 0), k3, 0, last);
;             PG8_WAIT_V(8); PG8_WAIT_L(0); PG8_BAR; PG8_MMA(1, 0, At, B0); PG8_MMA(1, 1, At, B1); PG8_BAR; PG8_SCHED;
;         }
;         if (wr == 0) PG8_BAR;
	s_add_u32 s42, s6, s42
	s_addc_u32 s43, s7, 0
	s_mov_b32 m0, s60
	v_lshl_add_u64 v[142:143], s[42:43], 0, v[134:135]
	s_add_i32 s85, s85, 0x20080
	global_load_lds_dwordx4 v[142:143], off
	v_lshl_add_u64 v[142:143], s[42:43], 0, v[130:131]
	s_add_u32 s42, s6, s85
	s_mov_b32 m0, s61
	s_addc_u32 s43, s7, 0
	global_load_lds_dwordx4 v[142:143], off
	v_lshl_add_u64 v[142:143], s[42:43], 0, v[134:135]
	s_mov_b32 m0, s65
	s_nop 0
	global_load_lds_dwordx4 v[142:143], off
	v_lshl_add_u64 v[142:143], s[42:43], 0, v[130:131]
	s_add_u32 s42, s88, 0x1d094080
	s_mov_b32 m0, s66
	s_addc_u32 s43, s89, 0
	global_load_lds_dwordx4 v[142:143], off
	v_lshl_add_u64 v[142:143], s[42:43], 0, v[136:137]
	s_mov_b32 m0, s62
	s_nop 0
	global_load_lds_dwordx4 v[142:143], off
	v_lshl_add_u64 v[142:143], s[42:43], 0, v[132:133]
	s_mov_b32 m0, s63
	s_nop 0
	global_load_lds_dwordx4 v[142:143], off
	ds_read_b128 v[182:185], v146 offset:49152
	ds_read_b128 v[186:189], v146 offset:50176
	ds_read_b128 v[190:193], v146 offset:51200
	ds_read_b128 v[194:197], v146 offset:52224
	ds_read_b128 v[198:201], v146 offset:53248
	ds_read_b128 v[202:205], v146 offset:54272
	ds_read_b128 v[212:215], v146 offset:55296
	ds_read_b128 v[216:219], v146 offset:56320
	s_waitcnt vmcnt(8)
	s_waitcnt lgkmcnt(0)
	s_barrier
	s_setprio 1
	s_waitcnt lgkmcnt(0)
	v_mfma_f32_16x16x32_bf16 v[62:65], v[150:153], v[182:185], v[62:65]
	v_mfma_f32_16x16x32_bf16 v[58:61], v[158:161], v[182:185], v[58:61]
	v_mfma_f32_16x16x32_bf16 v[46:49], v[150:153], v[190:193], v[46:49]
	v_mfma_f32_16x16x32_bf16 v[42:45], v[158:161], v[190:193], v[42:45]
	v_mfma_f32_16x16x32_bf16 v[30:33], v[150:153], v[198:201], v[30:33]
	v_mfma_f32_16x16x32_bf16 v[26:29], v[158:161], v[198:201], v[26:29]
	v_mfma_f32_16x16x32_bf16 v[14:17], v[150:153], v[212:215], v[14:17]
	v_mfma_f32_16x16x32_bf16 v[10:13], v[158:161], v[212:215], v[10:13]
	v_mfma_f32_16x16x32_bf16 v[62:65], v[154:157], v[186:189], v[62:65]
	v_mfma_f32_16x16x32_bf16 v[58:61], v[162:165], v[186:189], v[58:61]
	v_mfma_f32_16x16x32_bf16 v[46:49], v[154:157], v[194:197], v[46:49]
	v_mfma_f32_16x16x32_bf16 v[42:45], v[162:165], v[194:197], v[42:45]
	v_mfma_f32_16x16x32_bf16 v[30:33], v[154:157], v[202:205], v[30:33]
	v_mfma_f32_16x16x32_bf16 v[26:29], v[162:165], v[202:205], v[26:29]
	v_mfma_f32_16x16x32_bf16 v[14:17], v[154:157], v[216:219], v[14:17]
	v_mfma_f32_16x16x32_bf16 v[10:13], v[162:165], v[216:219], v[10:13]
	s_setprio 0
	s_setprio 1
	v_mfma_f32_16x16x32_bf16 v[54:57], v[166:169], v[182:185], v[54:57]
	v_mfma_f32_16x16x32_bf16 v[50:53], v[174:177], v[182:185], v[50:53]
	v_mfma_f32_16x16x32_bf16 v[38:41], v[166:169], v[190:193], v[38:41]
	v_mfma_f32_16x16x32_bf16 v[34:37], v[174:177], v[190:193], v[34:37]
	v_mfma_f32_16x16x32_bf16 v[22:25], v[166:169], v[198:201], v[22:25]
	v_mfma_f32_16x16x32_bf16 v[18:21], v[174:177], v[198:201], v[18:21]
	v_mfma_f32_16x16x32_bf16 v[6:9], v[166:169], v[212:215], v[6:9]
	v_mfma_f32_16x16x32_bf16 v[2:5], v[174:177], v[212:215], v[2:5]
	v_mfma_f32_16x16x32_bf16 v[54:57], v[170:173], v[186:189], v[54:57]
	v_mfma_f32_16x16x32_bf16 v[50:53], v[178:181], v[186:189], v[50:53]
	v_mfma_f32_16x16x32_bf16 v[38:41], v[170:173], v[194:197], v[38:41]
	v_mfma_f32_16x16x32_bf16 v[34:37], v[178:181], v[194:197], v[34:37]
	v_mfma_f32_16x16x32_bf16 v[22:25], v[170:173], v[202:205], v[22:25]
	v_mfma_f32_16x16x32_bf16 v[18:21], v[178:181], v[202:205], v[18:21]
	v_mfma_f32_16x16x32_bf16 v[6:9], v[170:173], v[216:219], v[6:9]
	v_mfma_f32_16x16x32_bf16 v[2:5], v[178:181], v[216:219], v[2:5]
	s_setprio 0
	s_barrier
	s_add_i32 s84, s84, 2
	s_cmp_gt_u32 s84, 5
	s_mov_b64 s[42:43], s[54:55]
	s_cbranch_scc0 .LBB0_725
	s_and_b64 vcc, exec, s[10:11]
	s_cbranch_vccz .LBB0_728
	s_barrier

; #define PG8_STAGE(bufoff, gbase, voff) do { _Pragma("unroll") for (int _i = 0; _i < 2; ++_i) \
;         __builtin_amdgcn_global_load_lds((const unsigned*)(wsb + (size_t)(gbase) + (voff)[_i]), (LAS unsigned*)(lds + (bufoff) + ldsw + _i * 8192), 16, 0, 0); } while (0)
; #define PG8_LDA(dst, b, h) do { _Pragma("unroll") for (int m = 0; m < 4; ++m) { if constexpr (FP8) dst##8[m] = PG8_LD8(pa, PG8_SA(b, h) + m * 2048); \
;         else { _Pragma("unroll") for (int k = 0; k < 2; ++k) dst[m][k] = *(const LAS bf16x8*)(pa + PG8_SA(b, h) + m * 2048 + k * 1024); } } } while (0)
; #define PG8_LDB(dst, b, h) do { _Pragma("unroll") for (int n = 0; n < 2; ++n) { if constexpr (FP8) dst##8[n] = PG8_LD8(pb, PG8_SA(b, h) + n * 2048); \
;         else { _Pragma("unroll") for (int k = 0; k < 2; ++k) dst[n][k] = *(const LAS bf16x8*)(pb + PG8_SA(b, h) + n * 2048 + k * 1024); } } } while (0)
; #define PG8_WAIT_V(n) asm volatile("s_waitcnt vmcnt(" #n ")" ::: "memory")
; #define PG8_WAIT_L(n) asm volatile("s_waitcnt lgkmcnt(" #n ")" ::: "memory")
; #define PG8_BAR __builtin_amdgcn_s_barrier()
; #define PG8_SCHED __builtin_amdgcn_sched_barrier(0)
; template <class Epi, class Sched, bool PERM, bool FP8 = false, bool GATHER = false>
; DI void gemm_phase(LAS unsigned char* lds, const unsigned char* wsb, const unsigned lda, const unsigned ldb, const int nt, const Sched& S, const Epi& E) {
;     ...
;             PG8_LDB(B0, 0, 0); PG8_LDB(B1, 0, 1); PG8_SCHED; PG8_LDA(At, 0, 0); PG8_STAGEA(PG8_SA(1, 1), t + 1, 1, false);
;             if constexpr (GATHER) { if (last) {
;                 int tz = tid; asm volatile("" : "+v"(tz));
; #pragma unroll
;                 for (int i = 0; i < 2; ++i) { int R, C; stage_rc(tz * 16 + i * 8192, R, C);
; #pragma unroll
;                     for (int h = 0; h < 2; ++h) { const unsigned tk = (unsigned)tokt[h * HALF + R]; offC[h][i] = (tk < (unsigned)NTOK ? tk : (unsigned)(NTOK - 1)) * lda + (unsigned)C * 2u; } } } }
;             PG8_WAIT_V(8); PG8_WAIT_L(0); PG8_BAR; PG8_MMA(0, 0, At, B0); PG8_MMA(0, 1, At, B1); PG8_BAR; PG8_SCHED;
;             PG8_LDA(At, 0, 1); PG8_STAGE(PG8_SB(0, 0), b2, voffB); PG8_STAGE(PG8_SB(0, 1), b2 + hstepB, voffB); PG8_STAGEA(PG8_SA(0, 0), k2, 0, last);
;             PG8_WAIT_V(8); PG8_WAIT_L(0); PG8_BAR; PG8_MMA(1, 0, At, B0); PG8_MMA(1, 1, At, B1); PG8_BAR; PG8_SCHED;
.LBB0_910:
	s_add_i32 s25, s21, 0xfffe0080
	s_cmp_eq_u32 s23, 4
	s_cselect_b32 s24, s59, s22
	s_cselect_b32 s25, s58, s25
	s_add_i32 s61, s24, 0x80
	s_add_u32 s62, s6, s21
	s_addc_u32 s63, s7, 0
	s_mov_b32 m0, s54
	v_lshl_add_u64 v[158:159], s[62:63], 0, v[148:149]
	global_load_lds_dwordx4 v[158:159], off
	v_lshl_add_u64 v[158:159], s[62:63], 0, v[146:147]
	s_mov_b32 m0, s55
	s_nop 0
	global_load_lds_dwordx4 v[158:159], off
	ds_read_b128 v[130:133], v162
	ds_read_b128 v[134:137], v162 offset:1024
	ds_read_b128 v[138:141], v162 offset:2048
	ds_read_b128 v[142:145], v162 offset:3072
	ds_read_b128 v[150:153], v162 offset:16384
	ds_read_b128 v[154:157], v162 offset:17408
	ds_read_b128 v[164:167], v162 offset:18432
	ds_read_b128 v[168:171], v162 offset:19456
	ds_read_b128 v[172:175], v161
	ds_read_b128 v[176:179], v161 offset:1024
	ds_read_b128 v[180:183], v161 offset:2048
	ds_read_b128 v[184:187], v161 offset:3072
	ds_read_b128 v[188:191], v161 offset:4096
	ds_read_b128 v[192:195], v161 offset:5120
	ds_read_b128 v[196:199], v161 offset:6144
	ds_read_b128 v[200:203], v161 offset:7168
	s_waitcnt vmcnt(8)
	s_waitcnt lgkmcnt(0)
	s_barrier
	s_setprio 1
	s_waitcnt lgkmcnt(0)
	v_mfma_f32_16x16x128_f8f6f4 v[126:129], v[130:137], v[172:179], v[126:129]
	v_mfma_f32_16x16x128_f8f6f4 v[122:125], v[138:145], v[172:179], v[122:125]
	v_mfma_f32_16x16x128_f8f6f4 v[118:121], v[130:137], v[180:187], v[118:121]
	v_mfma_f32_16x16x128_f8f6f4 v[114:117], v[138:145], v[180:187], v[114:117]
	v_mfma_f32_16x16x128_f8f6f4 v[102:105], v[130:137], v[188:195], v[102:105]
	v_mfma_f32_16x16x128_f8f6f4 v[98:101], v[138:145], v[188:195], v[98:101]
	v_mfma_f32_16x16x128_f8f6f4 v[204:207], v[130:137], v[196:203], v[86:89]
	v_mfma_f32_16x16x128_f8f6f4 v[208:211], v[138:145], v[196:203], v[78:81]
	s_setprio 0
	s_setprio 1
	v_mfma_f32_16x16x128_f8f6f4 v[110:113], v[150:157], v[172:179], v[110:113]
	v_mfma_f32_16x16x128_f8f6f4 v[106:109], v[164:171], v[172:179], v[106:109]
	v_mfma_f32_16x16x128_f8f6f4 v[172:175], v[150:157], v[180:187], v[94:97]
	v_mfma_f32_16x16x128_f8f6f4 v[176:179], v[164:171], v[180:187], v[90:93]
	v_mfma_f32_16x16x128_f8f6f4 v[180:183], v[150:157], v[188:195], v[82:85]
	v_mfma_f32_16x16x128_f8f6f4 v[184:187], v[164:171], v[188:195], v[74:77]
	v_mfma_f32_16x16x128_f8f6f4 v[188:191], v[150:157], v[196:203], v[70:73]
	v_mfma_f32_16x16x128_f8f6f4 v[192:195], v[164:171], v[196:203], v[66:69]
	s_setprio 0
	s_barrier
	s_add_u32 s62, s6, s24
	s_addc_u32 s63, s7, 0
	s_mov_b32 m0, s36
	v_lshl_add_u64 v[158:159], s[62:63], 0, v[148:149]
	s_nop 0
	global_load_lds_dwordx4 v[158:159], off
	v_lshl_add_u64 v[158:159], s[62:63], 0, v[146:147]
	s_add_i32 s62, s24, 0x20000
	s_add_u32 s62, s6, s62
	s_mov_b32 m0, s37
	s_addc_u32 s63, s7, 0
	global_load_lds_dwordx4 v[158:159], off
	v_lshl_add_u64 v[158:159], s[62:63], 0, v[148:149]
	s_mov_b32 m0, s38
	s_nop 0
	global_load_lds_dwordx4 v[158:159], off
	v_lshl_add_u64 v[158:159], s[62:63], 0, v[146:147]
	s_add_u32 s62, s6, s25
	s_mov_b32 m0, s39
	s_addc_u32 s63, s7, 0
	global_load_lds_dwordx4 v[158:159], off
	v_lshl_add_u64 v[158:159], s[62:63], 0, v[148:149]
	s_mov_b32 m0, s29
	s_nop 0
	global_load_lds_dwordx4 v[158:159], off
	v_lshl_add_u64 v[158:159], s[62:63], 0, v[146:147]
	s_mov_b32 m0, s40
	s_nop 0
	global_load_lds_dwordx4 v[158:159], off
	ds_read_b128 v[66:69], v161 offset:16384
	ds_read_b128 v[70:73], v161 offset:17408
	ds_read_b128 v[74:77], v161 offset:18432
	ds_read_b128 v[78:81], v161 offset:19456
	ds_read_b128 v[82:85], v161 offset:20480
	ds_read_b128 v[86:89], v161 offset:21504
	ds_read_b128 v[90:93], v161 offset:22528
	ds_read_b128 v[94:97], v161 offset:23552
	s_waitcnt vmcnt(8)
	s_waitcnt lgkmcnt(0)
	s_barrier
	s_setprio 1
	s_waitcnt lgkmcnt(0)
	v_mfma_f32_16x16x128_f8f6f4 v[62:65], v[130:137], v[66:73], v[62:65]
	v_mfma_f32_16x16x128_f8f6f4 v[58:61], v[138:145], v[66:73], v[58:61]
	v_mfma_f32_16x16x128_f8f6f4 v[50:53], v[130:137], v[74:81], v[50:53]
	v_mfma_f32_16x16x128_f8f6f4 v[196:199], v[138:145], v[74:81], v[42:45]
	v_mfma_f32_16x16x128_f8f6f4 v[200:203], v[130:137], v[82:89], v[38:41]
	v_mfma_f32_16x16x128_f8f6f4 v[212:215], v[138:145], v[82:89], v[30:33]
	v_mfma_f32_16x16x128_f8f6f4 v[216:219], v[130:137], v[90:97], v[22:25]
	v_mfma_f32_16x16x128_f8f6f4 v[220:223], v[138:145], v[90:97], v[14:17]
	s_setprio 0
	s_setprio 1
	v_mfma_f32_16x16x128_f8f6f4 v[54:57], v[150:157], v[66:73], v[54:57]
	v_mfma_f32_16x16x128_f8f6f4 v[224:227], v[164:171], v[66:73], v[46:49]
	v_mfma_f32_16x16x128_f8f6f4 v[228:231], v[150:157], v[74:81], v[34:37]
	v_mfma_f32_16x16x128_f8f6f4 v[232:235], v[164:171], v[74:81], v[26:29]
	v_mfma_f32_16x16x128_f8f6f4 v[236:239], v[150:157], v[82:89], v[18:21]
	v_mfma_f32_16x16x128_f8f6f4 v[240:243], v[164:171], v[82:89], v[10:13]
	v_mfma_f32_16x16x128_f8f6f4 v[244:247], v[150:157], v[90:97], v[6:9]
	v_mfma_f32_16x16x128_f8f6f4 v[248:251], v[164:171], v[90:97], v[2:5]
	s_setprio 0
	s_barrier
; #define PG8_STAGE(bufoff, gbase, voff) do { _Pragma("unroll") for (int _i = 0; _i < 2; ++_i) \
;         __builtin_amdgcn_global_load_lds((const unsigned*)(wsb + (size_t)(gbase) + (voff)[_i]), (LAS unsigned*)(lds + (bufoff) + ldsw + _i * 8192), 16, 0, 0); } while (0)
; #define PG8_LDA(dst, b, h) do { _Pragma("unroll") for (int m = 0; m < 4; ++m) { if constexpr (FP8) dst##8[m] = PG8_LD8(pa, PG8_SA(b, h) + m * 2048); \
;         else { _Pragma("unroll") for (int k = 0; k < 2; ++k) dst[m][k] = *(const LAS bf16x8*)(pa + PG8_SA(b, h) + m * 2048 + k * 1024); } } } while (0)
; #define PG8_LDB(dst, b, h) do { _Pragma("unroll") for (int n = 0; n < 2; ++n) { if constexpr (FP8) dst##8[n] = PG8_LD8(pb, PG8_SA(b, h) + n * 2048); \
;         else { _Pragma("unroll") for (int k = 0; k < 2; ++k) dst[n][k] = *(const LAS bf16x8*)(pb + PG8_SA(b, h) + n * 2048 + k * 1024); } } } while (0)
; #define PG8_WAIT_V(n) asm volatile("s_waitcnt vmcnt(" #n ")" ::: "memory")
; #define PG8_WAIT_L(n) asm volatile("s_waitcnt lgkmcnt(" #n ")" ::: "memory")
; #define PG8_BAR __builtin_amdgcn_s_barrier()
; #define PG8_SCHED __builtin_amdgcn_sched_barrier(0)
; template <class Epi, class Sched, bool PERM, bool FP8 = false, bool GATHER = false>
; DI void gemm_phase(LAS unsigned char* lds, const unsigned char* wsb, const unsigned lda, const unsigned ldb, const int nt, const Sched& S, const Epi& E) {
;     ...
;             PG8_LDB(B0, 1, 0); PG8_LDB(B1, 1, 1); PG8_SCHED; PG8_LDA(At, 1, 0); PG8_STAGEA(PG8_SA(0, 1), k2, 1, last);
;             PG8_WAIT_V(8); PG8_WAIT_L(0); PG8_BAR; PG8_MMA(0, 0, At, B0); PG8_MMA(0, 1, At, B1); PG8_BAR; PG8_SCHED;
;             PG8_LDA(At, 1, 1); PG8_STAGE(PG8_SB(1, 0), b3, voffB); PG8_STAGE(PG8_SB(1, 1), b3 + hstepB, voffB); PG8_STAGEA(PG8_SA(1, 0), k3, 0, last);
;             PG8_WAIT_V(8); PG8_WAIT_L(0); PG8_BAR; PG8_MMA(1, 0, At, B0); PG8_MMA(1, 1, At, B1); PG8_BAR; PG8_SCHED;
;         }
;         if (wr == 0) PG8_BAR;
	s_nop 4
	s_add_i32 s62, s25, 0x20000
	s_add_u32 s62, s6, s62
	s_addc_u32 s63, s7, 0
	s_mov_b32 m0, s41
	v_lshl_add_u64 v[66:67], s[62:63], 0, v[148:149]
	global_load_lds_dwordx4 v[66:67], off
	v_lshl_add_u64 v[66:67], s[62:63], 0, v[146:147]
	s_mov_b32 m0, s42
	s_nop 0
	global_load_lds_dwordx4 v[66:67], off
	ds_read_b128 v[2:5], v162 offset:32768
	ds_read_b128 v[6:9], v162 offset:33792
	ds_read_b128 v[10:13], v162 offset:34816
	ds_read_b128 v[14:17], v162 offset:35840
	ds_read_b128 v[130:133], v162 offset:49152
	ds_read_b128 v[134:137], v162 offset:50176
	ds_read_b128 v[138:141], v162 offset:51200
	ds_read_b128 v[142:145], v162 offset:52224
	ds_read_b128 v[18:21], v161 offset:32768
	ds_read_b128 v[22:25], v161 offset:33792
	ds_read_b128 v[26:29], v161 offset:34816
	ds_read_b128 v[30:33], v161 offset:35840
	ds_read_b128 v[34:37], v161 offset:36864
	ds_read_b128 v[38:41], v161 offset:37888
	ds_read_b128 v[42:45], v161 offset:38912
	ds_read_b128 v[46:49], v161 offset:39936
	s_waitcnt vmcnt(8)
	s_waitcnt lgkmcnt(0)
	s_barrier
	s_setprio 1
	s_waitcnt lgkmcnt(0)
	v_mfma_f32_16x16x128_f8f6f4 v[126:129], v[2:9], v[18:25], v[126:129]
	v_mfma_f32_16x16x128_f8f6f4 v[122:125], v[10:17], v[18:25], v[122:125]
	v_mfma_f32_16x16x128_f8f6f4 v[118:121], v[2:9], v[26:33], v[118:121]
	v_mfma_f32_16x16x128_f8f6f4 v[114:117], v[10:17], v[26:33], v[114:117]
	v_mfma_f32_16x16x128_f8f6f4 v[102:105], v[2:9], v[34:41], v[102:105]
	v_mfma_f32_16x16x128_f8f6f4 v[98:101], v[10:17], v[34:41], v[98:101]
	v_mfma_f32_16x16x128_f8f6f4 v[86:89], v[2:9], v[42:49], v[204:207]
	v_mfma_f32_16x16x128_f8f6f4 v[78:81], v[10:17], v[42:49], v[208:211]
	s_setprio 0
	s_setprio 1
	v_mfma_f32_16x16x128_f8f6f4 v[110:113], v[130:137], v[18:25], v[110:113]
	v_mfma_f32_16x16x128_f8f6f4 v[106:109], v[138:145], v[18:25], v[106:109]
	v_mfma_f32_16x16x128_f8f6f4 v[94:97], v[130:137], v[26:33], v[172:175]
	v_mfma_f32_16x16x128_f8f6f4 v[90:93], v[138:145], v[26:33], v[176:179]
	v_mfma_f32_16x16x128_f8f6f4 v[82:85], v[130:137], v[34:41], v[180:183]
	v_mfma_f32_16x16x128_f8f6f4 v[74:77], v[138:145], v[34:41], v[184:187]
	v_mfma_f32_16x16x128_f8f6f4 v[70:73], v[130:137], v[42:49], v[188:191]
	v_mfma_f32_16x16x128_f8f6f4 v[66:69], v[138:145], v[42:49], v[192:195]
	s_setprio 0
	s_barrier
	s_add_u32 s62, s6, s61
	s_addc_u32 s63, s7, 0
	s_mov_b32 m0, s46
	v_lshl_add_u64 v[18:19], s[62:63], 0, v[148:149]
	s_add_i32 s24, s24, 0x20080
	global_load_lds_dwordx4 v[18:19], off
	v_lshl_add_u64 v[18:19], s[62:63], 0, v[146:147]
	s_add_u32 s62, s6, s24
	s_mov_b32 m0, s47
	s_addc_u32 s63, s7, 0
	s_addk_i32 s25, 0x80
	global_load_lds_dwordx4 v[18:19], off
	v_lshl_add_u64 v[18:19], s[62:63], 0, v[148:149]
	s_mov_b32 m0, s50
	s_add_u32 s24, s6, s25
	global_load_lds_dwordx4 v[18:19], off
	v_lshl_add_u64 v[18:19], s[62:63], 0, v[146:147]
	s_mov_b32 m0, s51
	s_addc_u32 s25, s7, 0
	global_load_lds_dwordx4 v[18:19], off
	v_lshl_add_u64 v[18:19], s[24:25], 0, v[148:149]
	s_mov_b32 m0, s48
	s_nop 0
	global_load_lds_dwordx4 v[18:19], off
	v_lshl_add_u64 v[18:19], s[24:25], 0, v[146:147]
	s_mov_b32 m0, s49
	s_nop 0
	global_load_lds_dwordx4 v[18:19], off
	ds_read_b128 v[150:153], v161 offset:49152
	ds_read_b128 v[154:157], v161 offset:50176
	ds_read_b128 v[164:167], v161 offset:51200
	ds_read_b128 v[168:171], v161 offset:52224
	ds_read_b128 v[172:175], v161 offset:53248
	ds_read_b128 v[176:179], v161 offset:54272
	ds_read_b128 v[180:183], v161 offset:55296
	ds_read_b128 v[184:187], v161 offset:56320
	s_waitcnt vmcnt(8)
	s_waitcnt lgkmcnt(0)
	s_barrier
	s_setprio 1
	s_waitcnt lgkmcnt(0)
	v_mfma_f32_16x16x128_f8f6f4 v[62:65], v[2:9], v[150:157], v[62:65]
	v_mfma_f32_16x16x128_f8f6f4 v[58:61], v[10:17], v[150:157], v[58:61]
	v_mfma_f32_16x16x128_f8f6f4 v[50:53], v[2:9], v[164:171], v[50:53]
	v_mfma_f32_16x16x128_f8f6f4 v[42:45], v[10:17], v[164:171], v[196:199]
	v_mfma_f32_16x16x128_f8f6f4 v[38:41], v[2:9], v[172:179], v[200:203]
	v_mfma_f32_16x16x128_f8f6f4 v[30:33], v[10:17], v[172:179], v[212:215]
	v_mfma_f32_16x16x128_f8f6f4 v[22:25], v[2:9], v[180:187], v[216:219]
	v_mfma_f32_16x16x128_f8f6f4 v[14:17], v[10:17], v[180:187], v[220:223]
	s_setprio 0
	s_setprio 1
	v_mfma_f32_16x16x128_f8f6f4 v[54:57], v[130:137], v[150:157], v[54:57]
	v_mfma_f32_16x16x128_f8f6f4 v[46:49], v[138:145], v[150:157], v[224:227]
	v_mfma_f32_16x16x128_f8f6f4 v[34:37], v[130:137], v[164:171], v[228:231]
	v_mfma_f32_16x16x128_f8f6f4 v[26:29], v[138:145], v[164:171], v[232:235]
	v_mfma_f32_16x16x128_f8f6f4 v[18:21], v[130:137], v[172:179], v[236:239]
	v_mfma_f32_16x16x128_f8f6f4 v[10:13], v[138:145], v[172:179], v[240:243]
	v_mfma_f32_16x16x128_f8f6f4 v[6:9], v[130:137], v[180:187], v[244:247]
	v_mfma_f32_16x16x128_f8f6f4 v[2:5], v[138:145], v[180:187], v[248:251]
	s_setprio 0
	s_barrier
	s_add_i32 s23, s23, 2
	s_addk_i32 s21, 0x100
	s_addk_i32 s22, 0x100
	s_cmp_gt_u32 s23, 5
	s_cbranch_scc0 .LBB0_910
	s_and_b64 vcc, exec, s[10:11]
	s_cbranch_vccz .LBB0_913
	s_barrier

; #define PG8_STAGE(bufoff, gbase, voff) do { _Pragma("unroll") for (int _i = 0; _i < 2; ++_i) \
;         __builtin_amdgcn_global_load_lds((const unsigned*)(wsb + (size_t)(gbase) + (voff)[_i]), (LAS unsigned*)(lds + (bufoff) + ldsw + _i * 8192), 16, 0, 0); } while (0)
; #define PG8_LDA(dst, b, h) do { _Pragma("unroll") for (int m = 0; m < 4; ++m) { if constexpr (FP8) dst##8[m] = PG8_LD8(pa, PG8_SA(b, h) + m * 2048); \
;         else { _Pragma("unroll") for (int k = 0; k < 2; ++k) dst[m][k] = *(const LAS bf16x8*)(pa + PG8_SA(b, h) + m * 2048 + k * 1024); } } } while (0)
; #define PG8_LDB(dst, b, h) do { _Pragma("unroll") for (int n = 0; n < 2; ++n) { if constexpr (FP8) dst##8[n] = PG8_LD8(pb, PG8_SA(b, h) + n * 2048); \
;         else { _Pragma("unroll") for (int k = 0; k < 2; ++k) dst[n][k] = *(const LAS bf16x8*)(pb + PG8_SA(b, h) + n * 2048 + k * 1024); } } } while (0)
; #define PG8_WAIT_V(n) asm volatile("s_waitcnt vmcnt(" #n ")" ::: "memory")
; #define PG8_WAIT_L(n) asm volatile("s_waitcnt lgkmcnt(" #n ")" ::: "memory")
; #define PG8_BAR __builtin_amdgcn_s_barrier()
; #define PG8_SCHED __builtin_amdgcn_sched_barrier(0)
; template <class Epi, class Sched, bool PERM, bool FP8 = false, bool GATHER = false>
; DI void gemm_phase(LAS unsigned char* lds, const unsigned char* wsb, const unsigned lda, const unsigned ldb, const int nt, const Sched& S, const Epi& E) {
;     ...
;             PG8_WAIT_V(8); PG8_WAIT_L(0); PG8_BAR; PG8_MMA(0, 0, At, B0); PG8_MMA(0, 1, At, B1); PG8_BAR; PG8_SCHED;
;             PG8_LDA(At, 0, 1); PG8_STAGE(PG8_SB(0, 0), b2, voffB); PG8_STAGE(PG8_SB(0, 1), b2 + hstepB, voffB); PG8_STAGEA(PG8_SA(0, 0), k2, 0, last);
;             PG8_WAIT_V(8); PG8_WAIT_L(0); PG8_BAR; PG8_MMA(1, 0, At, B0); PG8_MMA(1, 1, At, B1); PG8_BAR; PG8_SCHED;
;             PG8_LDB(B0, 1, 0); PG8_LDB(B1, 1, 1); PG8_SCHED; PG8_LDA(At, 1, 0); PG8_STAGEA(PG8_SA(0, 1), k2, 1, last);
;             PG8_WAIT_V(8); PG8_WAIT_L(0); PG8_BAR; PG8_MMA(0, 0, At, B0); PG8_MMA(0, 1, At, B1); PG8_BAR; PG8_SCHED;
.LBB0_1342:
	s_waitcnt vmcnt(8)
	s_add_i32 s85, s83, s50
	s_waitcnt lgkmcnt(0)
	s_and_b64 s[86:87], s[52:53], exec
	s_cselect_b32 s85, s14, s85
	v_mov_b32_e32 v205, v197
	s_add_i32 s86, s85, 0x80
	s_barrier
	s_setprio 1
	s_waitcnt lgkmcnt(0)
	v_mfma_f32_16x16x128_f8f6f4 v[190:193], v[18:25], v[58:65], v[190:193]
	v_mfma_f32_16x16x128_f8f6f4 v[186:189], v[26:33], v[58:65], v[186:189]
	v_mfma_f32_16x16x128_f8f6f4 v[174:177], v[18:25], v[50:57], v[174:177]
	v_mfma_f32_16x16x128_f8f6f4 v[166:169], v[26:33], v[50:57], v[166:169]
	v_mfma_f32_16x16x128_f8f6f4 v[158:161], v[18:25], v[42:49], v[158:161]
	v_mfma_f32_16x16x128_f8f6f4 v[150:153], v[26:33], v[42:49], v[150:153]
	v_mfma_f32_16x16x128_f8f6f4 v[142:145], v[18:25], v[34:41], v[142:145]
	v_mfma_f32_16x16x128_f8f6f4 v[134:137], v[26:33], v[34:41], v[134:137]
	s_setprio 0
	s_setprio 1
	v_mfma_f32_16x16x128_f8f6f4 v[182:185], v[2:9], v[58:65], v[182:185]
	v_mfma_f32_16x16x128_f8f6f4 v[178:181], v[10:17], v[58:65], v[178:181]
	v_mfma_f32_16x16x128_f8f6f4 v[170:173], v[2:9], v[50:57], v[170:173]
	v_mfma_f32_16x16x128_f8f6f4 v[162:165], v[10:17], v[50:57], v[162:165]
	v_mfma_f32_16x16x128_f8f6f4 v[154:157], v[2:9], v[42:49], v[154:157]
	v_mfma_f32_16x16x128_f8f6f4 v[146:149], v[10:17], v[42:49], v[146:149]
	v_mfma_f32_16x16x128_f8f6f4 v[138:141], v[2:9], v[34:41], v[138:141]
	v_mfma_f32_16x16x128_f8f6f4 v[130:133], v[10:17], v[34:41], v[130:133]
	s_setprio 0
	s_barrier
	s_add_u32 s88, s10, s85
	s_addc_u32 s89, s11, 0
	s_mov_b32 m0, s41
	v_lshl_add_u64 v[214:215], s[88:89], 0, v[198:199]
	s_add_i32 s87, s85, 0x20000
	global_load_lds_dwordx4 v[214:215], off
	v_lshl_add_u64 v[214:215], s[88:89], 0, v[200:201]
	s_add_u32 s88, s10, s87
	s_addc_u32 s89, s11, 0
	s_add_u32 s50, s50, 0x100
	s_addc_u32 s51, s51, 0
	s_mov_b32 m0, s46
	s_and_b64 s[52:53], s[52:53], exec
	global_load_lds_dwordx4 v[214:215], off
	v_lshl_add_u64 v[214:215], s[88:89], 0, v[198:199]
	s_mov_b32 m0, s47
	s_cselect_b32 s87, 0, s50
	global_load_lds_dwordx4 v[214:215], off
	v_lshl_add_u64 v[214:215], s[88:89], 0, v[200:201]
	s_mov_b32 m0, s54
	s_add_u32 s52, s12, s87
	global_load_lds_dwordx4 v[214:215], off
	s_addc_u32 s53, s13, 0
	s_mov_b32 m0, s39
	s_nop 0
	global_load_lds_dwordx4 v212, s[52:53]
	s_mov_b32 m0, s55
	s_nop 0
	global_load_lds_dwordx4 v202, s[52:53]
	ds_read_b128 v[34:37], v209 offset:16384
	ds_read_b128 v[38:41], v209 offset:17408
	ds_read_b128 v[42:45], v209 offset:18432
	ds_read_b128 v[46:49], v209 offset:19456
	ds_read_b128 v[50:53], v209 offset:20480
	ds_read_b128 v[54:57], v209 offset:21504
	ds_read_b128 v[58:61], v209 offset:22528
	ds_read_b128 v[62:65], v209 offset:23552
	s_waitcnt vmcnt(8)
	s_waitcnt lgkmcnt(0)
	s_barrier
	s_setprio 1
	s_waitcnt lgkmcnt(0)
	v_mfma_f32_16x16x128_f8f6f4 v[126:129], v[18:25], v[34:41], v[126:129]
	v_mfma_f32_16x16x128_f8f6f4 v[118:121], v[26:33], v[34:41], v[118:121]
	v_mfma_f32_16x16x128_f8f6f4 v[110:113], v[18:25], v[42:49], v[110:113]
	v_mfma_f32_16x16x128_f8f6f4 v[102:105], v[26:33], v[42:49], v[102:105]
	v_mfma_f32_16x16x128_f8f6f4 v[94:97], v[18:25], v[50:57], v[94:97]
	v_mfma_f32_16x16x128_f8f6f4 v[86:89], v[26:33], v[50:57], v[86:89]
	v_mfma_f32_16x16x128_f8f6f4 v[78:81], v[18:25], v[58:65], v[78:81]
	v_mfma_f32_16x16x128_f8f6f4 v[70:73], v[26:33], v[58:65], v[70:73]
	s_setprio 0
	s_setprio 1
	v_mfma_f32_16x16x128_f8f6f4 v[122:125], v[2:9], v[34:41], v[122:125]
	v_mfma_f32_16x16x128_f8f6f4 v[114:117], v[10:17], v[34:41], v[114:117]
	v_mfma_f32_16x16x128_f8f6f4 v[106:109], v[2:9], v[42:49], v[106:109]
	v_mfma_f32_16x16x128_f8f6f4 v[98:101], v[10:17], v[42:49], v[98:101]
	v_mfma_f32_16x16x128_f8f6f4 v[90:93], v[2:9], v[50:57], v[90:93]
	v_mfma_f32_16x16x128_f8f6f4 v[82:85], v[10:17], v[50:57], v[82:85]
	v_mfma_f32_16x16x128_f8f6f4 v[74:77], v[2:9], v[58:65], v[74:77]
	v_mfma_f32_16x16x128_f8f6f4 v[66:69], v[10:17], v[58:65], v[66:69]
	s_setprio 0
	s_barrier
	s_mov_b32 m0, s56
	v_lshl_add_u64 v[214:215], s[52:53], 0, v[196:197]
	global_load_lds_dwordx4 v[214:215], off
	v_lshl_add_u64 v[214:215], s[52:53], 0, v[204:205]
	s_mov_b32 m0, s57
	s_nop 0
	global_load_lds_dwordx4 v[214:215], off
	ds_read_b128 v[2:5], v210 offset:32768
	ds_read_b128 v[6:9], v210 offset:33792
	ds_read_b128 v[10:13], v210 offset:34816
	ds_read_b128 v[14:17], v210 offset:35840
	ds_read_b128 v[18:21], v210 offset:49152
	ds_read_b128 v[22:25], v210 offset:50176
	ds_read_b128 v[26:29], v210 offset:51200
	ds_read_b128 v[30:33], v210 offset:52224
	ds_read_b128 v[34:37], v209 offset:32768
	ds_read_b128 v[38:41], v209 offset:33792
	ds_read_b128 v[42:45], v209 offset:34816
	ds_read_b128 v[46:49], v209 offset:35840
	ds_read_b128 v[50:53], v209 offset:36864
	ds_read_b128 v[54:57], v209 offset:37888
	ds_read_b128 v[58:61], v209 offset:38912
	ds_read_b128 v[62:65], v209 offset:39936
	s_waitcnt vmcnt(8)
	s_waitcnt lgkmcnt(0)
	s_barrier
	s_setprio 1
	s_waitcnt lgkmcnt(0)
	v_mfma_f32_16x16x128_f8f6f4 v[190:193], v[2:9], v[34:41], v[190:193]
	v_mfma_f32_16x16x128_f8f6f4 v[186:189], v[10:17], v[34:41], v[186:189]
	v_mfma_f32_16x16x128_f8f6f4 v[174:177], v[2:9], v[42:49], v[174:177]
	v_mfma_f32_16x16x128_f8f6f4 v[166:169], v[10:17], v[42:49], v[166:169]
	v_mfma_f32_16x16x128_f8f6f4 v[158:161], v[2:9], v[50:57], v[158:161]
	v_mfma_f32_16x16x128_f8f6f4 v[150:153], v[10:17], v[50:57], v[150:153]
	v_mfma_f32_16x16x128_f8f6f4 v[142:145], v[2:9], v[58:65], v[142:145]
	v_mfma_f32_16x16x128_f8f6f4 v[134:137], v[10:17], v[58:65], v[134:137]
	s_setprio 0
	s_setprio 1
	v_mfma_f32_16x16x128_f8f6f4 v[182:185], v[18:25], v[34:41], v[182:185]
	v_mfma_f32_16x16x128_f8f6f4 v[178:181], v[26:33], v[34:41], v[178:181]
	v_mfma_f32_16x16x128_f8f6f4 v[170:173], v[18:25], v[42:49], v[170:173]
	v_mfma_f32_16x16x128_f8f6f4 v[162:165], v[26:33], v[42:49], v[162:165]
	v_mfma_f32_16x16x128_f8f6f4 v[154:157], v[18:25], v[50:57], v[154:157]
	v_mfma_f32_16x16x128_f8f6f4 v[146:149], v[26:33], v[50:57], v[146:149]
	v_mfma_f32_16x16x128_f8f6f4 v[138:141], v[18:25], v[58:65], v[138:141]
	v_mfma_f32_16x16x128_f8f6f4 v[130:133], v[26:33], v[58:65], v[130:133]
	s_setprio 0
	s_barrier
; #define PG8_STAGE(bufoff, gbase, voff) do { _Pragma("unroll") for (int _i = 0; _i < 2; ++_i) \
;         __builtin_amdgcn_global_load_lds((const unsigned*)(wsb + (size_t)(gbase) + (voff)[_i]), (LAS unsigned*)(lds + (bufoff) + ldsw + _i * 8192), 16, 0, 0); } while (0)
; #define PG8_LDA(dst, b, h) do { _Pragma("unroll") for (int m = 0; m < 4; ++m) { if constexpr (FP8) dst##8[m] = PG8_LD8(pa, PG8_SA(b, h) + m * 2048); \
;         else { _Pragma("unroll") for (int k = 0; k < 2; ++k) dst[m][k] = *(const LAS bf16x8*)(pa + PG8_SA(b, h) + m * 2048 + k * 1024); } } } while (0)
; #define PG8_WAIT_V(n) asm volatile("s_waitcnt vmcnt(" #n ")" ::: "memory")
; template <class Epi, class Sched, bool PERM, bool FP8 = false, bool GATHER = false>
; DI void gemm_phase(LAS unsigned char* lds, const unsigned char* wsb, const unsigned lda, const unsigned ldb, const int nt, const Sched& S, const Epi& E) {
;     ...
;             PG8_LDB(B0, 0, 0); PG8_LDB(B1, 0, 1); PG8_SCHED; PG8_LDA(At, 0, 0); PG8_STAGEA(PG8_SA(1, 1), t + 1, 1, false);
;             if constexpr (GATHER) { if (last) {
;                 int tz = tid; asm volatile("" : "+v"(tz));
; #pragma unroll
;                 for (int i = 0; i < 2; ++i) { int R, C; stage_rc(tz * 16 + i * 8192, R, C);
; #pragma unroll
;                     for (int h = 0; h < 2; ++h) { const unsigned tk = (unsigned)tokt[h * HALF + R]; offC[h][i] = (tk < (unsigned)NTOK ? tk : (unsigned)(NTOK - 1)) * lda + (unsigned)C * 2u; } } } }
;             PG8_WAIT_V(8); PG8_WAIT_L(0); PG8_BAR; PG8_MMA(0, 0, At, B0); PG8_MMA(0, 1, At, B1); PG8_BAR; PG8_SCHED;
;             PG8_LDA(At, 0, 1); PG8_STAGE(PG8_SB(0, 0), b2, voffB); PG8_STAGE(PG8_SB(0, 1), b2 + hstepB, voffB); PG8_STAGEA(PG8_SA(0, 0), k2, 0, last);
;             PG8_WAIT_V(8); PG8_WAIT_L(0); PG8_BAR; PG8_MMA(1, 0, At, B0); PG8_MMA(1, 1, At, B1); PG8_BAR; PG8_SCHED;
;             PG8_LDB(B0, 1, 0); PG8_LDB(B1, 1, 1); PG8_SCHED; PG8_LDA(At, 1, 0); PG8_STAGEA(PG8_SA(0, 1), k2, 1, last);
;             PG8_WAIT_V(8); PG8_WAIT_L(0); PG8_BAR; PG8_MMA(0, 0, At, B0); PG8_MMA(0, 1, At, B1); PG8_BAR; PG8_SCHED;
;             PG8_LDA(At, 1, 1); PG8_STAGE(PG8_SB(1, 0), b3, voffB); PG8_STAGE(PG8_SB(1, 1), b3 + hstepB, voffB); PG8_STAGEA(PG8_SA(1, 0), k3, 0, last);
;             PG8_WAIT_V(8); PG8_WAIT_L(0); PG8_BAR; PG8_MMA(1, 0, At, B0); PG8_MMA(1, 1, At, B1); PG8_BAR; PG8_SCHED;
	s_add_u32 s52, s10, s86
	s_addc_u32 s53, s11, 0
	s_mov_b32 m0, s61
	v_lshl_add_u64 v[214:215], s[52:53], 0, v[198:199]
	s_add_i32 s85, s85, 0x20080
	global_load_lds_dwordx4 v[214:215], off
	v_lshl_add_u64 v[214:215], s[52:53], 0, v[200:201]
	s_add_u32 s52, s10, s85
	s_mov_b32 m0, s63
	s_addc_u32 s53, s11, 0
	global_load_lds_dwordx4 v[214:215], off
	v_lshl_add_u64 v[214:215], s[52:53], 0, v[198:199]
	s_mov_b32 m0, s66
	s_nop 0
	global_load_lds_dwordx4 v[214:215], off
	v_lshl_add_u64 v[214:215], s[52:53], 0, v[200:201]
	s_add_u32 s52, s10, s87
	s_addc_u32 s53, s11, 0
	s_mov_b32 m0, s67
	s_add_u32 s52, s52, 0x5b9d4080
	global_load_lds_dwordx4 v[214:215], off
	s_addc_u32 s53, s53, 0
	s_mov_b32 m0, s64
	s_nop 0
	global_load_lds_dwordx4 v212, s[52:53]
	s_mov_b32 m0, s65
	s_nop 0
	global_load_lds_dwordx4 v202, s[52:53]
	ds_read_b128 v[34:37], v209 offset:49152
	ds_read_b128 v[38:41], v209 offset:50176
	ds_read_b128 v[42:45], v209 offset:51200
	ds_read_b128 v[46:49], v209 offset:52224
	ds_read_b128 v[50:53], v209 offset:53248
	ds_read_b128 v[54:57], v209 offset:54272
	ds_read_b128 v[58:61], v209 offset:55296
	ds_read_b128 v[62:65], v209 offset:56320
	s_waitcnt vmcnt(8)
	s_waitcnt lgkmcnt(0)
	s_barrier
	s_setprio 1
	s_waitcnt lgkmcnt(0)
	v_mfma_f32_16x16x128_f8f6f4 v[126:129], v[2:9], v[34:41], v[126:129]
	v_mfma_f32_16x16x128_f8f6f4 v[118:121], v[10:17], v[34:41], v[118:121]
	v_mfma_f32_16x16x128_f8f6f4 v[110:113], v[2:9], v[42:49], v[110:113]
	v_mfma_f32_16x16x128_f8f6f4 v[102:105], v[10:17], v[42:49], v[102:105]
	v_mfma_f32_16x16x128_f8f6f4 v[94:97], v[2:9], v[50:57], v[94:97]
	v_mfma_f32_16x16x128_f8f6f4 v[86:89], v[10:17], v[50:57], v[86:89]
	v_mfma_f32_16x16x128_f8f6f4 v[78:81], v[2:9], v[58:65], v[78:81]
	v_mfma_f32_16x16x128_f8f6f4 v[70:73], v[10:17], v[58:65], v[70:73]
	s_setprio 0
	s_setprio 1
	v_mfma_f32_16x16x128_f8f6f4 v[122:125], v[18:25], v[34:41], v[122:125]
	v_mfma_f32_16x16x128_f8f6f4 v[114:117], v[26:33], v[34:41], v[114:117]
	v_mfma_f32_16x16x128_f8f6f4 v[106:109], v[18:25], v[42:49], v[106:109]
	v_mfma_f32_16x16x128_f8f6f4 v[98:101], v[26:33], v[42:49], v[98:101]
	v_mfma_f32_16x16x128_f8f6f4 v[90:93], v[18:25], v[50:57], v[90:93]
	v_mfma_f32_16x16x128_f8f6f4 v[82:85], v[26:33], v[50:57], v[82:85]
	v_mfma_f32_16x16x128_f8f6f4 v[74:77], v[18:25], v[58:65], v[74:77]
	v_mfma_f32_16x16x128_f8f6f4 v[66:69], v[26:33], v[58:65], v[66:69]
	s_setprio 0
	s_barrier
	s_add_i32 s84, s84, 2
	s_cmp_gt_u32 s84, 5
	s_cbranch_scc1 .LBB0_1345
.LBB0_1343:
	s_cmp_eq_u32 s84, 4
	s_cselect_b64 s[52:53], -1, 0
	s_add_i32 m0, s39, 0xc000
	s_add_u32 s86, s18, s50
	s_addc_u32 s87, s19, s51
	s_add_i32 s85, s39, 0xe000
	s_cmp_lg_u32 s84, 4
	global_load_lds_dwordx4 v196, s[86:87]
	s_mov_b32 m0, s85
	s_nop 0
	global_load_lds_dwordx4 v204, s[86:87]
	ds_read_b128 v[18:21], v210
	ds_read_b128 v[22:25], v210 offset:1024
	ds_read_b128 v[26:29], v210 offset:2048
	ds_read_b128 v[30:33], v210 offset:3072
	ds_read_b128 v[2:5], v210 offset:16384
	ds_read_b128 v[6:9], v210 offset:17408
	ds_read_b128 v[10:13], v210 offset:18432
	ds_read_b128 v[14:17], v210 offset:19456
	ds_read_b128 v[58:61], v209
	ds_read_b128 v[62:65], v209 offset:1024
	ds_read_b128 v[50:53], v209 offset:2048
	ds_read_b128 v[54:57], v209 offset:3072
	ds_read_b128 v[42:45], v209 offset:4096
	ds_read_b128 v[46:49], v209 offset:5120
	ds_read_b128 v[34:37], v209 offset:6144
	ds_read_b128 v[38:41], v209 offset:7168
	s_cbranch_scc1 .LBB0_1342
	v_mov_b32_e32 v196, v194
	s_add_i32 s85, 0, 0x20c00
	v_ashrrev_i32_e32 v204, 31, v196
	v_lshrrev_b32_e32 v204, 26, v204
	v_lshlrev_b32_e32 v202, 4, v196
	v_add_u32_e32 v204, v196, v204
	v_bfe_i32 v196, v196, 27, 1
	v_lshrrev_b32_e32 v196, 22, v196
	v_add_u32_e32 v196, v202, v196
	v_and_b32_e32 v196, 0xfffffc00, v196
	v_sub_u32_e32 v196, v202, v196
	v_lshrrev_b32_e32 v205, 4, v196
	v_bitop3_b32 v196, v205, v196, 32 bitop3:0x6c
	v_ashrrev_i32_e32 v205, 31, v196
	v_lshrrev_b32_e32 v205, 26, v205
	v_ashrrev_i32_e32 v204, 6, v204
	v_add_u32_e32 v205, v196, v205
	v_ashrrev_i32_e32 v212, 6, v205
	v_lshlrev_b32_e32 v204, 5, v204
	v_and_b32_e32 v213, 32, v204
	v_and_b32_e32 v214, 0xc0, v205
	v_lshlrev_b32_e32 v205, 2, v212
	v_and_b32_e32 v204, 0xffffffc0, v204
	v_add3_u32 v204, s85, v205, v204
	ds_read2st64_b32 v[204:205], v204 offset1:2
	v_sub_u32_e32 v196, v196, v214
	v_ashrrev_i16_sdwa v196, v211, sext(v196) dst_sel:DWORD dst_unused:UNUSED_PAD src0_sel:DWORD src1_sel:BYTE_0
	v_bfe_i32 v196, v196, 0, 16
	v_add_lshl_u32 v196, v213, v196, 1
	s_waitcnt lgkmcnt(0)
	v_min_u32_e32 v204, 0x87ff, v204
	v_lshl_add_u32 v212, v204, 10, v196
	v_min_u32_e32 v204, 0x87ff, v205
	v_add_u32_e32 v202, 0x2000, v202
	v_lshl_add_u32 v196, v204, 10, v196
	v_ashrrev_i32_e32 v204, 31, v202
	v_lshrrev_b32_e32 v204, 22, v204
	v_add_u32_e32 v204, v202, v204
	v_ashrrev_i32_e32 v204, 10, v204
	v_mul_i32_i24_e32 v205, 0x400, v204
	v_sub_u32_e32 v202, v202, v205
	v_lshrrev_b32_e32 v205, 4, v202
	v_bitop3_b32 v202, v205, v202, 32 bitop3:0x6c
	v_ashrrev_i32_e32 v205, 31, v202
	v_lshrrev_b32_e32 v205, 26, v205
	v_add_u32_e32 v205, v202, v205
	v_ashrrev_i32_e32 v213, 6, v205
	v_lshlrev_b32_e32 v204, 5, v204
	v_and_b32_e32 v214, 32, v204
	v_and_b32_e32 v215, 0xc0, v205
	v_lshlrev_b32_e32 v205, 2, v213
	v_and_b32_e32 v204, 0xffffffc0, v204
	v_add3_u32 v204, s85, v205, v204
	ds_read2st64_b32 v[204:205], v204 offset1:2
	v_sub_u32_e32 v202, v202, v215
	v_ashrrev_i16_sdwa v202, v211, sext(v202) dst_sel:DWORD dst_unused:UNUSED_PAD src0_sel:DWORD src1_sel:BYTE_0
	v_bfe_i32 v202, v202, 0, 16
	v_add_lshl_u32 v213, v214, v202, 1
	s_waitcnt lgkmcnt(0)
	v_min_u32_e32 v202, 0x87ff, v204
	v_min_u32_e32 v204, 0x87ff, v205
	v_lshl_add_u32 v202, v202, 10, v213
	v_lshl_add_u32 v204, v204, 10, v213
	s_branch .LBB0_1342

; #define PG8_STAGE(bufoff, gbase, voff) do { _Pragma("unroll") for (int _i = 0; _i < 2; ++_i) \
;         __builtin_amdgcn_global_load_lds((const unsigned*)(wsb + (size_t)(gbase) + (voff)[_i]), (LAS unsigned*)(lds + (bufoff) + ldsw + _i * 8192), 16, 0, 0); } while (0)
; #define PG8_LDA(dst, b, h) do { _Pragma("unroll") for (int m = 0; m < 4; ++m) { if constexpr (FP8) dst##8[m] = PG8_LD8(pa, PG8_SA(b, h) + m * 2048); \
;         else { _Pragma("unroll") for (int k = 0; k < 2; ++k) dst[m][k] = *(const LAS bf16x8*)(pa + PG8_SA(b, h) + m * 2048 + k * 1024); } } } while (0)
; #define PG8_LDB(dst, b, h) do { _Pragma("unroll") for (int n = 0; n < 2; ++n) { if constexpr (FP8) dst##8[n] = PG8_LD8(pb, PG8_SA(b, h) + n * 2048); \
;         else { _Pragma("unroll") for (int k = 0; k < 2; ++k) dst[n][k] = *(const LAS bf16x8*)(pb + PG8_SA(b, h) + n * 2048 + k * 1024); } } } while (0)
; #define PG8_WAIT_V(n) asm volatile("s_waitcnt vmcnt(" #n ")" ::: "memory")
; #define PG8_WAIT_L(n) asm volatile("s_waitcnt lgkmcnt(" #n ")" ::: "memory")
; #define PG8_BAR __builtin_amdgcn_s_barrier()
; #define PG8_SCHED __builtin_amdgcn_sched_barrier(0)
; template <class Epi, class Sched, bool PERM, bool FP8 = false, bool GATHER = false>
; DI void gemm_phase(LAS unsigned char* lds, const unsigned char* wsb, const unsigned lda, const unsigned ldb, const int nt, const Sched& S, const Epi& E) {
;     ...
;             PG8_LDB(B0, 0, 0); PG8_LDB(B1, 0, 1); PG8_SCHED; PG8_LDA(At, 0, 0); PG8_STAGEA(PG8_SA(1, 1), t + 1, 1, false);
;             if constexpr (GATHER) { if (last) {
;                 int tz = tid; asm volatile("" : "+v"(tz));
; #pragma unroll
;                 for (int i = 0; i < 2; ++i) { int R, C; stage_rc(tz * 16 + i * 8192, R, C);
; #pragma unroll
;                     for (int h = 0; h < 2; ++h) { const unsigned tk = (unsigned)tokt[h * HALF + R]; offC[h][i] = (tk < (unsigned)NTOK ? tk : (unsigned)(NTOK - 1)) * lda + (unsigned)C * 2u; } } } }
;             PG8_WAIT_V(8); PG8_WAIT_L(0); PG8_BAR; PG8_MMA(0, 0, At, B0); PG8_MMA(0, 1, At, B1); PG8_BAR; PG8_SCHED;
;             PG8_LDA(At, 0, 1); PG8_STAGE(PG8_SB(0, 0), b2, voffB); PG8_STAGE(PG8_SB(0, 1), b2 + hstepB, voffB); PG8_STAGEA(PG8_SA(0, 0), k2, 0, last);
;             PG8_WAIT_V(8); PG8_WAIT_L(0); PG8_BAR; PG8_MMA(1, 0, At, B0); PG8_MMA(1, 1, At, B1); PG8_BAR; PG8_SCHED;
.LBB0_1450:
	ds_read_b128 v[130:133], v154
	ds_read_b128 v[134:137], v154 offset:1024
	ds_read_b128 v[138:141], v154 offset:2048
	ds_read_b128 v[142:145], v154 offset:3072
	ds_read_b128 v[158:161], v154 offset:16384
	ds_read_b128 v[162:165], v154 offset:17408
	ds_read_b128 v[166:169], v154 offset:18432
	ds_read_b128 v[170:173], v154 offset:19456
	s_add_i32 s74, s71, 0xfffe0080
	s_add_i32 s75, s74, s68
	s_cmp_eq_u32 s70, 4
	s_cselect_b64 s[24:25], -1, 0
	s_and_b64 s[72:73], s[24:25], exec
	s_cselect_b32 s72, s69, s75
	s_cselect_b32 s76, 0, s74
	s_add_i32 s73, s72, 0x80
	s_add_i32 s74, s67, s71
	s_add_u32 s74, s10, s74
	s_addc_u32 s75, s11, 0
	v_lshl_add_u64 v[150:151], s[74:75], 0, v[146:147]
	s_add_i32 m0, s5, 0xc000
	ds_read_b128 v[174:177], v153
	ds_read_b128 v[178:181], v153 offset:1024
	ds_read_b128 v[182:185], v153 offset:2048
	ds_read_b128 v[186:189], v153 offset:3072
	ds_read_b128 v[190:193], v153 offset:4096
	ds_read_b128 v[194:197], v153 offset:5120
	ds_read_b128 v[198:201], v153 offset:6144
	ds_read_b128 v[202:205], v153 offset:7168
	global_load_lds_dwordx4 v[150:151], off
	v_lshl_add_u64 v[150:151], s[74:75], 0, v[148:149]
	s_add_i32 m0, s5, 0xe000
	s_nop 0
	global_load_lds_dwordx4 v[150:151], off
	s_waitcnt vmcnt(8)
	s_waitcnt lgkmcnt(0)
	s_barrier
	s_setprio 1
	s_waitcnt lgkmcnt(0)
	v_mfma_f32_16x16x128_f8f6f4 v[126:129], v[130:137], v[174:181], v[126:129]
	v_mfma_f32_16x16x128_f8f6f4 v[122:125], v[138:145], v[174:181], v[122:125]
	v_mfma_f32_16x16x128_f8f6f4 v[118:121], v[130:137], v[182:189], v[118:121]
	v_mfma_f32_16x16x128_f8f6f4 v[114:117], v[138:145], v[182:189], v[114:117]
	v_mfma_f32_16x16x128_f8f6f4 v[206:209], v[130:137], v[190:197], v[94:97]
	v_mfma_f32_16x16x128_f8f6f4 v[210:213], v[138:145], v[190:197], v[90:93]
	v_mfma_f32_16x16x128_f8f6f4 v[214:217], v[130:137], v[198:205], v[82:85]
	v_mfma_f32_16x16x128_f8f6f4 v[218:221], v[138:145], v[198:205], v[74:77]
	s_setprio 0
	s_setprio 1
	v_mfma_f32_16x16x128_f8f6f4 v[110:113], v[158:165], v[174:181], v[110:113]
	v_mfma_f32_16x16x128_f8f6f4 v[106:109], v[166:173], v[174:181], v[106:109]
	v_mfma_f32_16x16x128_f8f6f4 v[102:105], v[158:165], v[182:189], v[102:105]
	v_mfma_f32_16x16x128_f8f6f4 v[98:101], v[166:173], v[182:189], v[98:101]
	v_mfma_f32_16x16x128_f8f6f4 v[174:177], v[158:165], v[190:197], v[86:89]
	v_mfma_f32_16x16x128_f8f6f4 v[178:181], v[166:173], v[190:197], v[78:81]
	v_mfma_f32_16x16x128_f8f6f4 v[182:185], v[158:165], v[198:205], v[70:73]
	v_mfma_f32_16x16x128_f8f6f4 v[186:189], v[166:173], v[198:205], v[66:69]
	s_setprio 0
	s_barrier
	s_add_u32 s74, s10, s72
	s_addc_u32 s75, s11, 0
	s_mov_b32 m0, s19
	v_lshl_add_u64 v[150:151], s[74:75], 0, v[146:147]
	s_nop 0
	global_load_lds_dwordx4 v[150:151], off
	v_lshl_add_u64 v[150:151], s[74:75], 0, v[148:149]
	s_add_i32 s74, s72, 0x20000
	s_add_u32 s74, s10, s74
	s_addc_u32 s75, s11, 0
	s_and_b64 s[24:25], s[20:21], s[24:25]
	s_and_b64 s[24:25], s[24:25], exec
	s_mov_b32 m0, s28
	s_cselect_b32 s24, s60, s67
	global_load_lds_dwordx4 v[150:151], off
	v_lshl_add_u64 v[150:151], s[74:75], 0, v[146:147]
	s_mov_b32 m0, s29
	s_add_i32 s24, s76, s24
	global_load_lds_dwordx4 v[150:151], off
	v_lshl_add_u64 v[150:151], s[74:75], 0, v[148:149]
	s_add_u32 s74, s10, s24
	s_mov_b32 m0, s36
	s_addc_u32 s75, s11, 0
	global_load_lds_dwordx4 v[150:151], off
	v_lshl_add_u64 v[150:151], s[74:75], 0, v[146:147]
	s_mov_b32 m0, s5
	s_nop 0
	global_load_lds_dwordx4 v[150:151], off
	v_lshl_add_u64 v[150:151], s[74:75], 0, v[148:149]
	s_mov_b32 m0, s37
	s_nop 0
	global_load_lds_dwordx4 v[150:151], off
	ds_read_b128 v[66:69], v153 offset:16384
	ds_read_b128 v[70:73], v153 offset:17408
	ds_read_b128 v[74:77], v153 offset:18432
	ds_read_b128 v[78:81], v153 offset:19456
	ds_read_b128 v[82:85], v153 offset:20480
	ds_read_b128 v[86:89], v153 offset:21504
	ds_read_b128 v[90:93], v153 offset:22528
	ds_read_b128 v[94:97], v153 offset:23552
	s_waitcnt vmcnt(8)
	s_waitcnt lgkmcnt(0)
	s_barrier
	s_setprio 1
	s_waitcnt lgkmcnt(0)
	v_mfma_f32_16x16x128_f8f6f4 v[62:65], v[130:137], v[66:73], v[62:65]
	v_mfma_f32_16x16x128_f8f6f4 v[58:61], v[138:145], v[66:73], v[58:61]
	v_mfma_f32_16x16x128_f8f6f4 v[50:53], v[130:137], v[74:81], v[50:53]
	v_mfma_f32_16x16x128_f8f6f4 v[190:193], v[138:145], v[74:81], v[42:45]
	v_mfma_f32_16x16x128_f8f6f4 v[194:197], v[130:137], v[82:89], v[34:37]
	v_mfma_f32_16x16x128_f8f6f4 v[198:201], v[138:145], v[82:89], v[26:29]
	v_mfma_f32_16x16x128_f8f6f4 v[202:205], v[130:137], v[90:97], v[18:21]
	v_mfma_f32_16x16x128_f8f6f4 v[222:225], v[138:145], v[90:97], v[10:13]
	s_setprio 0
	s_setprio 1
	v_mfma_f32_16x16x128_f8f6f4 v[54:57], v[158:165], v[66:73], v[54:57]
	v_mfma_f32_16x16x128_f8f6f4 v[226:229], v[166:173], v[66:73], v[46:49]
	v_mfma_f32_16x16x128_f8f6f4 v[230:233], v[158:165], v[74:81], v[38:41]
	v_mfma_f32_16x16x128_f8f6f4 v[234:237], v[166:173], v[74:81], v[30:33]
	v_mfma_f32_16x16x128_f8f6f4 v[238:241], v[158:165], v[82:89], v[22:25]
	v_mfma_f32_16x16x128_f8f6f4 v[242:245], v[166:173], v[82:89], v[14:17]
	v_mfma_f32_16x16x128_f8f6f4 v[246:249], v[158:165], v[90:97], v[6:9]
	v_mfma_f32_16x16x128_f8f6f4 v[250:253], v[166:173], v[90:97], v[2:5]
	s_setprio 0
	s_barrier
; #define PG8_STAGE(bufoff, gbase, voff) do { _Pragma("unroll") for (int _i = 0; _i < 2; ++_i) \
;         __builtin_amdgcn_global_load_lds((const unsigned*)(wsb + (size_t)(gbase) + (voff)[_i]), (LAS unsigned*)(lds + (bufoff) + ldsw + _i * 8192), 16, 0, 0); } while (0)
; #define PG8_LDA(dst, b, h) do { _Pragma("unroll") for (int m = 0; m < 4; ++m) { if constexpr (FP8) dst##8[m] = PG8_LD8(pa, PG8_SA(b, h) + m * 2048); \
;         else { _Pragma("unroll") for (int k = 0; k < 2; ++k) dst[m][k] = *(const LAS bf16x8*)(pa + PG8_SA(b, h) + m * 2048 + k * 1024); } } } while (0)
; #define PG8_LDB(dst, b, h) do { _Pragma("unroll") for (int n = 0; n < 2; ++n) { if constexpr (FP8) dst##8[n] = PG8_LD8(pb, PG8_SA(b, h) + n * 2048); \
;         else { _Pragma("unroll") for (int k = 0; k < 2; ++k) dst[n][k] = *(const LAS bf16x8*)(pb + PG8_SA(b, h) + n * 2048 + k * 1024); } } } while (0)
; #define PG8_WAIT_V(n) asm volatile("s_waitcnt vmcnt(" #n ")" ::: "memory")
; #define PG8_WAIT_L(n) asm volatile("s_waitcnt lgkmcnt(" #n ")" ::: "memory")
; #define PG8_BAR __builtin_amdgcn_s_barrier()
; #define PG8_SCHED __builtin_amdgcn_sched_barrier(0)
; template <class Epi, class Sched, bool PERM, bool FP8 = false, bool GATHER = false>
; DI void gemm_phase(LAS unsigned char* lds, const unsigned char* wsb, const unsigned lda, const unsigned ldb, const int nt, const Sched& S, const Epi& E) {
;     ...
;             PG8_LDB(B0, 1, 0); PG8_LDB(B1, 1, 1); PG8_SCHED; PG8_LDA(At, 1, 0); PG8_STAGEA(PG8_SA(0, 1), k2, 1, last);
;             PG8_WAIT_V(8); PG8_WAIT_L(0); PG8_BAR; PG8_MMA(0, 0, At, B0); PG8_MMA(0, 1, At, B1); PG8_BAR; PG8_SCHED;
;             PG8_LDA(At, 1, 1); PG8_STAGE(PG8_SB(1, 0), b3, voffB); PG8_STAGE(PG8_SB(1, 1), b3 + hstepB, voffB); PG8_STAGEA(PG8_SA(1, 0), k3, 0, last);
;             PG8_WAIT_V(8); PG8_WAIT_L(0); PG8_BAR; PG8_MMA(1, 0, At, B0); PG8_MMA(1, 1, At, B1); PG8_BAR; PG8_SCHED;
;         }
;         if (wr == 0) PG8_BAR;
	s_nop 4
	s_add_i32 s25, s24, 0x20000
	s_add_u32 s74, s10, s25
	s_addc_u32 s75, s11, 0
	s_mov_b32 m0, s38
	v_lshl_add_u64 v[66:67], s[74:75], 0, v[146:147]
	global_load_lds_dwordx4 v[66:67], off
	v_lshl_add_u64 v[66:67], s[74:75], 0, v[148:149]
	s_mov_b32 m0, s39
	s_nop 0
	global_load_lds_dwordx4 v[66:67], off
	ds_read_b128 v[2:5], v154 offset:32768
	ds_read_b128 v[6:9], v154 offset:33792
	ds_read_b128 v[10:13], v154 offset:34816
	ds_read_b128 v[14:17], v154 offset:35840
	ds_read_b128 v[130:133], v154 offset:49152
	ds_read_b128 v[134:137], v154 offset:50176
	ds_read_b128 v[138:141], v154 offset:51200
	ds_read_b128 v[142:145], v154 offset:52224
	ds_read_b128 v[18:21], v153 offset:32768
	ds_read_b128 v[22:25], v153 offset:33792
	ds_read_b128 v[26:29], v153 offset:34816
	ds_read_b128 v[30:33], v153 offset:35840
	ds_read_b128 v[34:37], v153 offset:36864
	ds_read_b128 v[38:41], v153 offset:37888
	ds_read_b128 v[42:45], v153 offset:38912
	ds_read_b128 v[46:49], v153 offset:39936
	s_waitcnt vmcnt(8)
	s_waitcnt lgkmcnt(0)
	s_barrier
	s_setprio 1
	s_waitcnt lgkmcnt(0)
	v_mfma_f32_16x16x128_f8f6f4 v[126:129], v[2:9], v[18:25], v[126:129]
	v_mfma_f32_16x16x128_f8f6f4 v[122:125], v[10:17], v[18:25], v[122:125]
	v_mfma_f32_16x16x128_f8f6f4 v[118:121], v[2:9], v[26:33], v[118:121]
	v_mfma_f32_16x16x128_f8f6f4 v[114:117], v[10:17], v[26:33], v[114:117]
	v_mfma_f32_16x16x128_f8f6f4 v[94:97], v[2:9], v[34:41], v[206:209]
	v_mfma_f32_16x16x128_f8f6f4 v[90:93], v[10:17], v[34:41], v[210:213]
	v_mfma_f32_16x16x128_f8f6f4 v[82:85], v[2:9], v[42:49], v[214:217]
	v_mfma_f32_16x16x128_f8f6f4 v[74:77], v[10:17], v[42:49], v[218:221]
	s_setprio 0
	s_setprio 1
	v_mfma_f32_16x16x128_f8f6f4 v[110:113], v[130:137], v[18:25], v[110:113]
	v_mfma_f32_16x16x128_f8f6f4 v[106:109], v[138:145], v[18:25], v[106:109]
	v_mfma_f32_16x16x128_f8f6f4 v[102:105], v[130:137], v[26:33], v[102:105]
	v_mfma_f32_16x16x128_f8f6f4 v[98:101], v[138:145], v[26:33], v[98:101]
	v_mfma_f32_16x16x128_f8f6f4 v[86:89], v[130:137], v[34:41], v[174:177]
	v_mfma_f32_16x16x128_f8f6f4 v[78:81], v[138:145], v[34:41], v[178:181]
	v_mfma_f32_16x16x128_f8f6f4 v[70:73], v[130:137], v[42:49], v[182:185]
	v_mfma_f32_16x16x128_f8f6f4 v[66:69], v[138:145], v[42:49], v[186:189]
	s_setprio 0
	s_barrier
	s_add_u32 s74, s10, s73
	s_addc_u32 s75, s11, 0
	s_add_i32 s72, s72, 0x20080
	s_mov_b32 m0, s43
	v_lshl_add_u64 v[18:19], s[74:75], 0, v[146:147]
	s_add_u32 s72, s10, s72
	global_load_lds_dwordx4 v[18:19], off
	v_lshl_add_u64 v[18:19], s[74:75], 0, v[148:149]
	s_mov_b32 m0, s46
	s_addc_u32 s73, s11, 0
	s_addk_i32 s24, 0x80
	global_load_lds_dwordx4 v[18:19], off
	v_lshl_add_u64 v[18:19], s[72:73], 0, v[146:147]
	s_mov_b32 m0, s49
	s_add_u32 s24, s10, s24
	global_load_lds_dwordx4 v[18:19], off
	v_lshl_add_u64 v[18:19], s[72:73], 0, v[148:149]
	s_mov_b32 m0, s50
	s_addc_u32 s25, s11, 0
	global_load_lds_dwordx4 v[18:19], off
	v_lshl_add_u64 v[18:19], s[24:25], 0, v[146:147]
	s_mov_b32 m0, s47
	s_nop 0
	global_load_lds_dwordx4 v[18:19], off
	v_lshl_add_u64 v[18:19], s[24:25], 0, v[148:149]
	s_mov_b32 m0, s48
	s_nop 0
	global_load_lds_dwordx4 v[18:19], off
	ds_read_b128 v[158:161], v153 offset:49152
	ds_read_b128 v[162:165], v153 offset:50176
	ds_read_b128 v[166:169], v153 offset:51200
	ds_read_b128 v[170:173], v153 offset:52224
	ds_read_b128 v[174:177], v153 offset:53248
	ds_read_b128 v[178:181], v153 offset:54272
	ds_read_b128 v[182:185], v153 offset:55296
	ds_read_b128 v[186:189], v153 offset:56320
	s_waitcnt vmcnt(8)
	s_waitcnt lgkmcnt(0)
	s_barrier
	s_setprio 1
	s_waitcnt lgkmcnt(0)
	v_mfma_f32_16x16x128_f8f6f4 v[62:65], v[2:9], v[158:165], v[62:65]
	v_mfma_f32_16x16x128_f8f6f4 v[58:61], v[10:17], v[158:165], v[58:61]
	v_mfma_f32_16x16x128_f8f6f4 v[50:53], v[2:9], v[166:173], v[50:53]
	v_mfma_f32_16x16x128_f8f6f4 v[42:45], v[10:17], v[166:173], v[190:193]
	v_mfma_f32_16x16x128_f8f6f4 v[34:37], v[2:9], v[174:181], v[194:197]
	v_mfma_f32_16x16x128_f8f6f4 v[26:29], v[10:17], v[174:181], v[198:201]
	v_mfma_f32_16x16x128_f8f6f4 v[18:21], v[2:9], v[182:189], v[202:205]
	v_mfma_f32_16x16x128_f8f6f4 v[10:13], v[10:17], v[182:189], v[222:225]
	s_setprio 0
	s_setprio 1
	v_mfma_f32_16x16x128_f8f6f4 v[54:57], v[130:137], v[158:165], v[54:57]
	v_mfma_f32_16x16x128_f8f6f4 v[46:49], v[138:145], v[158:165], v[226:229]
	v_mfma_f32_16x16x128_f8f6f4 v[38:41], v[130:137], v[166:173], v[230:233]
	v_mfma_f32_16x16x128_f8f6f4 v[30:33], v[138:145], v[166:173], v[234:237]
	v_mfma_f32_16x16x128_f8f6f4 v[22:25], v[130:137], v[174:181], v[238:241]
	v_mfma_f32_16x16x128_f8f6f4 v[14:17], v[138:145], v[174:181], v[242:245]
	v_mfma_f32_16x16x128_f8f6f4 v[6:9], v[130:137], v[182:189], v[246:249]
	v_mfma_f32_16x16x128_f8f6f4 v[2:5], v[138:145], v[182:189], v[250:253]
	s_setprio 0
	s_barrier
	s_add_i32 s70, s70, 2
	s_addk_i32 s71, 0x100
	s_cmp_gt_u32 s70, 5
	s_cbranch_scc0 .LBB0_1450
	s_and_b64 vcc, exec, s[14:15]
	s_cbranch_vccz .LBB0_1453
	s_barrier

; #define PG8_STAGE(bufoff, gbase, voff) do { _Pragma("unroll") for (int _i = 0; _i < 2; ++_i) \
;         __builtin_amdgcn_global_load_lds((const unsigned*)(wsb + (size_t)(gbase) + (voff)[_i]), (LAS unsigned*)(lds + (bufoff) + ldsw + _i * 8192), 16, 0, 0); } while (0)
; #define PG8_LDA(dst, b, h) do { _Pragma("unroll") for (int m = 0; m < 4; ++m) { if constexpr (FP8) dst##8[m] = PG8_LD8(pa, PG8_SA(b, h) + m * 2048); \
;         else { _Pragma("unroll") for (int k = 0; k < 2; ++k) dst[m][k] = *(const LAS bf16x8*)(pa + PG8_SA(b, h) + m * 2048 + k * 1024); } } } while (0)
; #define PG8_LDB(dst, b, h) do { _Pragma("unroll") for (int n = 0; n < 2; ++n) { if constexpr (FP8) dst##8[n] = PG8_LD8(pb, PG8_SA(b, h) + n * 2048); \
;         else { _Pragma("unroll") for (int k = 0; k < 2; ++k) dst[n][k] = *(const LAS bf16x8*)(pb + PG8_SA(b, h) + n * 2048 + k * 1024); } } } while (0)
; #define PG8_BAR __builtin_amdgcn_s_barrier()
; template <class Epi, class Sched, bool PERM, bool FP8 = false, bool GATHER = false>
; DI void gemm_phase(LAS unsigned char* lds, const unsigned char* wsb, const unsigned lda, const unsigned ldb, const int nt, const Sched& S, const Epi& E) {
;     ...
;         for (int t = 0; t < nt; t += 2) {
;             const bool last = (t == nt - 2);
;             const unsigned b2 = last ? nB : cB + (unsigned)(t + 2) * kstep, b3 = b2 + kstep;
;             const int k2 = last ? 0 : t + 2, k3 = k2 + 1;
;             PG8_LDB(B0, 0, 0); PG8_LDB(B1, 0, 1); PG8_SCHED; PG8_LDA(At, 0, 0); PG8_STAGEA(PG8_SA(1, 1), t + 1, 1, false);
;             if constexpr (GATHER) { if (last) {
;                 int tz = tid; asm volatile("" : "+v"(tz));
; #pragma unroll
;                 for (int i = 0; i < 2; ++i) { int R, C; stage_rc(tz * 16 + i * 8192, R, C);
; #pragma unroll
;                     for (int h = 0; h < 2; ++h) { const unsigned tk = (unsigned)tokt[h * HALF + R]; offC[h][i] = (tk < (unsigned)NTOK ? tk : (unsigned)(NTOK - 1)) * lda + (unsigned)C * 2u; } } } }
;             PG8_WAIT_V(8); PG8_WAIT_L(0); PG8_BAR; PG8_MMA(0, 0, At, B0); PG8_MMA(0, 1, At, B1); PG8_BAR; PG8_SCHED;
;             PG8_LDA(At, 0, 1); PG8_STAGE(PG8_SB(0, 0), b2, voffB); PG8_STAGE(PG8_SB(0, 1), b2 + hstepB, voffB); PG8_STAGEA(PG8_SA(0, 0), k2, 0, last);
;             PG8_WAIT_V(8); PG8_WAIT_L(0); PG8_BAR; PG8_MMA(1, 0, At, B0); PG8_MMA(1, 1, At, B1); PG8_BAR; PG8_SCHED;
.LBB0_1626:
	ds_read_b128 v[130:133], v186
	ds_read_b128 v[134:137], v186 offset:1024
	ds_read_b128 v[138:141], v186 offset:2048
	ds_read_b128 v[142:145], v186 offset:3072
	ds_read_b128 v[146:149], v186 offset:16384
	ds_read_b128 v[150:153], v186 offset:17408
	ds_read_b128 v[160:163], v186 offset:18432
	ds_read_b128 v[164:167], v186 offset:19456
	s_add_i32 s53, s7, 0xfffe0080
	s_cmp_eq_u32 s8, 4
	s_cselect_b32 s9, s50, s6
	s_cselect_b32 s53, s49, s53
	s_add_i32 s58, s9, 0x80
	s_add_u32 s60, s12, s7
	s_addc_u32 s61, s13, 0
	v_lshl_add_u64 v[206:207], s[60:61], 0, v[154:155]
	s_add_i32 m0, s69, 0xc000
	ds_read_b128 v[168:171], v185
	ds_read_b128 v[172:175], v185 offset:1024
	ds_read_b128 v[176:179], v185 offset:2048
	ds_read_b128 v[180:183], v185 offset:3072
	ds_read_b128 v[190:193], v185 offset:4096
	ds_read_b128 v[194:197], v185 offset:5120
	ds_read_b128 v[198:201], v185 offset:6144
	ds_read_b128 v[202:205], v185 offset:7168
	global_load_lds_dwordx4 v[206:207], off
	v_lshl_add_u64 v[206:207], s[60:61], 0, v[156:157]
	s_add_i32 m0, s69, 0xe000
	s_nop 0
	global_load_lds_dwordx4 v[206:207], off
	s_waitcnt vmcnt(8)
	s_waitcnt lgkmcnt(0)
	s_barrier
	s_setprio 1
	s_waitcnt lgkmcnt(0)
	v_mfma_f32_16x16x128_f8f6f4 v[126:129], v[130:137], v[168:175], v[126:129]
	v_mfma_f32_16x16x128_f8f6f4 v[122:125], v[138:145], v[168:175], v[122:125]
	v_mfma_f32_16x16x128_f8f6f4 v[110:113], v[130:137], v[176:183], v[110:113]
	v_mfma_f32_16x16x128_f8f6f4 v[106:109], v[138:145], v[176:183], v[106:109]
	v_mfma_f32_16x16x128_f8f6f4 v[206:209], v[130:137], v[190:197], v[94:97]
	v_mfma_f32_16x16x128_f8f6f4 v[210:213], v[138:145], v[190:197], v[90:93]
	v_mfma_f32_16x16x128_f8f6f4 v[214:217], v[130:137], v[198:205], v[78:81]
	v_mfma_f32_16x16x128_f8f6f4 v[218:221], v[138:145], v[198:205], v[74:77]
	s_setprio 0
	s_setprio 1
	v_mfma_f32_16x16x128_f8f6f4 v[118:121], v[146:153], v[168:175], v[118:121]
	v_mfma_f32_16x16x128_f8f6f4 v[114:117], v[160:167], v[168:175], v[114:117]
	v_mfma_f32_16x16x128_f8f6f4 v[102:105], v[146:153], v[176:183], v[102:105]
	v_mfma_f32_16x16x128_f8f6f4 v[98:101], v[160:167], v[176:183], v[98:101]
	v_mfma_f32_16x16x128_f8f6f4 v[168:171], v[146:153], v[190:197], v[86:89]
	v_mfma_f32_16x16x128_f8f6f4 v[172:175], v[160:167], v[190:197], v[82:85]
	v_mfma_f32_16x16x128_f8f6f4 v[176:179], v[146:153], v[198:205], v[70:73]
	v_mfma_f32_16x16x128_f8f6f4 v[180:183], v[160:167], v[198:205], v[66:69]
	s_setprio 0
	s_barrier
	s_add_u32 s60, s12, s9
	s_addc_u32 s61, s13, 0
	s_mov_b32 m0, s70
	v_lshl_add_u64 v[190:191], s[60:61], 0, v[154:155]
	s_add_i32 s59, s9, 0x20000
	global_load_lds_dwordx4 v[190:191], off
	v_lshl_add_u64 v[190:191], s[60:61], 0, v[156:157]
	s_add_u32 s60, s12, s59
	s_mov_b32 m0, s71
	s_addc_u32 s61, s13, 0
	global_load_lds_dwordx4 v[190:191], off
	v_lshl_add_u64 v[190:191], s[60:61], 0, v[154:155]
	s_mov_b32 m0, s72
	s_nop 0
	global_load_lds_dwordx4 v[190:191], off
	v_lshl_add_u64 v[190:191], s[60:61], 0, v[156:157]
	s_add_u32 s60, s12, s53
	s_mov_b32 m0, s73
	s_addc_u32 s61, s13, 0
	global_load_lds_dwordx4 v[190:191], off
	v_lshl_add_u64 v[190:191], s[60:61], 0, v[154:155]
	s_mov_b32 m0, s69
	s_nop 0
	global_load_lds_dwordx4 v[190:191], off
	v_lshl_add_u64 v[190:191], s[60:61], 0, v[156:157]
	s_mov_b32 m0, s74
	s_nop 0
	global_load_lds_dwordx4 v[190:191], off
	ds_read_b128 v[66:69], v185 offset:16384
	ds_read_b128 v[70:73], v185 offset:17408
	ds_read_b128 v[74:77], v185 offset:18432
	ds_read_b128 v[78:81], v185 offset:19456
	ds_read_b128 v[82:85], v185 offset:20480
	ds_read_b128 v[86:89], v185 offset:21504
	ds_read_b128 v[90:93], v185 offset:22528
	ds_read_b128 v[94:97], v185 offset:23552
	s_waitcnt vmcnt(8)
	s_waitcnt lgkmcnt(0)
	s_barrier
	s_setprio 1
	s_waitcnt lgkmcnt(0)
	v_mfma_f32_16x16x128_f8f6f4 v[62:65], v[130:137], v[66:73], v[62:65]
	v_mfma_f32_16x16x128_f8f6f4 v[58:61], v[138:145], v[66:73], v[58:61]
	v_mfma_f32_16x16x128_f8f6f4 v[190:193], v[130:137], v[74:81], v[46:49]
	v_mfma_f32_16x16x128_f8f6f4 v[194:197], v[138:145], v[74:81], v[42:45]
	v_mfma_f32_16x16x128_f8f6f4 v[198:201], v[130:137], v[82:89], v[30:33]
	v_mfma_f32_16x16x128_f8f6f4 v[202:205], v[138:145], v[82:89], v[26:29]
	v_mfma_f32_16x16x128_f8f6f4 v[222:225], v[130:137], v[90:97], v[14:17]
	v_mfma_f32_16x16x128_f8f6f4 v[226:229], v[138:145], v[90:97], v[10:13]
	s_setprio 0
	s_setprio 1
	v_mfma_f32_16x16x128_f8f6f4 v[54:57], v[146:153], v[66:73], v[54:57]
	v_mfma_f32_16x16x128_f8f6f4 v[50:53], v[160:167], v[66:73], v[50:53]
	v_mfma_f32_16x16x128_f8f6f4 v[230:233], v[146:153], v[74:81], v[38:41]
	v_mfma_f32_16x16x128_f8f6f4 v[234:237], v[160:167], v[74:81], v[34:37]
	v_mfma_f32_16x16x128_f8f6f4 v[238:241], v[146:153], v[82:89], v[22:25]
	v_mfma_f32_16x16x128_f8f6f4 v[242:245], v[160:167], v[82:89], v[18:21]
	v_mfma_f32_16x16x128_f8f6f4 v[246:249], v[146:153], v[90:97], v[6:9]
	v_mfma_f32_16x16x128_f8f6f4 v[250:253], v[160:167], v[90:97], v[2:5]
	s_setprio 0
	s_barrier
; #define PG8_STAGE(bufoff, gbase, voff) do { _Pragma("unroll") for (int _i = 0; _i < 2; ++_i) \
;         __builtin_amdgcn_global_load_lds((const unsigned*)(wsb + (size_t)(gbase) + (voff)[_i]), (LAS unsigned*)(lds + (bufoff) + ldsw + _i * 8192), 16, 0, 0); } while (0)
; #define PG8_LDA(dst, b, h) do { _Pragma("unroll") for (int m = 0; m < 4; ++m) { if constexpr (FP8) dst##8[m] = PG8_LD8(pa, PG8_SA(b, h) + m * 2048); \
;         else { _Pragma("unroll") for (int k = 0; k < 2; ++k) dst[m][k] = *(const LAS bf16x8*)(pa + PG8_SA(b, h) + m * 2048 + k * 1024); } } } while (0)
; #define PG8_LDB(dst, b, h) do { _Pragma("unroll") for (int n = 0; n < 2; ++n) { if constexpr (FP8) dst##8[n] = PG8_LD8(pb, PG8_SA(b, h) + n * 2048); \
;         else { _Pragma("unroll") for (int k = 0; k < 2; ++k) dst[n][k] = *(const LAS bf16x8*)(pb + PG8_SA(b, h) + n * 2048 + k * 1024); } } } while (0)
; #define PG8_WAIT_V(n) asm volatile("s_waitcnt vmcnt(" #n ")" ::: "memory")
; #define PG8_WAIT_L(n) asm volatile("s_waitcnt lgkmcnt(" #n ")" ::: "memory")
; #define PG8_BAR __builtin_amdgcn_s_barrier()
; #define PG8_SCHED __builtin_amdgcn_sched_barrier(0)
; template <class Epi, class Sched, bool PERM, bool FP8 = false, bool GATHER = false>
; DI void gemm_phase(LAS unsigned char* lds, const unsigned char* wsb, const unsigned lda, const unsigned ldb, const int nt, const Sched& S, const Epi& E) {
;     ...
;             PG8_LDB(B0, 1, 0); PG8_LDB(B1, 1, 1); PG8_SCHED; PG8_LDA(At, 1, 0); PG8_STAGEA(PG8_SA(0, 1), k2, 1, last);
;             PG8_WAIT_V(8); PG8_WAIT_L(0); PG8_BAR; PG8_MMA(0, 0, At, B0); PG8_MMA(0, 1, At, B1); PG8_BAR; PG8_SCHED;
;             PG8_LDA(At, 1, 1); PG8_STAGE(PG8_SB(1, 0), b3, voffB); PG8_STAGE(PG8_SB(1, 1), b3 + hstepB, voffB); PG8_STAGEA(PG8_SA(1, 0), k3, 0, last);
;             PG8_WAIT_V(8); PG8_WAIT_L(0); PG8_BAR; PG8_MMA(1, 0, At, B0); PG8_MMA(1, 1, At, B1); PG8_BAR; PG8_SCHED;
;         }
;         if (wr == 0) PG8_BAR;
	s_nop 4
	s_add_i32 s59, s53, 0x20000
	s_add_u32 s60, s12, s59
	s_addc_u32 s61, s13, 0
	s_mov_b32 m0, s75
	v_lshl_add_u64 v[66:67], s[60:61], 0, v[154:155]
	global_load_lds_dwordx4 v[66:67], off
	v_lshl_add_u64 v[66:67], s[60:61], 0, v[156:157]
	s_mov_b32 m0, s76
	s_nop 0
	global_load_lds_dwordx4 v[66:67], off
	ds_read_b128 v[2:5], v186 offset:32768
	ds_read_b128 v[6:9], v186 offset:33792
	ds_read_b128 v[18:21], v186 offset:34816
	ds_read_b128 v[22:25], v186 offset:35840
	ds_read_b128 v[130:133], v186 offset:49152
	ds_read_b128 v[134:137], v186 offset:50176
	ds_read_b128 v[138:141], v186 offset:51200
	ds_read_b128 v[142:145], v186 offset:52224
	ds_read_b128 v[10:13], v185 offset:32768
	ds_read_b128 v[14:17], v185 offset:33792
	ds_read_b128 v[26:29], v185 offset:34816
	ds_read_b128 v[30:33], v185 offset:35840
	ds_read_b128 v[34:37], v185 offset:36864
	ds_read_b128 v[38:41], v185 offset:37888
	ds_read_b128 v[42:45], v185 offset:38912
	ds_read_b128 v[46:49], v185 offset:39936
	s_waitcnt vmcnt(8)
	s_waitcnt lgkmcnt(0)
	s_barrier
	s_setprio 1
	s_waitcnt lgkmcnt(0)
	v_mfma_f32_16x16x128_f8f6f4 v[126:129], v[2:9], v[10:17], v[126:129]
	v_mfma_f32_16x16x128_f8f6f4 v[122:125], v[18:25], v[10:17], v[122:125]
	v_mfma_f32_16x16x128_f8f6f4 v[110:113], v[2:9], v[26:33], v[110:113]
	v_mfma_f32_16x16x128_f8f6f4 v[106:109], v[18:25], v[26:33], v[106:109]
	v_mfma_f32_16x16x128_f8f6f4 v[94:97], v[2:9], v[34:41], v[206:209]
	v_mfma_f32_16x16x128_f8f6f4 v[90:93], v[18:25], v[34:41], v[210:213]
	v_mfma_f32_16x16x128_f8f6f4 v[78:81], v[2:9], v[42:49], v[214:217]
	v_mfma_f32_16x16x128_f8f6f4 v[74:77], v[18:25], v[42:49], v[218:221]
	s_setprio 0
	s_setprio 1
	v_mfma_f32_16x16x128_f8f6f4 v[118:121], v[130:137], v[10:17], v[118:121]
	v_mfma_f32_16x16x128_f8f6f4 v[114:117], v[138:145], v[10:17], v[114:117]
	v_mfma_f32_16x16x128_f8f6f4 v[102:105], v[130:137], v[26:33], v[102:105]
	v_mfma_f32_16x16x128_f8f6f4 v[98:101], v[138:145], v[26:33], v[98:101]
	v_mfma_f32_16x16x128_f8f6f4 v[86:89], v[130:137], v[34:41], v[168:171]
	v_mfma_f32_16x16x128_f8f6f4 v[82:85], v[138:145], v[34:41], v[172:175]
	v_mfma_f32_16x16x128_f8f6f4 v[70:73], v[130:137], v[42:49], v[176:179]
	v_mfma_f32_16x16x128_f8f6f4 v[66:69], v[138:145], v[42:49], v[180:183]
	s_setprio 0
	s_barrier
	s_add_u32 s58, s12, s58
	s_addc_u32 s59, s13, 0
	s_mov_b32 m0, s85
	v_lshl_add_u64 v[10:11], s[58:59], 0, v[154:155]
	s_add_i32 s9, s9, 0x20080
	global_load_lds_dwordx4 v[10:11], off
	v_lshl_add_u64 v[10:11], s[58:59], 0, v[156:157]
	s_add_u32 s58, s12, s9
	s_mov_b32 m0, s86
	s_addc_u32 s59, s13, 0
	global_load_lds_dwordx4 v[10:11], off
	v_lshl_add_u64 v[10:11], s[58:59], 0, v[154:155]
	s_mov_b32 m0, s89
	s_addk_i32 s53, 0x80
	global_load_lds_dwordx4 v[10:11], off
	v_lshl_add_u64 v[10:11], s[58:59], 0, v[156:157]
	s_add_u32 s58, s12, s53
	s_mov_b32 m0, s90
	s_addc_u32 s59, s13, 0
	global_load_lds_dwordx4 v[10:11], off
	v_lshl_add_u64 v[10:11], s[58:59], 0, v[154:155]
	s_mov_b32 m0, s87
	s_nop 0
	global_load_lds_dwordx4 v[10:11], off
	v_lshl_add_u64 v[10:11], s[58:59], 0, v[156:157]
	s_mov_b32 m0, s88
	s_nop 0
	global_load_lds_dwordx4 v[10:11], off
	ds_read_b128 v[34:37], v185 offset:49152
	ds_read_b128 v[38:41], v185 offset:50176
	ds_read_b128 v[146:149], v185 offset:51200
	ds_read_b128 v[150:153], v185 offset:52224
	ds_read_b128 v[160:163], v185 offset:53248
	ds_read_b128 v[164:167], v185 offset:54272
	ds_read_b128 v[168:171], v185 offset:55296
	ds_read_b128 v[172:175], v185 offset:56320
	s_waitcnt vmcnt(8)
	s_waitcnt lgkmcnt(0)
	s_barrier
	s_setprio 1
	s_waitcnt lgkmcnt(0)
	v_mfma_f32_16x16x128_f8f6f4 v[62:65], v[2:9], v[34:41], v[62:65]
	v_mfma_f32_16x16x128_f8f6f4 v[58:61], v[18:25], v[34:41], v[58:61]
	v_mfma_f32_16x16x128_f8f6f4 v[46:49], v[2:9], v[146:153], v[190:193]
	v_mfma_f32_16x16x128_f8f6f4 v[42:45], v[18:25], v[146:153], v[194:197]
	v_mfma_f32_16x16x128_f8f6f4 v[30:33], v[2:9], v[160:167], v[198:201]
	v_mfma_f32_16x16x128_f8f6f4 v[26:29], v[18:25], v[160:167], v[202:205]
	v_mfma_f32_16x16x128_f8f6f4 v[14:17], v[2:9], v[168:175], v[222:225]
	v_mfma_f32_16x16x128_f8f6f4 v[10:13], v[18:25], v[168:175], v[226:229]
	s_setprio 0
	s_setprio 1
	v_mfma_f32_16x16x128_f8f6f4 v[54:57], v[130:137], v[34:41], v[54:57]
	v_mfma_f32_16x16x128_f8f6f4 v[50:53], v[138:145], v[34:41], v[50:53]
	v_mfma_f32_16x16x128_f8f6f4 v[38:41], v[130:137], v[146:153], v[230:233]
	v_mfma_f32_16x16x128_f8f6f4 v[34:37], v[138:145], v[146:153], v[234:237]
	v_mfma_f32_16x16x128_f8f6f4 v[22:25], v[130:137], v[160:167], v[238:241]
	v_mfma_f32_16x16x128_f8f6f4 v[18:21], v[138:145], v[160:167], v[242:245]
	v_mfma_f32_16x16x128_f8f6f4 v[6:9], v[130:137], v[168:175], v[246:249]
	v_mfma_f32_16x16x128_f8f6f4 v[2:5], v[138:145], v[168:175], v[250:253]
	s_setprio 0
	s_barrier
	s_add_i32 s8, s8, 2
	s_addk_i32 s7, 0x100
	s_addk_i32 s6, 0x100
	s_cmp_gt_u32 s8, 5
	s_cbranch_scc0 .LBB0_1626
	s_and_b64 vcc, exec, s[16:17]
	s_cbranch_vccz .LBB0_1629
	s_barrier

; #define PG8_STAGE(bufoff, gbase, voff) do { _Pragma("unroll") for (int _i = 0; _i < 2; ++_i) \
;         __builtin_amdgcn_global_load_lds((const unsigned*)(wsb + (size_t)(gbase) + (voff)[_i]), (LAS unsigned*)(lds + (bufoff) + ldsw + _i * 8192), 16, 0, 0); } while (0)
; #define PG8_LDA(dst, b, h) do { _Pragma("unroll") for (int m = 0; m < 4; ++m) { if constexpr (FP8) dst##8[m] = PG8_LD8(pa, PG8_SA(b, h) + m * 2048); \
;         else { _Pragma("unroll") for (int k = 0; k < 2; ++k) dst[m][k] = *(const LAS bf16x8*)(pa + PG8_SA(b, h) + m * 2048 + k * 1024); } } } while (0)
; #define PG8_LDB(dst, b, h) do { _Pragma("unroll") for (int n = 0; n < 2; ++n) { if constexpr (FP8) dst##8[n] = PG8_LD8(pb, PG8_SA(b, h) + n * 2048); \
;         else { _Pragma("unroll") for (int k = 0; k < 2; ++k) dst[n][k] = *(const LAS bf16x8*)(pb + PG8_SA(b, h) + n * 2048 + k * 1024); } } } while (0)
; #define PG8_BAR __builtin_amdgcn_s_barrier()
; template <class Epi, class Sched, bool PERM, bool FP8 = false, bool GATHER = false>
; DI void gemm_phase(LAS unsigned char* lds, const unsigned char* wsb, const unsigned lda, const unsigned ldb, const int nt, const Sched& S, const Epi& E) {
;     ...
;         for (int t = 0; t < nt; t += 2) {
;             const bool last = (t == nt - 2);
;             const unsigned b2 = last ? nB : cB + (unsigned)(t + 2) * kstep, b3 = b2 + kstep;
;             const int k2 = last ? 0 : t + 2, k3 = k2 + 1;
;             PG8_LDB(B0, 0, 0); PG8_LDB(B1, 0, 1); PG8_SCHED; PG8_LDA(At, 0, 0); PG8_STAGEA(PG8_SA(1, 1), t + 1, 1, false);
;             if constexpr (GATHER) { if (last) {
;                 int tz = tid; asm volatile("" : "+v"(tz));
; #pragma unroll
;                 for (int i = 0; i < 2; ++i) { int R, C; stage_rc(tz * 16 + i * 8192, R, C);
; #pragma unroll
;                     for (int h = 0; h < 2; ++h) { const unsigned tk = (unsigned)tokt[h * HALF + R]; offC[h][i] = (tk < (unsigned)NTOK ? tk : (unsigned)(NTOK - 1)) * lda + (unsigned)C * 2u; } } } }
;             PG8_WAIT_V(8); PG8_WAIT_L(0); PG8_BAR; PG8_MMA(0, 0, At, B0); PG8_MMA(0, 1, At, B1); PG8_BAR; PG8_SCHED;
;             PG8_LDA(At, 0, 1); PG8_STAGE(PG8_SB(0, 0), b2, voffB); PG8_STAGE(PG8_SB(0, 1), b2 + hstepB, voffB); PG8_STAGEA(PG8_SA(0, 0), k2, 0, last);
;             PG8_WAIT_V(8); PG8_WAIT_L(0); PG8_BAR; PG8_MMA(1, 0, At, B0); PG8_MMA(1, 1, At, B1); PG8_BAR; PG8_SCHED;
.LBB0_1802:
	s_add_i32 s24, s20, 0xfffe0080
	s_cmp_eq_u32 s21, 4
	s_cselect_b32 s22, s72, s8
	s_cselect_b32 s24, s71, s24
	s_add_i32 s36, s22, 0x80
	s_add_u32 s38, s6, s20
	s_addc_u32 s39, s7, 0
	s_mov_b32 m0, s65
	v_lshl_add_u64 v[130:131], s[38:39], 0, v[138:139]
	global_load_lds_dwordx4 v[130:131], off
	v_lshl_add_u64 v[130:131], s[38:39], 0, v[134:135]
	s_mov_b32 m0, s66
	s_nop 0
	global_load_lds_dwordx4 v[130:131], off
	ds_read_b128 v[144:147], v142
	ds_read_b128 v[148:151], v142 offset:1024
	ds_read_b128 v[152:155], v142 offset:2048
	ds_read_b128 v[156:159], v142 offset:3072
	ds_read_b128 v[160:163], v142 offset:16384
	ds_read_b128 v[164:167], v142 offset:17408
	ds_read_b128 v[168:171], v142 offset:18432
	ds_read_b128 v[172:175], v142 offset:19456
	ds_read_b128 v[176:179], v141
	ds_read_b128 v[180:183], v141 offset:1024
	ds_read_b128 v[184:187], v141 offset:2048
	ds_read_b128 v[188:191], v141 offset:3072
	ds_read_b128 v[192:195], v141 offset:4096
	ds_read_b128 v[196:199], v141 offset:5120
	ds_read_b128 v[200:203], v141 offset:6144
	ds_read_b128 v[204:207], v141 offset:7168
	s_waitcnt vmcnt(8)
	s_waitcnt lgkmcnt(0)
	s_barrier
	s_setprio 1
	s_waitcnt lgkmcnt(0)
	v_mfma_f32_16x16x128_f8f6f4 v[126:129], v[144:151], v[176:183], v[126:129]
	v_mfma_f32_16x16x128_f8f6f4 v[122:125], v[152:159], v[176:183], v[122:125]
	v_mfma_f32_16x16x128_f8f6f4 v[114:117], v[144:151], v[184:191], v[114:117]
	v_mfma_f32_16x16x128_f8f6f4 v[106:109], v[152:159], v[184:191], v[106:109]
	v_mfma_f32_16x16x128_f8f6f4 v[98:101], v[144:151], v[192:199], v[98:101]
	v_mfma_f32_16x16x128_f8f6f4 v[208:211], v[152:159], v[192:199], v[90:93]
	v_mfma_f32_16x16x128_f8f6f4 v[212:215], v[144:151], v[200:207], v[82:85]
	v_mfma_f32_16x16x128_f8f6f4 v[216:219], v[152:159], v[200:207], v[74:77]
	s_setprio 0
	s_setprio 1
	v_mfma_f32_16x16x128_f8f6f4 v[118:121], v[160:167], v[176:183], v[118:121]
	v_mfma_f32_16x16x128_f8f6f4 v[110:113], v[168:175], v[176:183], v[110:113]
	v_mfma_f32_16x16x128_f8f6f4 v[102:105], v[160:167], v[184:191], v[102:105]
	v_mfma_f32_16x16x128_f8f6f4 v[176:179], v[168:175], v[184:191], v[94:97]
	v_mfma_f32_16x16x128_f8f6f4 v[180:183], v[160:167], v[192:199], v[86:89]
	v_mfma_f32_16x16x128_f8f6f4 v[184:187], v[168:175], v[192:199], v[78:81]
	v_mfma_f32_16x16x128_f8f6f4 v[188:191], v[160:167], v[200:207], v[70:73]
	v_mfma_f32_16x16x128_f8f6f4 v[192:195], v[168:175], v[200:207], v[66:69]
	s_setprio 0
	s_barrier
	s_add_u32 s38, s6, s22
	s_addc_u32 s39, s7, 0
	s_mov_b32 m0, s28
	v_lshl_add_u64 v[130:131], s[38:39], 0, v[252:253]
	s_add_i32 s37, s22, 0x20000
	global_load_lds_dwordx4 v[130:131], off
	v_lshl_add_u64 v[130:131], s[38:39], 0, v[136:137]
	s_add_u32 s38, s6, s37
	s_mov_b32 m0, s29
	s_addc_u32 s39, s7, 0
	global_load_lds_dwordx4 v[130:131], off
	v_lshl_add_u64 v[130:131], s[38:39], 0, v[252:253]
	s_mov_b32 m0, s42
	s_nop 0
	global_load_lds_dwordx4 v[130:131], off
	v_lshl_add_u64 v[130:131], s[38:39], 0, v[136:137]
	s_add_u32 s38, s6, s24
	s_mov_b32 m0, s43
	s_addc_u32 s39, s7, 0
	global_load_lds_dwordx4 v[130:131], off
	v_lshl_add_u64 v[130:131], s[38:39], 0, v[138:139]
	s_mov_b32 m0, s17
	s_nop 0
	global_load_lds_dwordx4 v[130:131], off
	v_lshl_add_u64 v[130:131], s[38:39], 0, v[134:135]
	s_mov_b32 m0, s46
	s_nop 0
	global_load_lds_dwordx4 v[130:131], off
	ds_read_b128 v[66:69], v141 offset:16384
	ds_read_b128 v[70:73], v141 offset:17408
	ds_read_b128 v[74:77], v141 offset:18432
	ds_read_b128 v[78:81], v141 offset:19456
	ds_read_b128 v[82:85], v141 offset:20480
	ds_read_b128 v[86:89], v141 offset:21504
	ds_read_b128 v[90:93], v141 offset:22528
	ds_read_b128 v[94:97], v141 offset:23552
	s_waitcnt vmcnt(8)
	s_waitcnt lgkmcnt(0)
	s_barrier
	s_setprio 1
	s_waitcnt lgkmcnt(0)
	v_mfma_f32_16x16x128_f8f6f4 v[62:65], v[144:151], v[66:73], v[62:65]
	v_mfma_f32_16x16x128_f8f6f4 v[58:61], v[152:159], v[66:73], v[58:61]
	v_mfma_f32_16x16x128_f8f6f4 v[50:53], v[144:151], v[74:81], v[50:53]
	v_mfma_f32_16x16x128_f8f6f4 v[196:199], v[152:159], v[74:81], v[42:45]
	v_mfma_f32_16x16x128_f8f6f4 v[200:203], v[144:151], v[82:89], v[34:37]
	v_mfma_f32_16x16x128_f8f6f4 v[204:207], v[152:159], v[82:89], v[26:29]
	v_mfma_f32_16x16x128_f8f6f4 v[220:223], v[144:151], v[90:97], v[18:21]
	v_mfma_f32_16x16x128_f8f6f4 v[224:227], v[152:159], v[90:97], v[10:13]
	s_setprio 0
	s_setprio 1
	v_mfma_f32_16x16x128_f8f6f4 v[54:57], v[160:167], v[66:73], v[54:57]
	v_mfma_f32_16x16x128_f8f6f4 v[228:231], v[168:175], v[66:73], v[46:49]
	v_mfma_f32_16x16x128_f8f6f4 v[232:235], v[160:167], v[74:81], v[38:41]
	v_mfma_f32_16x16x128_f8f6f4 v[236:239], v[168:175], v[74:81], v[30:33]
	v_mfma_f32_16x16x128_f8f6f4 v[240:243], v[160:167], v[82:89], v[22:25]
	v_mfma_f32_16x16x128_f8f6f4 v[244:247], v[168:175], v[82:89], v[14:17]
	v_mfma_f32_16x16x128_f8f6f4 v[248:251], v[160:167], v[90:97], v[6:9]
	v_mfma_f32_16x16x128_f8f6f4 v[130:133], v[168:175], v[90:97], v[2:5]
	s_setprio 0
	s_barrier
; #define PG8_STAGE(bufoff, gbase, voff) do { _Pragma("unroll") for (int _i = 0; _i < 2; ++_i) \
;         __builtin_amdgcn_global_load_lds((const unsigned*)(wsb + (size_t)(gbase) + (voff)[_i]), (LAS unsigned*)(lds + (bufoff) + ldsw + _i * 8192), 16, 0, 0); } while (0)
; #define PG8_LDA(dst, b, h) do { _Pragma("unroll") for (int m = 0; m < 4; ++m) { if constexpr (FP8) dst##8[m] = PG8_LD8(pa, PG8_SA(b, h) + m * 2048); \
;         else { _Pragma("unroll") for (int k = 0; k < 2; ++k) dst[m][k] = *(const LAS bf16x8*)(pa + PG8_SA(b, h) + m * 2048 + k * 1024); } } } while (0)
; #define PG8_LDB(dst, b, h) do { _Pragma("unroll") for (int n = 0; n < 2; ++n) { if constexpr (FP8) dst##8[n] = PG8_LD8(pb, PG8_SA(b, h) + n * 2048); \
;         else { _Pragma("unroll") for (int k = 0; k < 2; ++k) dst[n][k] = *(const LAS bf16x8*)(pb + PG8_SA(b, h) + n * 2048 + k * 1024); } } } while (0)
; #define PG8_WAIT_V(n) asm volatile("s_waitcnt vmcnt(" #n ")" ::: "memory")
; #define PG8_WAIT_L(n) asm volatile("s_waitcnt lgkmcnt(" #n ")" ::: "memory")
; #define PG8_BAR __builtin_amdgcn_s_barrier()
; #define PG8_SCHED __builtin_amdgcn_sched_barrier(0)
; template <class Epi, class Sched, bool PERM, bool FP8 = false, bool GATHER = false>
; DI void gemm_phase(LAS unsigned char* lds, const unsigned char* wsb, const unsigned lda, const unsigned ldb, const int nt, const Sched& S, const Epi& E) {
;     ...
;             PG8_LDB(B0, 1, 0); PG8_LDB(B1, 1, 1); PG8_SCHED; PG8_LDA(At, 1, 0); PG8_STAGEA(PG8_SA(0, 1), k2, 1, last);
;             PG8_WAIT_V(8); PG8_WAIT_L(0); PG8_BAR; PG8_MMA(0, 0, At, B0); PG8_MMA(0, 1, At, B1); PG8_BAR; PG8_SCHED;
;             PG8_LDA(At, 1, 1); PG8_STAGE(PG8_SB(1, 0), b3, voffB); PG8_STAGE(PG8_SB(1, 1), b3 + hstepB, voffB); PG8_STAGEA(PG8_SA(1, 0), k3, 0, last);
;             PG8_WAIT_V(8); PG8_WAIT_L(0); PG8_BAR; PG8_MMA(1, 0, At, B0); PG8_MMA(1, 1, At, B1); PG8_BAR; PG8_SCHED;
;         }
;         if (wr == 0) PG8_BAR;
	s_nop 4
	s_add_i32 s37, s24, 0x20000
	s_add_u32 s38, s6, s37
	s_addc_u32 s39, s7, 0
	s_mov_b32 m0, s47
	v_lshl_add_u64 v[66:67], s[38:39], 0, v[138:139]
	global_load_lds_dwordx4 v[66:67], off
	v_lshl_add_u64 v[66:67], s[38:39], 0, v[134:135]
	s_mov_b32 m0, s48
	s_nop 0
	global_load_lds_dwordx4 v[66:67], off
	ds_read_b128 v[2:5], v142 offset:32768
	ds_read_b128 v[6:9], v142 offset:33792
	ds_read_b128 v[10:13], v142 offset:34816
	ds_read_b128 v[14:17], v142 offset:35840
	ds_read_b128 v[144:147], v142 offset:49152
	ds_read_b128 v[148:151], v142 offset:50176
	ds_read_b128 v[152:155], v142 offset:51200
	ds_read_b128 v[156:159], v142 offset:52224
	ds_read_b128 v[18:21], v141 offset:32768
	ds_read_b128 v[22:25], v141 offset:33792
	ds_read_b128 v[26:29], v141 offset:34816
	ds_read_b128 v[30:33], v141 offset:35840
	ds_read_b128 v[34:37], v141 offset:36864
	ds_read_b128 v[38:41], v141 offset:37888
	ds_read_b128 v[42:45], v141 offset:38912
	ds_read_b128 v[46:49], v141 offset:39936
	s_waitcnt vmcnt(8)
	s_waitcnt lgkmcnt(0)
	s_barrier
	s_setprio 1
	s_waitcnt lgkmcnt(0)
	v_mfma_f32_16x16x128_f8f6f4 v[126:129], v[2:9], v[18:25], v[126:129]
	v_mfma_f32_16x16x128_f8f6f4 v[122:125], v[10:17], v[18:25], v[122:125]
	v_mfma_f32_16x16x128_f8f6f4 v[114:117], v[2:9], v[26:33], v[114:117]
	v_mfma_f32_16x16x128_f8f6f4 v[106:109], v[10:17], v[26:33], v[106:109]
	v_mfma_f32_16x16x128_f8f6f4 v[98:101], v[2:9], v[34:41], v[98:101]
	v_mfma_f32_16x16x128_f8f6f4 v[90:93], v[10:17], v[34:41], v[208:211]
	v_mfma_f32_16x16x128_f8f6f4 v[82:85], v[2:9], v[42:49], v[212:215]
	v_mfma_f32_16x16x128_f8f6f4 v[74:77], v[10:17], v[42:49], v[216:219]
	s_setprio 0
	s_setprio 1
	v_mfma_f32_16x16x128_f8f6f4 v[118:121], v[144:151], v[18:25], v[118:121]
	v_mfma_f32_16x16x128_f8f6f4 v[110:113], v[152:159], v[18:25], v[110:113]
	v_mfma_f32_16x16x128_f8f6f4 v[102:105], v[144:151], v[26:33], v[102:105]
	v_mfma_f32_16x16x128_f8f6f4 v[94:97], v[152:159], v[26:33], v[176:179]
	v_mfma_f32_16x16x128_f8f6f4 v[86:89], v[144:151], v[34:41], v[180:183]
	v_mfma_f32_16x16x128_f8f6f4 v[78:81], v[152:159], v[34:41], v[184:187]
	v_mfma_f32_16x16x128_f8f6f4 v[70:73], v[144:151], v[42:49], v[188:191]
	v_mfma_f32_16x16x128_f8f6f4 v[66:69], v[152:159], v[42:49], v[192:195]
	s_setprio 0
	s_barrier
	s_add_u32 s36, s6, s36
	s_addc_u32 s37, s7, 0
	s_mov_b32 m0, s50
	v_lshl_add_u64 v[18:19], s[36:37], 0, v[252:253]
	s_add_i32 s22, s22, 0x20080
	global_load_lds_dwordx4 v[18:19], off
	v_lshl_add_u64 v[18:19], s[36:37], 0, v[136:137]
	s_add_u32 s36, s6, s22
	s_mov_b32 m0, s51
	s_addc_u32 s37, s7, 0
	global_load_lds_dwordx4 v[18:19], off
	v_lshl_add_u64 v[18:19], s[36:37], 0, v[252:253]
	s_mov_b32 m0, s54
	s_addk_i32 s24, 0x80
	global_load_lds_dwordx4 v[18:19], off
	v_lshl_add_u64 v[18:19], s[36:37], 0, v[136:137]
	s_add_u32 s36, s6, s24
	s_mov_b32 m0, s55
	s_addc_u32 s37, s7, 0
	global_load_lds_dwordx4 v[18:19], off
	v_lshl_add_u64 v[18:19], s[36:37], 0, v[138:139]
	s_mov_b32 m0, s52
	s_nop 0
	global_load_lds_dwordx4 v[18:19], off
	v_lshl_add_u64 v[18:19], s[36:37], 0, v[134:135]
	s_mov_b32 m0, s53
	s_nop 0
	global_load_lds_dwordx4 v[18:19], off
	ds_read_b128 v[160:163], v141 offset:49152
	ds_read_b128 v[164:167], v141 offset:50176
	ds_read_b128 v[168:171], v141 offset:51200
	ds_read_b128 v[172:175], v141 offset:52224
	ds_read_b128 v[176:179], v141 offset:53248
	ds_read_b128 v[180:183], v141 offset:54272
	ds_read_b128 v[184:187], v141 offset:55296
	ds_read_b128 v[188:191], v141 offset:56320
	s_waitcnt vmcnt(8)
	s_waitcnt lgkmcnt(0)
	s_barrier
	s_setprio 1
	s_waitcnt lgkmcnt(0)
	v_mfma_f32_16x16x128_f8f6f4 v[62:65], v[2:9], v[160:167], v[62:65]
	v_mfma_f32_16x16x128_f8f6f4 v[58:61], v[10:17], v[160:167], v[58:61]
	v_mfma_f32_16x16x128_f8f6f4 v[50:53], v[2:9], v[168:175], v[50:53]
	v_mfma_f32_16x16x128_f8f6f4 v[42:45], v[10:17], v[168:175], v[196:199]
	v_mfma_f32_16x16x128_f8f6f4 v[34:37], v[2:9], v[176:183], v[200:203]
	v_mfma_f32_16x16x128_f8f6f4 v[26:29], v[10:17], v[176:183], v[204:207]
	v_mfma_f32_16x16x128_f8f6f4 v[18:21], v[2:9], v[184:191], v[220:223]
	v_mfma_f32_16x16x128_f8f6f4 v[10:13], v[10:17], v[184:191], v[224:227]
	s_setprio 0
	s_setprio 1
	v_mfma_f32_16x16x128_f8f6f4 v[54:57], v[144:151], v[160:167], v[54:57]
	v_mfma_f32_16x16x128_f8f6f4 v[46:49], v[152:159], v[160:167], v[228:231]
	v_mfma_f32_16x16x128_f8f6f4 v[38:41], v[144:151], v[168:175], v[232:235]
	v_mfma_f32_16x16x128_f8f6f4 v[30:33], v[152:159], v[168:175], v[236:239]
	v_mfma_f32_16x16x128_f8f6f4 v[22:25], v[144:151], v[176:183], v[240:243]
	v_mfma_f32_16x16x128_f8f6f4 v[14:17], v[152:159], v[176:183], v[244:247]
	v_mfma_f32_16x16x128_f8f6f4 v[6:9], v[144:151], v[184:191], v[248:251]
	v_mfma_f32_16x16x128_f8f6f4 v[2:5], v[152:159], v[184:191], v[130:133]
	s_setprio 0
	s_barrier
	s_add_i32 s21, s21, 2
	s_addk_i32 s20, 0x100
	s_addk_i32 s8, 0x100
	s_cmp_gt_u32 s21, 5
	s_cbranch_scc0 .LBB0_1802
	s_and_b64 vcc, exec, s[14:15]
	s_cbranch_vccz .LBB0_1805
	s_barrier

; #define PG8_STAGE(bufoff, gbase, voff) do { _Pragma("unroll") for (int _i = 0; _i < 2; ++_i) \
;         __builtin_amdgcn_global_load_lds((const unsigned*)(wsb + (size_t)(gbase) + (voff)[_i]), (LAS unsigned*)(lds + (bufoff) + ldsw + _i * 8192), 16, 0, 0); } while (0)
; #define PG8_LDA(dst, b, h) do { _Pragma("unroll") for (int m = 0; m < 4; ++m) { if constexpr (FP8) dst##8[m] = PG8_LD8(pa, PG8_SA(b, h) + m * 2048); \
;         else { _Pragma("unroll") for (int k = 0; k < 2; ++k) dst[m][k] = *(const LAS bf16x8*)(pa + PG8_SA(b, h) + m * 2048 + k * 1024); } } } while (0)
; #define PG8_LDB(dst, b, h) do { _Pragma("unroll") for (int n = 0; n < 2; ++n) { if constexpr (FP8) dst##8[n] = PG8_LD8(pb, PG8_SA(b, h) + n * 2048); \
;         else { _Pragma("unroll") for (int k = 0; k < 2; ++k) dst[n][k] = *(const LAS bf16x8*)(pb + PG8_SA(b, h) + n * 2048 + k * 1024); } } } while (0)
; #define PG8_BAR __builtin_amdgcn_s_barrier()
; template <class Epi, class Sched, bool PERM, bool FP8 = false, bool GATHER = false>
; DI void gemm_phase(LAS unsigned char* lds, const unsigned char* wsb, const unsigned lda, const unsigned ldb, const int nt, const Sched& S, const Epi& E) {
;     ...
;         for (int t = 0; t < nt; t += 2) {
;             const bool last = (t == nt - 2);
;             const unsigned b2 = last ? nB : cB + (unsigned)(t + 2) * kstep, b3 = b2 + kstep;
;             const int k2 = last ? 0 : t + 2, k3 = k2 + 1;
;             PG8_LDB(B0, 0, 0); PG8_LDB(B1, 0, 1); PG8_SCHED; PG8_LDA(At, 0, 0); PG8_STAGEA(PG8_SA(1, 1), t + 1, 1, false);
;             if constexpr (GATHER) { if (last) {
;                 int tz = tid; asm volatile("" : "+v"(tz));
; #pragma unroll
;                 for (int i = 0; i < 2; ++i) { int R, C; stage_rc(tz * 16 + i * 8192, R, C);
; #pragma unroll
;                     for (int h = 0; h < 2; ++h) { const unsigned tk = (unsigned)tokt[h * HALF + R]; offC[h][i] = (tk < (unsigned)NTOK ? tk : (unsigned)(NTOK - 1)) * lda + (unsigned)C * 2u; } } } }
;             PG8_WAIT_V(8); PG8_WAIT_L(0); PG8_BAR; PG8_MMA(0, 0, At, B0); PG8_MMA(0, 1, At, B1); PG8_BAR; PG8_SCHED;
;             PG8_LDA(At, 0, 1); PG8_STAGE(PG8_SB(0, 0), b2, voffB); PG8_STAGE(PG8_SB(0, 1), b2 + hstepB, voffB); PG8_STAGEA(PG8_SA(0, 0), k2, 0, last);
;             PG8_WAIT_V(8); PG8_WAIT_L(0); PG8_BAR; PG8_MMA(1, 0, At, B0); PG8_MMA(1, 1, At, B1); PG8_BAR; PG8_SCHED;
.LBB0_2116:
	s_add_i32 s75, s71, 0xfffe0080
	s_cmp_eq_u32 s73, 4
	s_cselect_b32 s74, s68, s72
	s_cselect_b32 s75, s67, s75
	s_add_i32 s76, s74, 0x80
	s_add_u32 s78, s8, s71
	s_addc_u32 s79, s9, 0
	s_mov_b32 m0, s60
	v_lshl_add_u64 v[162:163], s[78:79], 0, v[168:169]
	global_load_lds_dwordx4 v[162:163], off
	v_lshl_add_u64 v[162:163], s[78:79], 0, v[166:167]
	s_mov_b32 m0, s61
	s_nop 0
	global_load_lds_dwordx4 v[162:163], off
	ds_read_b128 v[130:133], v200
	ds_read_b128 v[134:137], v200 offset:1024
	ds_read_b128 v[138:141], v200 offset:2048
	ds_read_b128 v[142:145], v200 offset:3072
	ds_read_b128 v[146:149], v200 offset:16384
	ds_read_b128 v[150:153], v200 offset:17408
	ds_read_b128 v[154:157], v200 offset:18432
	ds_read_b128 v[158:161], v200 offset:19456
	ds_read_b128 v[170:173], v199
	ds_read_b128 v[174:177], v199 offset:1024
	ds_read_b128 v[178:181], v199 offset:2048
	ds_read_b128 v[182:185], v199 offset:3072
	ds_read_b128 v[186:189], v199 offset:4096
	ds_read_b128 v[190:193], v199 offset:5120
	ds_read_b128 v[202:205], v199 offset:6144
	ds_read_b128 v[206:209], v199 offset:7168
	s_waitcnt vmcnt(8)
	s_waitcnt lgkmcnt(0)
	s_barrier
	s_setprio 1
	s_waitcnt lgkmcnt(0)
	v_mfma_f32_16x16x128_f8f6f4 v[126:129], v[130:137], v[170:177], v[126:129]
	v_mfma_f32_16x16x128_f8f6f4 v[122:125], v[138:145], v[170:177], v[122:125]
	v_mfma_f32_16x16x128_f8f6f4 v[114:117], v[130:137], v[178:185], v[114:117]
	v_mfma_f32_16x16x128_f8f6f4 v[106:109], v[138:145], v[178:185], v[106:109]
	v_mfma_f32_16x16x128_f8f6f4 v[98:101], v[130:137], v[186:193], v[98:101]
	v_mfma_f32_16x16x128_f8f6f4 v[162:165], v[138:145], v[186:193], v[90:93]
	v_mfma_f32_16x16x128_f8f6f4 v[194:197], v[130:137], v[202:209], v[82:85]
	v_mfma_f32_16x16x128_f8f6f4 v[210:213], v[138:145], v[202:209], v[74:77]
	s_setprio 0
	s_setprio 1
	v_mfma_f32_16x16x128_f8f6f4 v[118:121], v[146:153], v[170:177], v[118:121]
	v_mfma_f32_16x16x128_f8f6f4 v[110:113], v[154:161], v[170:177], v[110:113]
	v_mfma_f32_16x16x128_f8f6f4 v[102:105], v[146:153], v[178:185], v[102:105]
	v_mfma_f32_16x16x128_f8f6f4 v[170:173], v[154:161], v[178:185], v[94:97]
	v_mfma_f32_16x16x128_f8f6f4 v[174:177], v[146:153], v[186:193], v[86:89]
	v_mfma_f32_16x16x128_f8f6f4 v[178:181], v[154:161], v[186:193], v[78:81]
	v_mfma_f32_16x16x128_f8f6f4 v[182:185], v[146:153], v[202:209], v[70:73]
	v_mfma_f32_16x16x128_f8f6f4 v[186:189], v[154:161], v[202:209], v[66:69]
	s_setprio 0
	s_barrier
	s_add_u32 s78, s8, s74
	s_addc_u32 s79, s9, 0
	s_mov_b32 m0, s28
	v_lshl_add_u64 v[190:191], s[78:79], 0, v[168:169]
	s_add_i32 s77, s74, 0x20000
	global_load_lds_dwordx4 v[190:191], off
	v_lshl_add_u64 v[190:191], s[78:79], 0, v[166:167]
	s_add_u32 s78, s8, s77
	s_mov_b32 m0, s29
	s_addc_u32 s79, s9, 0
	global_load_lds_dwordx4 v[190:191], off
	v_lshl_add_u64 v[190:191], s[78:79], 0, v[168:169]
	s_mov_b32 m0, s46
	s_nop 0
	global_load_lds_dwordx4 v[190:191], off
	v_lshl_add_u64 v[190:191], s[78:79], 0, v[166:167]
	s_add_u32 s78, s8, s75
	s_mov_b32 m0, s47
	s_addc_u32 s79, s9, 0
	global_load_lds_dwordx4 v[190:191], off
	v_lshl_add_u64 v[190:191], s[78:79], 0, v[168:169]
	s_mov_b32 m0, s21
	s_nop 0
	global_load_lds_dwordx4 v[190:191], off
	v_lshl_add_u64 v[190:191], s[78:79], 0, v[166:167]
	s_mov_b32 m0, s48
	s_nop 0
	global_load_lds_dwordx4 v[190:191], off
	ds_read_b128 v[66:69], v199 offset:16384
	ds_read_b128 v[70:73], v199 offset:17408
	ds_read_b128 v[74:77], v199 offset:18432
	ds_read_b128 v[78:81], v199 offset:19456
	ds_read_b128 v[82:85], v199 offset:20480
	ds_read_b128 v[86:89], v199 offset:21504
	ds_read_b128 v[90:93], v199 offset:22528
	ds_read_b128 v[94:97], v199 offset:23552
	s_waitcnt vmcnt(8)
	s_waitcnt lgkmcnt(0)
	s_barrier
	s_setprio 1
	s_waitcnt lgkmcnt(0)
	v_mfma_f32_16x16x128_f8f6f4 v[62:65], v[130:137], v[66:73], v[62:65]
	v_mfma_f32_16x16x128_f8f6f4 v[58:61], v[138:145], v[66:73], v[58:61]
	v_mfma_f32_16x16x128_f8f6f4 v[50:53], v[130:137], v[74:81], v[50:53]
	v_mfma_f32_16x16x128_f8f6f4 v[190:193], v[138:145], v[74:81], v[42:45]
	v_mfma_f32_16x16x128_f8f6f4 v[202:205], v[130:137], v[82:89], v[34:37]
	v_mfma_f32_16x16x128_f8f6f4 v[206:209], v[138:145], v[82:89], v[26:29]
	v_mfma_f32_16x16x128_f8f6f4 v[214:217], v[130:137], v[90:97], v[18:21]
	v_mfma_f32_16x16x128_f8f6f4 v[218:221], v[138:145], v[90:97], v[10:13]
	s_setprio 0
	s_setprio 1
	v_mfma_f32_16x16x128_f8f6f4 v[54:57], v[146:153], v[66:73], v[54:57]
	v_mfma_f32_16x16x128_f8f6f4 v[222:225], v[154:161], v[66:73], v[46:49]
	v_mfma_f32_16x16x128_f8f6f4 v[226:229], v[146:153], v[74:81], v[38:41]
	v_mfma_f32_16x16x128_f8f6f4 v[230:233], v[154:161], v[74:81], v[30:33]
	v_mfma_f32_16x16x128_f8f6f4 v[234:237], v[146:153], v[82:89], v[22:25]
	v_mfma_f32_16x16x128_f8f6f4 v[238:241], v[154:161], v[82:89], v[14:17]
	v_mfma_f32_16x16x128_f8f6f4 v[242:245], v[146:153], v[90:97], v[6:9]
	v_mfma_f32_16x16x128_f8f6f4 v[246:249], v[154:161], v[90:97], v[2:5]
	s_setprio 0
	s_barrier
; #define PG8_STAGE(bufoff, gbase, voff) do { _Pragma("unroll") for (int _i = 0; _i < 2; ++_i) \
;         __builtin_amdgcn_global_load_lds((const unsigned*)(wsb + (size_t)(gbase) + (voff)[_i]), (LAS unsigned*)(lds + (bufoff) + ldsw + _i * 8192), 16, 0, 0); } while (0)
; #define PG8_LDA(dst, b, h) do { _Pragma("unroll") for (int m = 0; m < 4; ++m) { if constexpr (FP8) dst##8[m] = PG8_LD8(pa, PG8_SA(b, h) + m * 2048); \
;         else { _Pragma("unroll") for (int k = 0; k < 2; ++k) dst[m][k] = *(const LAS bf16x8*)(pa + PG8_SA(b, h) + m * 2048 + k * 1024); } } } while (0)
; #define PG8_LDB(dst, b, h) do { _Pragma("unroll") for (int n = 0; n < 2; ++n) { if constexpr (FP8) dst##8[n] = PG8_LD8(pb, PG8_SA(b, h) + n * 2048); \
;         else { _Pragma("unroll") for (int k = 0; k < 2; ++k) dst[n][k] = *(const LAS bf16x8*)(pb + PG8_SA(b, h) + n * 2048 + k * 1024); } } } while (0)
; #define PG8_WAIT_V(n) asm volatile("s_waitcnt vmcnt(" #n ")" ::: "memory")
; #define PG8_WAIT_L(n) asm volatile("s_waitcnt lgkmcnt(" #n ")" ::: "memory")
; #define PG8_BAR __builtin_amdgcn_s_barrier()
; #define PG8_SCHED __builtin_amdgcn_sched_barrier(0)
; template <class Epi, class Sched, bool PERM, bool FP8 = false, bool GATHER = false>
; DI void gemm_phase(LAS unsigned char* lds, const unsigned char* wsb, const unsigned lda, const unsigned ldb, const int nt, const Sched& S, const Epi& E) {
;     ...
;             PG8_LDB(B0, 1, 0); PG8_LDB(B1, 1, 1); PG8_SCHED; PG8_LDA(At, 1, 0); PG8_STAGEA(PG8_SA(0, 1), k2, 1, last);
;             PG8_WAIT_V(8); PG8_WAIT_L(0); PG8_BAR; PG8_MMA(0, 0, At, B0); PG8_MMA(0, 1, At, B1); PG8_BAR; PG8_SCHED;
;             PG8_LDA(At, 1, 1); PG8_STAGE(PG8_SB(1, 0), b3, voffB); PG8_STAGE(PG8_SB(1, 1), b3 + hstepB, voffB); PG8_STAGEA(PG8_SA(1, 0), k3, 0, last);
;             PG8_WAIT_V(8); PG8_WAIT_L(0); PG8_BAR; PG8_MMA(1, 0, At, B0); PG8_MMA(1, 1, At, B1); PG8_BAR; PG8_SCHED;
;         }
;         if (wr == 0) PG8_BAR;
	s_nop 4
	s_add_i32 s77, s75, 0x20000
	s_add_u32 s78, s8, s77
	s_addc_u32 s79, s9, 0
	s_mov_b32 m0, s49
	v_lshl_add_u64 v[66:67], s[78:79], 0, v[168:169]
	global_load_lds_dwordx4 v[66:67], off
	v_lshl_add_u64 v[66:67], s[78:79], 0, v[166:167]
	s_mov_b32 m0, s50
	s_nop 0
	global_load_lds_dwordx4 v[66:67], off
	ds_read_b128 v[2:5], v200 offset:32768
	ds_read_b128 v[6:9], v200 offset:33792
	ds_read_b128 v[10:13], v200 offset:34816
	ds_read_b128 v[14:17], v200 offset:35840
	ds_read_b128 v[130:133], v200 offset:49152
	ds_read_b128 v[134:137], v200 offset:50176
	ds_read_b128 v[138:141], v200 offset:51200
	ds_read_b128 v[142:145], v200 offset:52224
	ds_read_b128 v[18:21], v199 offset:32768
	ds_read_b128 v[22:25], v199 offset:33792
	ds_read_b128 v[26:29], v199 offset:34816
	ds_read_b128 v[30:33], v199 offset:35840
	ds_read_b128 v[34:37], v199 offset:36864
	ds_read_b128 v[38:41], v199 offset:37888
	ds_read_b128 v[42:45], v199 offset:38912
	ds_read_b128 v[46:49], v199 offset:39936
	s_waitcnt vmcnt(8)
	s_waitcnt lgkmcnt(0)
	s_barrier
	s_setprio 1
	s_waitcnt lgkmcnt(0)
	v_mfma_f32_16x16x128_f8f6f4 v[126:129], v[2:9], v[18:25], v[126:129]
	v_mfma_f32_16x16x128_f8f6f4 v[122:125], v[10:17], v[18:25], v[122:125]
	v_mfma_f32_16x16x128_f8f6f4 v[114:117], v[2:9], v[26:33], v[114:117]
	v_mfma_f32_16x16x128_f8f6f4 v[106:109], v[10:17], v[26:33], v[106:109]
	v_mfma_f32_16x16x128_f8f6f4 v[98:101], v[2:9], v[34:41], v[98:101]
	v_mfma_f32_16x16x128_f8f6f4 v[90:93], v[10:17], v[34:41], v[162:165]
	v_mfma_f32_16x16x128_f8f6f4 v[82:85], v[2:9], v[42:49], v[194:197]
	v_mfma_f32_16x16x128_f8f6f4 v[74:77], v[10:17], v[42:49], v[210:213]
	s_setprio 0
	s_setprio 1
	v_mfma_f32_16x16x128_f8f6f4 v[118:121], v[130:137], v[18:25], v[118:121]
	v_mfma_f32_16x16x128_f8f6f4 v[110:113], v[138:145], v[18:25], v[110:113]
	v_mfma_f32_16x16x128_f8f6f4 v[102:105], v[130:137], v[26:33], v[102:105]
	v_mfma_f32_16x16x128_f8f6f4 v[94:97], v[138:145], v[26:33], v[170:173]
	v_mfma_f32_16x16x128_f8f6f4 v[86:89], v[130:137], v[34:41], v[174:177]
	v_mfma_f32_16x16x128_f8f6f4 v[78:81], v[138:145], v[34:41], v[178:181]
	v_mfma_f32_16x16x128_f8f6f4 v[70:73], v[130:137], v[42:49], v[182:185]
	v_mfma_f32_16x16x128_f8f6f4 v[66:69], v[138:145], v[42:49], v[186:189]
	s_setprio 0
	s_barrier
	s_add_u32 s76, s8, s76
	s_addc_u32 s77, s9, 0
	s_mov_b32 m0, s52
	v_lshl_add_u64 v[18:19], s[76:77], 0, v[168:169]
	s_add_i32 s74, s74, 0x20080
	global_load_lds_dwordx4 v[18:19], off
	v_lshl_add_u64 v[18:19], s[76:77], 0, v[166:167]
	s_add_u32 s76, s8, s74
	s_mov_b32 m0, s53
	s_addc_u32 s77, s9, 0
	s_addk_i32 s75, 0x80
	global_load_lds_dwordx4 v[18:19], off
	v_lshl_add_u64 v[18:19], s[76:77], 0, v[168:169]
	s_mov_b32 m0, s56
	s_add_u32 s74, s8, s75
	global_load_lds_dwordx4 v[18:19], off
	v_lshl_add_u64 v[18:19], s[76:77], 0, v[166:167]
	s_mov_b32 m0, s57
	s_addc_u32 s75, s9, 0
	global_load_lds_dwordx4 v[18:19], off
	v_lshl_add_u64 v[18:19], s[74:75], 0, v[168:169]
	s_mov_b32 m0, s54
	s_nop 0
	global_load_lds_dwordx4 v[18:19], off
	v_lshl_add_u64 v[18:19], s[74:75], 0, v[166:167]
	s_mov_b32 m0, s55
	s_nop 0
	global_load_lds_dwordx4 v[18:19], off
	ds_read_b128 v[146:149], v199 offset:49152
	ds_read_b128 v[150:153], v199 offset:50176
	ds_read_b128 v[154:157], v199 offset:51200
	ds_read_b128 v[158:161], v199 offset:52224
	ds_read_b128 v[170:173], v199 offset:53248
	ds_read_b128 v[174:177], v199 offset:54272
	ds_read_b128 v[178:181], v199 offset:55296
	ds_read_b128 v[182:185], v199 offset:56320
	s_waitcnt vmcnt(8)
	s_waitcnt lgkmcnt(0)
	s_barrier
	s_setprio 1
	s_waitcnt lgkmcnt(0)
	v_mfma_f32_16x16x128_f8f6f4 v[62:65], v[2:9], v[146:153], v[62:65]
	v_mfma_f32_16x16x128_f8f6f4 v[58:61], v[10:17], v[146:153], v[58:61]
	v_mfma_f32_16x16x128_f8f6f4 v[50:53], v[2:9], v[154:161], v[50:53]
	v_mfma_f32_16x16x128_f8f6f4 v[42:45], v[10:17], v[154:161], v[190:193]
	v_mfma_f32_16x16x128_f8f6f4 v[34:37], v[2:9], v[170:177], v[202:205]
	v_mfma_f32_16x16x128_f8f6f4 v[26:29], v[10:17], v[170:177], v[206:209]
	v_mfma_f32_16x16x128_f8f6f4 v[18:21], v[2:9], v[178:185], v[214:217]
	v_mfma_f32_16x16x128_f8f6f4 v[10:13], v[10:17], v[178:185], v[218:221]
	s_setprio 0
	s_setprio 1
	v_mfma_f32_16x16x128_f8f6f4 v[54:57], v[130:137], v[146:153], v[54:57]
	v_mfma_f32_16x16x128_f8f6f4 v[46:49], v[138:145], v[146:153], v[222:225]
	v_mfma_f32_16x16x128_f8f6f4 v[38:41], v[130:137], v[154:161], v[226:229]
	v_mfma_f32_16x16x128_f8f6f4 v[30:33], v[138:145], v[154:161], v[230:233]
	v_mfma_f32_16x16x128_f8f6f4 v[22:25], v[130:137], v[170:177], v[234:237]
	v_mfma_f32_16x16x128_f8f6f4 v[14:17], v[138:145], v[170:177], v[238:241]
	v_mfma_f32_16x16x128_f8f6f4 v[6:9], v[130:137], v[178:185], v[242:245]
	v_mfma_f32_16x16x128_f8f6f4 v[2:5], v[138:145], v[178:185], v[246:249]
	s_setprio 0
	s_barrier
	s_add_i32 s73, s73, 2
	s_addk_i32 s71, 0x100
	s_addk_i32 s72, 0x100
	s_cmp_gt_u32 s73, 5
	s_cbranch_scc0 .LBB0_2116
	s_and_b64 vcc, exec, s[12:13]
	s_cbranch_vccz .LBB0_2119
	s_barrier

; #define PG8_STAGE(bufoff, gbase, voff) do { _Pragma("unroll") for (int _i = 0; _i < 2; ++_i) \
;         __builtin_amdgcn_global_load_lds((const unsigned*)(wsb + (size_t)(gbase) + (voff)[_i]), (LAS unsigned*)(lds + (bufoff) + ldsw + _i * 8192), 16, 0, 0); } while (0)
; #define PG8_LDA(dst, b, h) do { _Pragma("unroll") for (int m = 0; m < 4; ++m) { if constexpr (FP8) dst##8[m] = PG8_LD8(pa, PG8_SA(b, h) + m * 2048); \
;         else { _Pragma("unroll") for (int k = 0; k < 2; ++k) dst[m][k] = *(const LAS bf16x8*)(pa + PG8_SA(b, h) + m * 2048 + k * 1024); } } } while (0)
; #define PG8_LDB(dst, b, h) do { _Pragma("unroll") for (int n = 0; n < 2; ++n) { if constexpr (FP8) dst##8[n] = PG8_LD8(pb, PG8_SA(b, h) + n * 2048); \
;         else { _Pragma("unroll") for (int k = 0; k < 2; ++k) dst[n][k] = *(const LAS bf16x8*)(pb + PG8_SA(b, h) + n * 2048 + k * 1024); } } } while (0)
; #define PG8_WAIT_V(n) asm volatile("s_waitcnt vmcnt(" #n ")" ::: "memory")
; #define PG8_WAIT_L(n) asm volatile("s_waitcnt lgkmcnt(" #n ")" ::: "memory")
; #define PG8_BAR __builtin_amdgcn_s_barrier()
; #define PG8_SCHED __builtin_amdgcn_sched_barrier(0)
; template <class Epi, class Sched, bool PERM, bool FP8 = false, bool GATHER = false>
; DI void gemm_phase(LAS unsigned char* lds, const unsigned char* wsb, const unsigned lda, const unsigned ldb, const int nt, const Sched& S, const Epi& E) {
;     ...
;             PG8_WAIT_V(8); PG8_WAIT_L(0); PG8_BAR; PG8_MMA(0, 0, At, B0); PG8_MMA(0, 1, At, B1); PG8_BAR; PG8_SCHED;
;             PG8_LDA(At, 0, 1); PG8_STAGE(PG8_SB(0, 0), b2, voffB); PG8_STAGE(PG8_SB(0, 1), b2 + hstepB, voffB); PG8_STAGEA(PG8_SA(0, 0), k2, 0, last);
;             PG8_WAIT_V(8); PG8_WAIT_L(0); PG8_BAR; PG8_MMA(1, 0, At, B0); PG8_MMA(1, 1, At, B1); PG8_BAR; PG8_SCHED;
;             PG8_LDB(B0, 1, 0); PG8_LDB(B1, 1, 1); PG8_SCHED; PG8_LDA(At, 1, 0); PG8_STAGEA(PG8_SA(0, 1), k2, 1, last);
;             PG8_WAIT_V(8); PG8_WAIT_L(0); PG8_BAR; PG8_MMA(0, 0, At, B0); PG8_MMA(0, 1, At, B1); PG8_BAR; PG8_SCHED;
.LBB0_2544:
	s_waitcnt vmcnt(8)
	s_add_i32 s84, s80, s44
	s_waitcnt lgkmcnt(0)
	s_and_b64 s[82:83], s[46:47], exec
	s_cselect_b32 s82, s12, s84
	v_mov_b32_e32 v205, v197
	s_add_i32 s83, s82, 0x80
	s_barrier
	s_setprio 1
	s_waitcnt lgkmcnt(0)
	v_mfma_f32_16x16x128_f8f6f4 v[190:193], v[18:25], v[58:65], v[190:193]
	v_mfma_f32_16x16x128_f8f6f4 v[186:189], v[26:33], v[58:65], v[186:189]
	v_mfma_f32_16x16x128_f8f6f4 v[174:177], v[18:25], v[50:57], v[174:177]
	v_mfma_f32_16x16x128_f8f6f4 v[166:169], v[26:33], v[50:57], v[166:169]
	v_mfma_f32_16x16x128_f8f6f4 v[158:161], v[18:25], v[42:49], v[158:161]
	v_mfma_f32_16x16x128_f8f6f4 v[150:153], v[26:33], v[42:49], v[150:153]
	v_mfma_f32_16x16x128_f8f6f4 v[142:145], v[18:25], v[34:41], v[142:145]
	v_mfma_f32_16x16x128_f8f6f4 v[134:137], v[26:33], v[34:41], v[134:137]
	s_setprio 0
	s_setprio 1
	v_mfma_f32_16x16x128_f8f6f4 v[182:185], v[2:9], v[58:65], v[182:185]
	v_mfma_f32_16x16x128_f8f6f4 v[178:181], v[10:17], v[58:65], v[178:181]
	v_mfma_f32_16x16x128_f8f6f4 v[170:173], v[2:9], v[50:57], v[170:173]
	v_mfma_f32_16x16x128_f8f6f4 v[162:165], v[10:17], v[50:57], v[162:165]
	v_mfma_f32_16x16x128_f8f6f4 v[154:157], v[2:9], v[42:49], v[154:157]
	v_mfma_f32_16x16x128_f8f6f4 v[146:149], v[10:17], v[42:49], v[146:149]
	v_mfma_f32_16x16x128_f8f6f4 v[138:141], v[2:9], v[34:41], v[138:141]
	v_mfma_f32_16x16x128_f8f6f4 v[130:133], v[10:17], v[34:41], v[130:133]
	s_setprio 0
	s_barrier
	s_add_u32 s84, s8, s82
	s_addc_u32 s85, s9, 0
	s_mov_b32 m0, s48
	v_lshl_add_u64 v[214:215], s[84:85], 0, v[198:199]
	global_load_lds_dwordx4 v[214:215], off
	v_lshl_add_u64 v[214:215], s[84:85], 0, v[200:201]
	s_add_i32 s84, s82, 0x20000
	s_add_u32 s84, s8, s84
	s_addc_u32 s85, s9, 0
	s_add_u32 s44, s44, 0x100
	s_mov_b32 m0, s49
	s_addc_u32 s45, s45, 0
	global_load_lds_dwordx4 v[214:215], off
	v_lshl_add_u64 v[214:215], s[84:85], 0, v[198:199]
	s_mov_b32 m0, s50
	s_and_b64 s[46:47], s[46:47], exec
	global_load_lds_dwordx4 v[214:215], off
	v_lshl_add_u64 v[214:215], s[84:85], 0, v[200:201]
	s_cselect_b32 s84, 0, s44
	s_mov_b32 m0, s51
	s_add_u32 s46, s10, s84
	global_load_lds_dwordx4 v[214:215], off
	s_addc_u32 s47, s11, 0
	s_mov_b32 m0, s39
	s_nop 0
	global_load_lds_dwordx4 v212, s[46:47]
	s_mov_b32 m0, s52
	s_nop 0
	global_load_lds_dwordx4 v202, s[46:47]
	ds_read_b128 v[34:37], v209 offset:16384
	ds_read_b128 v[38:41], v209 offset:17408
	ds_read_b128 v[42:45], v209 offset:18432
	ds_read_b128 v[46:49], v209 offset:19456
	ds_read_b128 v[50:53], v209 offset:20480
	ds_read_b128 v[54:57], v209 offset:21504
	ds_read_b128 v[58:61], v209 offset:22528
	ds_read_b128 v[62:65], v209 offset:23552
	s_waitcnt vmcnt(8)
	s_waitcnt lgkmcnt(0)
	s_barrier
	s_setprio 1
	s_waitcnt lgkmcnt(0)
	v_mfma_f32_16x16x128_f8f6f4 v[126:129], v[18:25], v[34:41], v[126:129]
	v_mfma_f32_16x16x128_f8f6f4 v[118:121], v[26:33], v[34:41], v[118:121]
	v_mfma_f32_16x16x128_f8f6f4 v[110:113], v[18:25], v[42:49], v[110:113]
	v_mfma_f32_16x16x128_f8f6f4 v[102:105], v[26:33], v[42:49], v[102:105]
	v_mfma_f32_16x16x128_f8f6f4 v[94:97], v[18:25], v[50:57], v[94:97]
	v_mfma_f32_16x16x128_f8f6f4 v[86:89], v[26:33], v[50:57], v[86:89]
	v_mfma_f32_16x16x128_f8f6f4 v[78:81], v[18:25], v[58:65], v[78:81]
	v_mfma_f32_16x16x128_f8f6f4 v[70:73], v[26:33], v[58:65], v[70:73]
	s_setprio 0
	s_setprio 1
	v_mfma_f32_16x16x128_f8f6f4 v[122:125], v[2:9], v[34:41], v[122:125]
	v_mfma_f32_16x16x128_f8f6f4 v[114:117], v[10:17], v[34:41], v[114:117]
	v_mfma_f32_16x16x128_f8f6f4 v[106:109], v[2:9], v[42:49], v[106:109]
	v_mfma_f32_16x16x128_f8f6f4 v[98:101], v[10:17], v[42:49], v[98:101]
	v_mfma_f32_16x16x128_f8f6f4 v[90:93], v[2:9], v[50:57], v[90:93]
	v_mfma_f32_16x16x128_f8f6f4 v[82:85], v[10:17], v[50:57], v[82:85]
	v_mfma_f32_16x16x128_f8f6f4 v[74:77], v[2:9], v[58:65], v[74:77]
	v_mfma_f32_16x16x128_f8f6f4 v[66:69], v[10:17], v[58:65], v[66:69]
	s_setprio 0
	s_barrier
	s_mov_b32 m0, s53
	v_lshl_add_u64 v[214:215], s[46:47], 0, v[196:197]
	global_load_lds_dwordx4 v[214:215], off
	v_lshl_add_u64 v[214:215], s[46:47], 0, v[204:205]
	s_mov_b32 m0, s54
	s_nop 0
	global_load_lds_dwordx4 v[214:215], off
	ds_read_b128 v[2:5], v210 offset:32768
	ds_read_b128 v[6:9], v210 offset:33792
	ds_read_b128 v[10:13], v210 offset:34816
	ds_read_b128 v[14:17], v210 offset:35840
	ds_read_b128 v[18:21], v210 offset:49152
	ds_read_b128 v[22:25], v210 offset:50176
	ds_read_b128 v[26:29], v210 offset:51200
	ds_read_b128 v[30:33], v210 offset:52224
	ds_read_b128 v[34:37], v209 offset:32768
	ds_read_b128 v[38:41], v209 offset:33792
	ds_read_b128 v[42:45], v209 offset:34816
	ds_read_b128 v[46:49], v209 offset:35840
	ds_read_b128 v[50:53], v209 offset:36864
	ds_read_b128 v[54:57], v209 offset:37888
	ds_read_b128 v[58:61], v209 offset:38912
	ds_read_b128 v[62:65], v209 offset:39936
	s_waitcnt vmcnt(8)
	s_waitcnt lgkmcnt(0)
	s_barrier
	s_setprio 1
	s_waitcnt lgkmcnt(0)
	v_mfma_f32_16x16x128_f8f6f4 v[190:193], v[2:9], v[34:41], v[190:193]
	v_mfma_f32_16x16x128_f8f6f4 v[186:189], v[10:17], v[34:41], v[186:189]
	v_mfma_f32_16x16x128_f8f6f4 v[174:177], v[2:9], v[42:49], v[174:177]
	v_mfma_f32_16x16x128_f8f6f4 v[166:169], v[10:17], v[42:49], v[166:169]
	v_mfma_f32_16x16x128_f8f6f4 v[158:161], v[2:9], v[50:57], v[158:161]
	v_mfma_f32_16x16x128_f8f6f4 v[150:153], v[10:17], v[50:57], v[150:153]
	v_mfma_f32_16x16x128_f8f6f4 v[142:145], v[2:9], v[58:65], v[142:145]
	v_mfma_f32_16x16x128_f8f6f4 v[134:137], v[10:17], v[58:65], v[134:137]
	s_setprio 0
	s_setprio 1
	v_mfma_f32_16x16x128_f8f6f4 v[182:185], v[18:25], v[34:41], v[182:185]
	v_mfma_f32_16x16x128_f8f6f4 v[178:181], v[26:33], v[34:41], v[178:181]
	v_mfma_f32_16x16x128_f8f6f4 v[170:173], v[18:25], v[42:49], v[170:173]
	v_mfma_f32_16x16x128_f8f6f4 v[162:165], v[26:33], v[42:49], v[162:165]
	v_mfma_f32_16x16x128_f8f6f4 v[154:157], v[18:25], v[50:57], v[154:157]
	v_mfma_f32_16x16x128_f8f6f4 v[146:149], v[26:33], v[50:57], v[146:149]
	v_mfma_f32_16x16x128_f8f6f4 v[138:141], v[18:25], v[58:65], v[138:141]
	v_mfma_f32_16x16x128_f8f6f4 v[130:133], v[26:33], v[58:65], v[130:133]
	s_setprio 0
	s_barrier
; #define PG8_STAGE(bufoff, gbase, voff) do { _Pragma("unroll") for (int _i = 0; _i < 2; ++_i) \
;         __builtin_amdgcn_global_load_lds((const unsigned*)(wsb + (size_t)(gbase) + (voff)[_i]), (LAS unsigned*)(lds + (bufoff) + ldsw + _i * 8192), 16, 0, 0); } while (0)
; #define PG8_LDA(dst, b, h) do { _Pragma("unroll") for (int m = 0; m < 4; ++m) { if constexpr (FP8) dst##8[m] = PG8_LD8(pa, PG8_SA(b, h) + m * 2048); \
;         else { _Pragma("unroll") for (int k = 0; k < 2; ++k) dst[m][k] = *(const LAS bf16x8*)(pa + PG8_SA(b, h) + m * 2048 + k * 1024); } } } while (0)
; #define PG8_LDB(dst, b, h) do { _Pragma("unroll") for (int n = 0; n < 2; ++n) { if constexpr (FP8) dst##8[n] = PG8_LD8(pb, PG8_SA(b, h) + n * 2048); \
;         else { _Pragma("unroll") for (int k = 0; k < 2; ++k) dst[n][k] = *(const LAS bf16x8*)(pb + PG8_SA(b, h) + n * 2048 + k * 1024); } } } while (0)
; #define PG8_WAIT_V(n) asm volatile("s_waitcnt vmcnt(" #n ")" ::: "memory")
; #define PG8_WAIT_L(n) asm volatile("s_waitcnt lgkmcnt(" #n ")" ::: "memory")
; template <class Epi, class Sched, bool PERM, bool FP8 = false, bool GATHER = false>
; DI void gemm_phase(LAS unsigned char* lds, const unsigned char* wsb, const unsigned lda, const unsigned ldb, const int nt, const Sched& S, const Epi& E) {
;     ...
;         for (int t = 0; t < nt; t += 2) {
;             const bool last = (t == nt - 2);
;             const unsigned b2 = last ? nB : cB + (unsigned)(t + 2) * kstep, b3 = b2 + kstep;
;             const int k2 = last ? 0 : t + 2, k3 = k2 + 1;
;             PG8_LDB(B0, 0, 0); PG8_LDB(B1, 0, 1); PG8_SCHED; PG8_LDA(At, 0, 0); PG8_STAGEA(PG8_SA(1, 1), t + 1, 1, false);
;             if constexpr (GATHER) { if (last) {
;                 int tz = tid; asm volatile("" : "+v"(tz));
; #pragma unroll
;                 for (int i = 0; i < 2; ++i) { int R, C; stage_rc(tz * 16 + i * 8192, R, C);
; #pragma unroll
;                     for (int h = 0; h < 2; ++h) { const unsigned tk = (unsigned)tokt[h * HALF + R]; offC[h][i] = (tk < (unsigned)NTOK ? tk : (unsigned)(NTOK - 1)) * lda + (unsigned)C * 2u; } } } }
;     ...
;             PG8_LDA(At, 1, 1); PG8_STAGE(PG8_SB(1, 0), b3, voffB); PG8_STAGE(PG8_SB(1, 1), b3 + hstepB, voffB); PG8_STAGEA(PG8_SA(1, 0), k3, 0, last);
;             PG8_WAIT_V(8); PG8_WAIT_L(0); PG8_BAR; PG8_MMA(1, 0, At, B0); PG8_MMA(1, 1, At, B1); PG8_BAR; PG8_SCHED;
	s_add_u32 s46, s8, s83
	s_addc_u32 s47, s9, 0
	s_mov_b32 m0, s58
	v_lshl_add_u64 v[214:215], s[46:47], 0, v[198:199]
	s_add_i32 s82, s82, 0x20080
	global_load_lds_dwordx4 v[214:215], off
	v_lshl_add_u64 v[214:215], s[46:47], 0, v[200:201]
	s_add_u32 s46, s8, s82
	s_mov_b32 m0, s59
	s_addc_u32 s47, s9, 0
	global_load_lds_dwordx4 v[214:215], off
	v_lshl_add_u64 v[214:215], s[46:47], 0, v[198:199]
	s_mov_b32 m0, s64
	s_nop 0
	global_load_lds_dwordx4 v[214:215], off
	v_lshl_add_u64 v[214:215], s[46:47], 0, v[200:201]
	s_add_u32 s46, s8, s84
	s_addc_u32 s47, s9, 0
	s_mov_b32 m0, s65
	s_add_u32 s46, s46, 0x5b9d4080
	global_load_lds_dwordx4 v[214:215], off
	s_addc_u32 s47, s47, 0
	s_mov_b32 m0, s60
	s_nop 0
	global_load_lds_dwordx4 v212, s[46:47]
	s_mov_b32 m0, s61
	s_nop 0
	global_load_lds_dwordx4 v202, s[46:47]
	ds_read_b128 v[34:37], v209 offset:49152
	ds_read_b128 v[38:41], v209 offset:50176
	ds_read_b128 v[42:45], v209 offset:51200
	ds_read_b128 v[46:49], v209 offset:52224
	ds_read_b128 v[50:53], v209 offset:53248
	ds_read_b128 v[54:57], v209 offset:54272
	ds_read_b128 v[58:61], v209 offset:55296
	ds_read_b128 v[62:65], v209 offset:56320
	s_waitcnt vmcnt(8)
	s_waitcnt lgkmcnt(0)
	s_barrier
	s_setprio 1
	s_waitcnt lgkmcnt(0)
	v_mfma_f32_16x16x128_f8f6f4 v[126:129], v[2:9], v[34:41], v[126:129]
	v_mfma_f32_16x16x128_f8f6f4 v[118:121], v[10:17], v[34:41], v[118:121]
	v_mfma_f32_16x16x128_f8f6f4 v[110:113], v[2:9], v[42:49], v[110:113]
	v_mfma_f32_16x16x128_f8f6f4 v[102:105], v[10:17], v[42:49], v[102:105]
	v_mfma_f32_16x16x128_f8f6f4 v[94:97], v[2:9], v[50:57], v[94:97]
	v_mfma_f32_16x16x128_f8f6f4 v[86:89], v[10:17], v[50:57], v[86:89]
	v_mfma_f32_16x16x128_f8f6f4 v[78:81], v[2:9], v[58:65], v[78:81]
	v_mfma_f32_16x16x128_f8f6f4 v[70:73], v[10:17], v[58:65], v[70:73]
	s_setprio 0
	s_setprio 1
	v_mfma_f32_16x16x128_f8f6f4 v[122:125], v[18:25], v[34:41], v[122:125]
	v_mfma_f32_16x16x128_f8f6f4 v[114:117], v[26:33], v[34:41], v[114:117]
	v_mfma_f32_16x16x128_f8f6f4 v[106:109], v[18:25], v[42:49], v[106:109]
	v_mfma_f32_16x16x128_f8f6f4 v[98:101], v[26:33], v[42:49], v[98:101]
	v_mfma_f32_16x16x128_f8f6f4 v[90:93], v[18:25], v[50:57], v[90:93]
	v_mfma_f32_16x16x128_f8f6f4 v[82:85], v[26:33], v[50:57], v[82:85]
	v_mfma_f32_16x16x128_f8f6f4 v[74:77], v[18:25], v[58:65], v[74:77]
	v_mfma_f32_16x16x128_f8f6f4 v[66:69], v[26:33], v[58:65], v[66:69]
	s_setprio 0
	s_barrier
	s_add_i32 s81, s81, 2
	s_cmp_gt_u32 s81, 5
	s_cbranch_scc1 .LBB0_2547
.LBB0_2545:
	s_cmp_eq_u32 s81, 4
	s_cselect_b64 s[46:47], -1, 0
	s_add_i32 m0, s39, 0xc000
	s_add_u32 s82, s16, s44
	s_addc_u32 s83, s17, s45
	s_add_i32 s84, s39, 0xe000
	s_cmp_lg_u32 s81, 4
	global_load_lds_dwordx4 v196, s[82:83]
	s_mov_b32 m0, s84
	s_nop 0
	global_load_lds_dwordx4 v204, s[82:83]
	ds_read_b128 v[18:21], v210
	ds_read_b128 v[22:25], v210 offset:1024
	ds_read_b128 v[26:29], v210 offset:2048
	ds_read_b128 v[30:33], v210 offset:3072
	ds_read_b128 v[2:5], v210 offset:16384
	ds_read_b128 v[6:9], v210 offset:17408
	ds_read_b128 v[10:13], v210 offset:18432
	ds_read_b128 v[14:17], v210 offset:19456
	ds_read_b128 v[58:61], v209
	ds_read_b128 v[62:65], v209 offset:1024
	ds_read_b128 v[50:53], v209 offset:2048
	ds_read_b128 v[54:57], v209 offset:3072
	ds_read_b128 v[42:45], v209 offset:4096
	ds_read_b128 v[46:49], v209 offset:5120
	ds_read_b128 v[34:37], v209 offset:6144
	ds_read_b128 v[38:41], v209 offset:7168
	s_cbranch_scc1 .LBB0_2544
	v_mov_b32_e32 v196, v194
	s_add_i32 s82, 0, 0x20c00
	v_ashrrev_i32_e32 v204, 31, v196
	v_lshrrev_b32_e32 v204, 26, v204
	v_lshlrev_b32_e32 v202, 4, v196
	v_add_u32_e32 v204, v196, v204
	v_bfe_i32 v196, v196, 27, 1
	v_lshrrev_b32_e32 v196, 22, v196
	v_add_u32_e32 v196, v202, v196
	v_and_b32_e32 v196, 0xfffffc00, v196
	v_sub_u32_e32 v196, v202, v196
	v_lshrrev_b32_e32 v205, 4, v196
	v_bitop3_b32 v196, v205, v196, 32 bitop3:0x6c
	v_ashrrev_i32_e32 v205, 31, v196
	v_lshrrev_b32_e32 v205, 26, v205
	v_ashrrev_i32_e32 v204, 6, v204
	v_add_u32_e32 v205, v196, v205
	v_ashrrev_i32_e32 v212, 6, v205
	v_lshlrev_b32_e32 v204, 5, v204
	v_and_b32_e32 v213, 32, v204
	v_and_b32_e32 v214, 0xc0, v205
	v_lshlrev_b32_e32 v205, 2, v212
	v_and_b32_e32 v204, 0xffffffc0, v204
	v_add3_u32 v204, s82, v205, v204
	ds_read2st64_b32 v[204:205], v204 offset1:2
	v_sub_u32_e32 v196, v196, v214
	v_ashrrev_i16_sdwa v196, v211, sext(v196) dst_sel:DWORD dst_unused:UNUSED_PAD src0_sel:DWORD src1_sel:BYTE_0
	v_bfe_i32 v196, v196, 0, 16
	v_add_lshl_u32 v196, v213, v196, 1
	s_waitcnt lgkmcnt(0)
	v_min_u32_e32 v204, 0x87ff, v204
	v_lshl_add_u32 v212, v204, 10, v196
	v_min_u32_e32 v204, 0x87ff, v205
	v_add_u32_e32 v202, 0x2000, v202
	v_lshl_add_u32 v196, v204, 10, v196
	v_ashrrev_i32_e32 v204, 31, v202
	v_lshrrev_b32_e32 v204, 22, v204
	v_add_u32_e32 v204, v202, v204
	v_ashrrev_i32_e32 v204, 10, v204
	v_mul_i32_i24_e32 v205, 0x400, v204
	v_sub_u32_e32 v202, v202, v205
	v_lshrrev_b32_e32 v205, 4, v202
	v_bitop3_b32 v202, v205, v202, 32 bitop3:0x6c
	v_ashrrev_i32_e32 v205, 31, v202
	v_lshrrev_b32_e32 v205, 26, v205
	v_add_u32_e32 v205, v202, v205
	v_ashrrev_i32_e32 v213, 6, v205
	v_lshlrev_b32_e32 v204, 5, v204
	v_and_b32_e32 v214, 32, v204
	v_and_b32_e32 v215, 0xc0, v205
	v_lshlrev_b32_e32 v205, 2, v213
	v_and_b32_e32 v204, 0xffffffc0, v204
	v_add3_u32 v204, s82, v205, v204
	ds_read2st64_b32 v[204:205], v204 offset1:2
	v_sub_u32_e32 v202, v202, v215
	v_ashrrev_i16_sdwa v202, v211, sext(v202) dst_sel:DWORD dst_unused:UNUSED_PAD src0_sel:DWORD src1_sel:BYTE_0
	v_bfe_i32 v202, v202, 0, 16
	v_add_lshl_u32 v213, v214, v202, 1
	s_waitcnt lgkmcnt(0)
	v_min_u32_e32 v202, 0x87ff, v204
	v_min_u32_e32 v204, 0x87ff, v205
	v_lshl_add_u32 v202, v202, 10, v213
	v_lshl_add_u32 v204, v204, 10, v213
	s_branch .LBB0_2544

; #define PG8_STAGE(bufoff, gbase, voff) do { _Pragma("unroll") for (int _i = 0; _i < 2; ++_i) \
;         __builtin_amdgcn_global_load_lds((const unsigned*)(wsb + (size_t)(gbase) + (voff)[_i]), (LAS unsigned*)(lds + (bufoff) + ldsw + _i * 8192), 16, 0, 0); } while (0)
; #define PG8_LDA(dst, b, h) do { _Pragma("unroll") for (int m = 0; m < 4; ++m) { if constexpr (FP8) dst##8[m] = PG8_LD8(pa, PG8_SA(b, h) + m * 2048); \
;         else { _Pragma("unroll") for (int k = 0; k < 2; ++k) dst[m][k] = *(const LAS bf16x8*)(pa + PG8_SA(b, h) + m * 2048 + k * 1024); } } } while (0)
; #define PG8_LDB(dst, b, h) do { _Pragma("unroll") for (int n = 0; n < 2; ++n) { if constexpr (FP8) dst##8[n] = PG8_LD8(pb, PG8_SA(b, h) + n * 2048); \
;         else { _Pragma("unroll") for (int k = 0; k < 2; ++k) dst[n][k] = *(const LAS bf16x8*)(pb + PG8_SA(b, h) + n * 2048 + k * 1024); } } } while (0)
; #define PG8_BAR __builtin_amdgcn_s_barrier()
; template <class Epi, class Sched, bool PERM, bool FP8 = false, bool GATHER = false>
; DI void gemm_phase(LAS unsigned char* lds, const unsigned char* wsb, const unsigned lda, const unsigned ldb, const int nt, const Sched& S, const Epi& E) {
;     ...
;         for (int t = 0; t < nt; t += 2) {
;             const bool last = (t == nt - 2);
;             const unsigned b2 = last ? nB : cB + (unsigned)(t + 2) * kstep, b3 = b2 + kstep;
;             const int k2 = last ? 0 : t + 2, k3 = k2 + 1;
;             PG8_LDB(B0, 0, 0); PG8_LDB(B1, 0, 1); PG8_SCHED; PG8_LDA(At, 0, 0); PG8_STAGEA(PG8_SA(1, 1), t + 1, 1, false);
;             if constexpr (GATHER) { if (last) {
;                 int tz = tid; asm volatile("" : "+v"(tz));
; #pragma unroll
;                 for (int i = 0; i < 2; ++i) { int R, C; stage_rc(tz * 16 + i * 8192, R, C);
; #pragma unroll
;                     for (int h = 0; h < 2; ++h) { const unsigned tk = (unsigned)tokt[h * HALF + R]; offC[h][i] = (tk < (unsigned)NTOK ? tk : (unsigned)(NTOK - 1)) * lda + (unsigned)C * 2u; } } } }
;             PG8_WAIT_V(8); PG8_WAIT_L(0); PG8_BAR; PG8_MMA(0, 0, At, B0); PG8_MMA(0, 1, At, B1); PG8_BAR; PG8_SCHED;
;             PG8_LDA(At, 0, 1); PG8_STAGE(PG8_SB(0, 0), b2, voffB); PG8_STAGE(PG8_SB(0, 1), b2 + hstepB, voffB); PG8_STAGEA(PG8_SA(0, 0), k2, 0, last);
;             PG8_WAIT_V(8); PG8_WAIT_L(0); PG8_BAR; PG8_MMA(1, 0, At, B0); PG8_MMA(1, 1, At, B1); PG8_BAR; PG8_SCHED;
.LBB0_2652:
	ds_read_b128 v[130:133], v154
	ds_read_b128 v[134:137], v154 offset:1024
	ds_read_b128 v[138:141], v154 offset:2048
	ds_read_b128 v[142:145], v154 offset:3072
	ds_read_b128 v[158:161], v154 offset:16384
	ds_read_b128 v[162:165], v154 offset:17408
	ds_read_b128 v[166:169], v154 offset:18432
	ds_read_b128 v[170:173], v154 offset:19456
	s_add_i32 s70, s67, 0xfffe0080
	s_add_i32 s71, s70, s64
	s_cmp_eq_u32 s66, 4
	s_cselect_b64 s[24:25], -1, 0
	s_and_b64 s[68:69], s[24:25], exec
	s_cselect_b32 s68, s65, s71
	s_cselect_b32 s72, 0, s70
	s_add_i32 s69, s68, 0x80
	s_add_i32 s70, s62, s67
	s_add_u32 s70, s8, s70
	s_addc_u32 s71, s9, 0
	v_lshl_add_u64 v[150:151], s[70:71], 0, v[146:147]
	s_add_i32 m0, s26, 0xc000
	ds_read_b128 v[174:177], v153
	ds_read_b128 v[178:181], v153 offset:1024
	ds_read_b128 v[182:185], v153 offset:2048
	ds_read_b128 v[186:189], v153 offset:3072
	ds_read_b128 v[190:193], v153 offset:4096
	ds_read_b128 v[194:197], v153 offset:5120
	ds_read_b128 v[198:201], v153 offset:6144
	ds_read_b128 v[202:205], v153 offset:7168
	global_load_lds_dwordx4 v[150:151], off
	v_lshl_add_u64 v[150:151], s[70:71], 0, v[148:149]
	s_add_i32 m0, s26, 0xe000
	s_nop 0
	global_load_lds_dwordx4 v[150:151], off
	s_waitcnt vmcnt(8)
	s_waitcnt lgkmcnt(0)
	s_barrier
	s_setprio 1
	s_waitcnt lgkmcnt(0)
	v_mfma_f32_16x16x128_f8f6f4 v[126:129], v[130:137], v[174:181], v[126:129]
	v_mfma_f32_16x16x128_f8f6f4 v[122:125], v[138:145], v[174:181], v[122:125]
	v_mfma_f32_16x16x128_f8f6f4 v[118:121], v[130:137], v[182:189], v[118:121]
	v_mfma_f32_16x16x128_f8f6f4 v[114:117], v[138:145], v[182:189], v[114:117]
	v_mfma_f32_16x16x128_f8f6f4 v[206:209], v[130:137], v[190:197], v[94:97]
	v_mfma_f32_16x16x128_f8f6f4 v[210:213], v[138:145], v[190:197], v[90:93]
	v_mfma_f32_16x16x128_f8f6f4 v[214:217], v[130:137], v[198:205], v[82:85]
	v_mfma_f32_16x16x128_f8f6f4 v[218:221], v[138:145], v[198:205], v[74:77]
	s_setprio 0
	s_setprio 1
	v_mfma_f32_16x16x128_f8f6f4 v[110:113], v[158:165], v[174:181], v[110:113]
	v_mfma_f32_16x16x128_f8f6f4 v[106:109], v[166:173], v[174:181], v[106:109]
	v_mfma_f32_16x16x128_f8f6f4 v[102:105], v[158:165], v[182:189], v[102:105]
	v_mfma_f32_16x16x128_f8f6f4 v[98:101], v[166:173], v[182:189], v[98:101]
	v_mfma_f32_16x16x128_f8f6f4 v[174:177], v[158:165], v[190:197], v[86:89]
	v_mfma_f32_16x16x128_f8f6f4 v[178:181], v[166:173], v[190:197], v[78:81]
	v_mfma_f32_16x16x128_f8f6f4 v[182:185], v[158:165], v[198:205], v[70:73]
	v_mfma_f32_16x16x128_f8f6f4 v[186:189], v[166:173], v[198:205], v[66:69]
	s_setprio 0
	s_barrier
	s_add_u32 s70, s8, s68
	s_addc_u32 s71, s9, 0
	s_mov_b32 m0, s27
	v_lshl_add_u64 v[150:151], s[70:71], 0, v[146:147]
	s_nop 0
	global_load_lds_dwordx4 v[150:151], off
	v_lshl_add_u64 v[150:151], s[70:71], 0, v[148:149]
	s_add_i32 s70, s68, 0x20000
	s_add_u32 s70, s8, s70
	s_addc_u32 s71, s9, 0
	s_and_b64 s[24:25], s[20:21], s[24:25]
	s_and_b64 s[24:25], s[24:25], exec
	s_mov_b32 m0, s28
	s_cselect_b32 s24, s58, s62
	global_load_lds_dwordx4 v[150:151], off
	v_lshl_add_u64 v[150:151], s[70:71], 0, v[146:147]
	s_mov_b32 m0, s29
	s_add_i32 s24, s72, s24
	global_load_lds_dwordx4 v[150:151], off
	v_lshl_add_u64 v[150:151], s[70:71], 0, v[148:149]
	s_add_u32 s70, s8, s24
	s_mov_b32 m0, s36
	s_addc_u32 s71, s9, 0
	global_load_lds_dwordx4 v[150:151], off
	v_lshl_add_u64 v[150:151], s[70:71], 0, v[146:147]
	s_mov_b32 m0, s26
	s_nop 0
	global_load_lds_dwordx4 v[150:151], off
	v_lshl_add_u64 v[150:151], s[70:71], 0, v[148:149]
	s_mov_b32 m0, s37
	s_nop 0
	global_load_lds_dwordx4 v[150:151], off
	ds_read_b128 v[66:69], v153 offset:16384
	ds_read_b128 v[70:73], v153 offset:17408
	ds_read_b128 v[74:77], v153 offset:18432
	ds_read_b128 v[78:81], v153 offset:19456
	ds_read_b128 v[82:85], v153 offset:20480
	ds_read_b128 v[86:89], v153 offset:21504
	ds_read_b128 v[90:93], v153 offset:22528
	ds_read_b128 v[94:97], v153 offset:23552
	s_waitcnt vmcnt(8)
	s_waitcnt lgkmcnt(0)
	s_barrier
	s_setprio 1
	s_waitcnt lgkmcnt(0)
	v_mfma_f32_16x16x128_f8f6f4 v[62:65], v[130:137], v[66:73], v[62:65]
	v_mfma_f32_16x16x128_f8f6f4 v[58:61], v[138:145], v[66:73], v[58:61]
	v_mfma_f32_16x16x128_f8f6f4 v[50:53], v[130:137], v[74:81], v[50:53]
	v_mfma_f32_16x16x128_f8f6f4 v[190:193], v[138:145], v[74:81], v[42:45]
	v_mfma_f32_16x16x128_f8f6f4 v[194:197], v[130:137], v[82:89], v[34:37]
	v_mfma_f32_16x16x128_f8f6f4 v[198:201], v[138:145], v[82:89], v[26:29]
	v_mfma_f32_16x16x128_f8f6f4 v[202:205], v[130:137], v[90:97], v[18:21]
	v_mfma_f32_16x16x128_f8f6f4 v[222:225], v[138:145], v[90:97], v[10:13]
	s_setprio 0
	s_setprio 1
	v_mfma_f32_16x16x128_f8f6f4 v[54:57], v[158:165], v[66:73], v[54:57]
	v_mfma_f32_16x16x128_f8f6f4 v[226:229], v[166:173], v[66:73], v[46:49]
	v_mfma_f32_16x16x128_f8f6f4 v[230:233], v[158:165], v[74:81], v[38:41]
	v_mfma_f32_16x16x128_f8f6f4 v[234:237], v[166:173], v[74:81], v[30:33]
	v_mfma_f32_16x16x128_f8f6f4 v[238:241], v[158:165], v[82:89], v[22:25]
	v_mfma_f32_16x16x128_f8f6f4 v[242:245], v[166:173], v[82:89], v[14:17]
	v_mfma_f32_16x16x128_f8f6f4 v[246:249], v[158:165], v[90:97], v[6:9]
	v_mfma_f32_16x16x128_f8f6f4 v[250:253], v[166:173], v[90:97], v[2:5]
	s_setprio 0
	s_barrier
; #define PG8_STAGE(bufoff, gbase, voff) do { _Pragma("unroll") for (int _i = 0; _i < 2; ++_i) \
;         __builtin_amdgcn_global_load_lds((const unsigned*)(wsb + (size_t)(gbase) + (voff)[_i]), (LAS unsigned*)(lds + (bufoff) + ldsw + _i * 8192), 16, 0, 0); } while (0)
; #define PG8_LDA(dst, b, h) do { _Pragma("unroll") for (int m = 0; m < 4; ++m) { if constexpr (FP8) dst##8[m] = PG8_LD8(pa, PG8_SA(b, h) + m * 2048); \
;         else { _Pragma("unroll") for (int k = 0; k < 2; ++k) dst[m][k] = *(const LAS bf16x8*)(pa + PG8_SA(b, h) + m * 2048 + k * 1024); } } } while (0)
; #define PG8_LDB(dst, b, h) do { _Pragma("unroll") for (int n = 0; n < 2; ++n) { if constexpr (FP8) dst##8[n] = PG8_LD8(pb, PG8_SA(b, h) + n * 2048); \
;         else { _Pragma("unroll") for (int k = 0; k < 2; ++k) dst[n][k] = *(const LAS bf16x8*)(pb + PG8_SA(b, h) + n * 2048 + k * 1024); } } } while (0)
; #define PG8_WAIT_V(n) asm volatile("s_waitcnt vmcnt(" #n ")" ::: "memory")
; #define PG8_WAIT_L(n) asm volatile("s_waitcnt lgkmcnt(" #n ")" ::: "memory")
; #define PG8_BAR __builtin_amdgcn_s_barrier()
; #define PG8_SCHED __builtin_amdgcn_sched_barrier(0)
; template <class Epi, class Sched, bool PERM, bool FP8 = false, bool GATHER = false>
; DI void gemm_phase(LAS unsigned char* lds, const unsigned char* wsb, const unsigned lda, const unsigned ldb, const int nt, const Sched& S, const Epi& E) {
;     ...
;             PG8_LDB(B0, 1, 0); PG8_LDB(B1, 1, 1); PG8_SCHED; PG8_LDA(At, 1, 0); PG8_STAGEA(PG8_SA(0, 1), k2, 1, last);
;             PG8_WAIT_V(8); PG8_WAIT_L(0); PG8_BAR; PG8_MMA(0, 0, At, B0); PG8_MMA(0, 1, At, B1); PG8_BAR; PG8_SCHED;
;             PG8_LDA(At, 1, 1); PG8_STAGE(PG8_SB(1, 0), b3, voffB); PG8_STAGE(PG8_SB(1, 1), b3 + hstepB, voffB); PG8_STAGEA(PG8_SA(1, 0), k3, 0, last);
;             PG8_WAIT_V(8); PG8_WAIT_L(0); PG8_BAR; PG8_MMA(1, 0, At, B0); PG8_MMA(1, 1, At, B1); PG8_BAR; PG8_SCHED;
;         }
;         if (wr == 0) PG8_BAR;
	s_nop 4
	s_add_i32 s25, s24, 0x20000
	s_add_u32 s70, s8, s25
	s_addc_u32 s71, s9, 0
	s_mov_b32 m0, s38
	v_lshl_add_u64 v[66:67], s[70:71], 0, v[146:147]
	global_load_lds_dwordx4 v[66:67], off
	v_lshl_add_u64 v[66:67], s[70:71], 0, v[148:149]
	s_mov_b32 m0, s39
	s_nop 0
	global_load_lds_dwordx4 v[66:67], off
	ds_read_b128 v[2:5], v154 offset:32768
	ds_read_b128 v[6:9], v154 offset:33792
	ds_read_b128 v[10:13], v154 offset:34816
	ds_read_b128 v[14:17], v154 offset:35840
	ds_read_b128 v[130:133], v154 offset:49152
	ds_read_b128 v[134:137], v154 offset:50176
	ds_read_b128 v[138:141], v154 offset:51200
	ds_read_b128 v[142:145], v154 offset:52224
	ds_read_b128 v[18:21], v153 offset:32768
	ds_read_b128 v[22:25], v153 offset:33792
	ds_read_b128 v[26:29], v153 offset:34816
	ds_read_b128 v[30:33], v153 offset:35840
	ds_read_b128 v[34:37], v153 offset:36864
	ds_read_b128 v[38:41], v153 offset:37888
	ds_read_b128 v[42:45], v153 offset:38912
	ds_read_b128 v[46:49], v153 offset:39936
	s_waitcnt vmcnt(8)
	s_waitcnt lgkmcnt(0)
	s_barrier
	s_setprio 1
	s_waitcnt lgkmcnt(0)
	v_mfma_f32_16x16x128_f8f6f4 v[126:129], v[2:9], v[18:25], v[126:129]
	v_mfma_f32_16x16x128_f8f6f4 v[122:125], v[10:17], v[18:25], v[122:125]
	v_mfma_f32_16x16x128_f8f6f4 v[118:121], v[2:9], v[26:33], v[118:121]
	v_mfma_f32_16x16x128_f8f6f4 v[114:117], v[10:17], v[26:33], v[114:117]
	v_mfma_f32_16x16x128_f8f6f4 v[94:97], v[2:9], v[34:41], v[206:209]
	v_mfma_f32_16x16x128_f8f6f4 v[90:93], v[10:17], v[34:41], v[210:213]
	v_mfma_f32_16x16x128_f8f6f4 v[82:85], v[2:9], v[42:49], v[214:217]
	v_mfma_f32_16x16x128_f8f6f4 v[74:77], v[10:17], v[42:49], v[218:221]
	s_setprio 0
	s_setprio 1
	v_mfma_f32_16x16x128_f8f6f4 v[110:113], v[130:137], v[18:25], v[110:113]
	v_mfma_f32_16x16x128_f8f6f4 v[106:109], v[138:145], v[18:25], v[106:109]
	v_mfma_f32_16x16x128_f8f6f4 v[102:105], v[130:137], v[26:33], v[102:105]
	v_mfma_f32_16x16x128_f8f6f4 v[98:101], v[138:145], v[26:33], v[98:101]
	v_mfma_f32_16x16x128_f8f6f4 v[86:89], v[130:137], v[34:41], v[174:177]
	v_mfma_f32_16x16x128_f8f6f4 v[78:81], v[138:145], v[34:41], v[178:181]
	v_mfma_f32_16x16x128_f8f6f4 v[70:73], v[130:137], v[42:49], v[182:185]
	v_mfma_f32_16x16x128_f8f6f4 v[66:69], v[138:145], v[42:49], v[186:189]
	s_setprio 0
	s_barrier
	s_add_u32 s70, s8, s69
	s_addc_u32 s71, s9, 0
	s_add_i32 s68, s68, 0x20080
	s_mov_b32 m0, s43
	v_lshl_add_u64 v[18:19], s[70:71], 0, v[146:147]
	s_add_u32 s68, s8, s68
	global_load_lds_dwordx4 v[18:19], off
	v_lshl_add_u64 v[18:19], s[70:71], 0, v[148:149]
	s_mov_b32 m0, s44
	s_addc_u32 s69, s9, 0
	s_addk_i32 s24, 0x80
	global_load_lds_dwordx4 v[18:19], off
	v_lshl_add_u64 v[18:19], s[68:69], 0, v[146:147]
	s_mov_b32 m0, s47
	s_add_u32 s24, s8, s24
	global_load_lds_dwordx4 v[18:19], off
	v_lshl_add_u64 v[18:19], s[68:69], 0, v[148:149]
	s_mov_b32 m0, s48
	s_addc_u32 s25, s9, 0
	global_load_lds_dwordx4 v[18:19], off
	v_lshl_add_u64 v[18:19], s[24:25], 0, v[146:147]
	s_mov_b32 m0, s45
	s_nop 0
	global_load_lds_dwordx4 v[18:19], off
	v_lshl_add_u64 v[18:19], s[24:25], 0, v[148:149]
	s_mov_b32 m0, s46
	s_nop 0
	global_load_lds_dwordx4 v[18:19], off
	ds_read_b128 v[158:161], v153 offset:49152
	ds_read_b128 v[162:165], v153 offset:50176
	ds_read_b128 v[166:169], v153 offset:51200
	ds_read_b128 v[170:173], v153 offset:52224
	ds_read_b128 v[174:177], v153 offset:53248
	ds_read_b128 v[178:181], v153 offset:54272
	ds_read_b128 v[182:185], v153 offset:55296
	ds_read_b128 v[186:189], v153 offset:56320
	s_waitcnt vmcnt(8)
	s_waitcnt lgkmcnt(0)
	s_barrier
	s_setprio 1
	s_waitcnt lgkmcnt(0)
	v_mfma_f32_16x16x128_f8f6f4 v[62:65], v[2:9], v[158:165], v[62:65]
	v_mfma_f32_16x16x128_f8f6f4 v[58:61], v[10:17], v[158:165], v[58:61]
	v_mfma_f32_16x16x128_f8f6f4 v[50:53], v[2:9], v[166:173], v[50:53]
	v_mfma_f32_16x16x128_f8f6f4 v[42:45], v[10:17], v[166:173], v[190:193]
	v_mfma_f32_16x16x128_f8f6f4 v[34:37], v[2:9], v[174:181], v[194:197]
	v_mfma_f32_16x16x128_f8f6f4 v[26:29], v[10:17], v[174:181], v[198:201]
	v_mfma_f32_16x16x128_f8f6f4 v[18:21], v[2:9], v[182:189], v[202:205]
	v_mfma_f32_16x16x128_f8f6f4 v[10:13], v[10:17], v[182:189], v[222:225]
	s_setprio 0
	s_setprio 1
	v_mfma_f32_16x16x128_f8f6f4 v[54:57], v[130:137], v[158:165], v[54:57]
	v_mfma_f32_16x16x128_f8f6f4 v[46:49], v[138:145], v[158:165], v[226:229]
	v_mfma_f32_16x16x128_f8f6f4 v[38:41], v[130:137], v[166:173], v[230:233]
	v_mfma_f32_16x16x128_f8f6f4 v[30:33], v[138:145], v[166:173], v[234:237]
	v_mfma_f32_16x16x128_f8f6f4 v[22:25], v[130:137], v[174:181], v[238:241]
	v_mfma_f32_16x16x128_f8f6f4 v[14:17], v[138:145], v[174:181], v[242:245]
	v_mfma_f32_16x16x128_f8f6f4 v[6:9], v[130:137], v[182:189], v[246:249]
	v_mfma_f32_16x16x128_f8f6f4 v[2:5], v[138:145], v[182:189], v[250:253]
	s_setprio 0
	s_barrier
	s_add_i32 s66, s66, 2
	s_addk_i32 s67, 0x100
	s_cmp_gt_u32 s66, 5
	s_cbranch_scc0 .LBB0_2652
	s_and_b64 vcc, exec, s[12:13]
	s_cbranch_vccz .LBB0_2655
	s_barrier
